# branchless f32 tanh (exp2/rcp) for all 254 tanhf instances: sgu, sgu_prep, shift
# speedup vs baseline: 1.0174x; 1.0000x over previous
.LBB0_794:
	s_waitcnt vmcnt(0)
	v_lshlrev_b32_e32 v26, 16, v14
	v_mul_f32_e32 v27, 0x3d372713, v26
	v_mul_f32_e32 v27, v27, v26
	v_fma_f32 v27, v27, v26, v26
	v_mul_f32_e32 v27, 0x3f4c422a, v27
	v_add_f32_e64 v28, |v27|, |v27|
	v_mul_f32_e32 v28, 0x3fb8aa3b, v28
	v_exp_f32_e32 v28, v28
	s_nop 0
	v_add_f32_e32 v28, 1.0, v28
	v_rcp_f32_e32 v28, v28
	s_nop 0
	v_fma_f32 v28, v28, -2.0, 1.0
	v_and_b32_e32 v14, 0xffff0000, v14
	v_mul_f32_e32 v29, 0x3d372713, v14
	v_mul_f32_e32 v29, v29, v14
	v_fma_f32 v29, v29, v14, v14
	v_mul_f32_e32 v29, 0x3f4c422a, v29
	v_add_f32_e64 v30, |v29|, |v29|
	v_mul_f32_e32 v30, 0x3fb8aa3b, v30
	v_exp_f32_e32 v30, v30
	s_nop 0
	v_add_f32_e32 v30, 1.0, v30
	v_rcp_f32_e32 v30, v30
	s_nop 0
	v_fma_f32 v30, v30, -2.0, 1.0
	v_lshlrev_b32_e32 v31, 16, v15
	v_mul_f32_e32 v32, 0x3d372713, v31
	v_mul_f32_e32 v32, v32, v31
	v_fma_f32 v32, v32, v31, v31
	v_mul_f32_e32 v32, 0x3f4c422a, v32
	v_add_f32_e64 v33, |v32|, |v32|
	v_mul_f32_e32 v33, 0x3fb8aa3b, v33
	v_exp_f32_e32 v33, v33
	s_nop 0
	v_add_f32_e32 v33, 1.0, v33
	v_rcp_f32_e32 v33, v33
	s_nop 0
	v_fma_f32 v33, v33, -2.0, 1.0
	v_and_b32_e32 v15, 0xffff0000, v15
	v_mul_f32_e32 v34, 0x3d372713, v15
	v_mul_f32_e32 v34, v34, v15
	v_fma_f32 v34, v34, v15, v15
	v_mul_f32_e32 v34, 0x3f4c422a, v34
	v_add_f32_e64 v35, |v34|, |v34|
	v_mul_f32_e32 v35, 0x3fb8aa3b, v35
	v_exp_f32_e32 v35, v35
	s_nop 0
	v_add_f32_e32 v35, 1.0, v35
	v_rcp_f32_e32 v35, v35
	s_nop 0
	v_fma_f32 v35, v35, -2.0, 1.0
	v_lshlrev_b32_e32 v36, 16, v16
	v_mul_f32_e32 v37, 0x3d372713, v36
	v_mul_f32_e32 v37, v37, v36
	v_fma_f32 v37, v37, v36, v36
	v_mul_f32_e32 v37, 0x3f4c422a, v37
	v_add_f32_e64 v38, |v37|, |v37|
	v_mul_f32_e32 v38, 0x3fb8aa3b, v38
	v_exp_f32_e32 v38, v38
	s_nop 0
	v_add_f32_e32 v38, 1.0, v38
	v_rcp_f32_e32 v38, v38
	s_nop 0
	v_fma_f32 v38, v38, -2.0, 1.0
	v_and_b32_e32 v16, 0xffff0000, v16
	v_mul_f32_e32 v39, 0x3d372713, v16
	v_mul_f32_e32 v39, v39, v16
	v_fma_f32 v39, v39, v16, v16
	v_mul_f32_e32 v39, 0x3f4c422a, v39
	v_add_f32_e64 v40, |v39|, |v39|
	v_mul_f32_e32 v40, 0x3fb8aa3b, v40
	v_exp_f32_e32 v40, v40
	s_nop 0
	v_add_f32_e32 v40, 1.0, v40
	v_rcp_f32_e32 v40, v40
	s_nop 0
	v_fma_f32 v40, v40, -2.0, 1.0
	v_lshlrev_b32_e32 v41, 16, v17
	v_mul_f32_e32 v42, 0x3d372713, v41
	v_mul_f32_e32 v42, v42, v41
	v_fma_f32 v42, v42, v41, v41
	v_mul_f32_e32 v42, 0x3f4c422a, v42
	v_add_f32_e64 v43, |v42|, |v42|
	v_mul_f32_e32 v43, 0x3fb8aa3b, v43
	v_exp_f32_e32 v43, v43
	s_nop 0
	v_add_f32_e32 v43, 1.0, v43
	v_rcp_f32_e32 v43, v43
	s_nop 0
	v_fma_f32 v43, v43, -2.0, 1.0
	v_and_b32_e32 v17, 0xffff0000, v17
	v_mul_f32_e32 v44, 0x3d372713, v17
	v_mul_f32_e32 v44, v44, v17
	v_fma_f32 v44, v44, v17, v17
	v_mul_f32_e32 v44, 0x3f4c422a, v44
	v_add_f32_e64 v45, |v44|, |v44|
	v_mul_f32_e32 v45, 0x3fb8aa3b, v45
	v_exp_f32_e32 v45, v45
	s_nop 0
	v_add_f32_e32 v45, 1.0, v45
	v_rcp_f32_e32 v45, v45
	s_nop 0
	v_fma_f32 v45, v45, -2.0, 1.0
	v_lshlrev_b32_e32 v46, 16, v10
	v_mul_f32_e32 v47, 0x3d372713, v46
	v_mul_f32_e32 v47, v47, v46
	v_fma_f32 v47, v47, v46, v46
	v_mul_f32_e32 v47, 0x3f4c422a, v47
	s_waitcnt lgkmcnt(0)
	v_add_f32_e64 v48, |v47|, |v47|
	v_mul_f32_e32 v48, 0x3fb8aa3b, v48
	v_exp_f32_e32 v48, v48
	s_nop 0
	v_add_f32_e32 v48, 1.0, v48
	v_rcp_f32_e32 v48, v48
	s_nop 0
	v_fma_f32 v48, v48, -2.0, 1.0
	v_and_b32_e32 v10, 0xffff0000, v10
	v_mul_f32_e32 v49, 0x3d372713, v10
	v_mul_f32_e32 v49, v49, v10
	v_fma_f32 v49, v49, v10, v10
	v_mul_f32_e32 v49, 0x3f4c422a, v49
	s_waitcnt lgkmcnt(0)
	s_waitcnt lgkmcnt(0)
	v_add_f32_e64 v55, |v49|, |v49|
	v_mul_f32_e32 v55, 0x3fb8aa3b, v55
	v_exp_f32_e32 v55, v55
	s_nop 0
	v_add_f32_e32 v55, 1.0, v55
	v_rcp_f32_e32 v55, v55
	s_nop 0
	v_fma_f32 v55, v55, -2.0, 1.0
	s_waitcnt lgkmcnt(0)
	v_lshlrev_b32_e32 v56, 16, v11
	v_mul_f32_e32 v57, 0x3d372713, v56
	v_mul_f32_e32 v57, v57, v56
	v_fma_f32 v57, v57, v56, v56
	v_mul_f32_e32 v57, 0x3f4c422a, v57
	v_add_f32_e64 v58, |v57|, |v57|
	v_mul_f32_e32 v58, 0x3fb8aa3b, v58
	v_exp_f32_e32 v58, v58
	s_nop 0
	v_add_f32_e32 v58, 1.0, v58
	v_rcp_f32_e32 v58, v58
	s_nop 0
	v_fma_f32 v58, v58, -2.0, 1.0
	v_and_b32_e32 v11, 0xffff0000, v11
	v_mul_f32_e32 v59, 0x3d372713, v11
	v_mul_f32_e32 v59, v59, v11
	v_fma_f32 v59, v59, v11, v11
	v_mul_f32_e32 v59, 0x3f4c422a, v59
	v_add_f32_e64 v60, |v59|, |v59|
	v_mul_f32_e32 v60, 0x3fb8aa3b, v60
	v_exp_f32_e32 v60, v60
	s_nop 0
	v_add_f32_e32 v60, 1.0, v60
	v_rcp_f32_e32 v60, v60
	s_nop 0
	v_fma_f32 v60, v60, -2.0, 1.0
	v_lshlrev_b32_e32 v61, 16, v12
	v_mul_f32_e32 v62, 0x3d372713, v61
	v_mul_f32_e32 v62, v62, v61
	v_fma_f32 v62, v62, v61, v61
	v_mul_f32_e32 v62, 0x3f4c422a, v62
	v_add_f32_e64 v63, |v62|, |v62|
	v_mul_f32_e32 v63, 0x3fb8aa3b, v63
	v_exp_f32_e32 v63, v63
	s_nop 0
	v_add_f32_e32 v63, 1.0, v63
	v_rcp_f32_e32 v63, v63
	s_nop 0
	v_fma_f32 v63, v63, -2.0, 1.0
	v_and_b32_e32 v12, 0xffff0000, v12
	v_mul_f32_e32 v64, 0x3d372713, v12
	v_mul_f32_e32 v64, v64, v12
	v_fma_f32 v64, v64, v12, v12
	v_mul_f32_e32 v64, 0x3f4c422a, v64
	v_add_f32_e64 v65, |v64|, |v64|
	v_mul_f32_e32 v65, 0x3fb8aa3b, v65
	v_exp_f32_e32 v65, v65
	s_nop 0
	v_add_f32_e32 v65, 1.0, v65
	v_rcp_f32_e32 v65, v65
	s_nop 0
	v_fma_f32 v65, v65, -2.0, 1.0
	v_lshlrev_b32_e32 v66, 16, v13
	v_mul_f32_e32 v67, 0x3d372713, v66
	v_mul_f32_e32 v67, v67, v66
	v_fma_f32 v67, v67, v66, v66
	v_mul_f32_e32 v67, 0x3f4c422a, v67
	v_add_f32_e64 v68, |v67|, |v67|
	v_mul_f32_e32 v68, 0x3fb8aa3b, v68
	v_exp_f32_e32 v68, v68
	s_nop 0
	v_add_f32_e32 v68, 1.0, v68
	v_rcp_f32_e32 v68, v68
	s_nop 0
	v_fma_f32 v68, v68, -2.0, 1.0
	v_and_b32_e32 v13, 0xffff0000, v13
	v_mul_f32_e32 v69, 0x3d372713, v13
	v_mul_f32_e32 v69, v69, v13
	v_fma_f32 v69, v69, v13, v13
	v_mul_f32_e32 v69, 0x3f4c422a, v69
	v_add_f32_e64 v70, |v69|, |v69|
	v_mul_f32_e32 v70, 0x3fb8aa3b, v70
	v_exp_f32_e32 v70, v70
	s_nop 0
	v_add_f32_e32 v70, 1.0, v70
	v_rcp_f32_e32 v70, v70
	s_nop 0
	v_fma_f32 v70, v70, -2.0, 1.0
	v_lshlrev_b32_e32 v71, 16, v6
	v_mul_f32_e32 v72, 0x3d372713, v71
	v_mul_f32_e32 v72, v72, v71
	v_fma_f32 v72, v72, v71, v71
	v_mul_f32_e32 v72, 0x3f4c422a, v72
	v_add_f32_e64 v73, |v72|, |v72|
	v_mul_f32_e32 v73, 0x3fb8aa3b, v73
	v_exp_f32_e32 v73, v73
	s_nop 0
	v_add_f32_e32 v73, 1.0, v73
	v_rcp_f32_e32 v73, v73
	s_nop 0
	v_fma_f32 v73, v73, -2.0, 1.0
	v_and_b32_e32 v74, 0xffff0000, v6
	v_mul_f32_e32 v6, 0x3d372713, v74
	v_mul_f32_e32 v6, v6, v74
	v_fma_f32 v6, v6, v74, v74
	v_mul_f32_e32 v75, 0x3f4c422a, v6
	v_add_f32_e64 v76, |v75|, |v75|
	v_mul_f32_e32 v76, 0x3fb8aa3b, v76
	v_exp_f32_e32 v76, v76
	s_nop 0
	v_add_f32_e32 v76, 1.0, v76
	v_rcp_f32_e32 v76, v76
	s_nop 0
	v_fma_f32 v76, v76, -2.0, 1.0
	v_lshlrev_b32_e32 v77, 16, v7
	v_mul_f32_e32 v6, 0x3d372713, v77
	v_mul_f32_e32 v6, v6, v77
	v_fma_f32 v6, v6, v77, v77
	v_mul_f32_e32 v78, 0x3f4c422a, v6
	v_add_f32_e64 v79, |v78|, |v78|
	v_mul_f32_e32 v79, 0x3fb8aa3b, v79
	v_exp_f32_e32 v79, v79
	s_nop 0
	v_add_f32_e32 v79, 1.0, v79
	v_rcp_f32_e32 v79, v79
	s_nop 0
	v_fma_f32 v79, v79, -2.0, 1.0
	v_and_b32_e32 v80, 0xffff0000, v7
	v_mul_f32_e32 v6, 0x3d372713, v80
	v_mul_f32_e32 v6, v6, v80
	v_fma_f32 v6, v6, v80, v80
	v_mul_f32_e32 v81, 0x3f4c422a, v6
	v_add_f32_e64 v82, |v81|, |v81|
	v_mul_f32_e32 v82, 0x3fb8aa3b, v82
	v_exp_f32_e32 v82, v82
	s_nop 0
	v_add_f32_e32 v82, 1.0, v82
	v_rcp_f32_e32 v82, v82
	s_nop 0
	v_fma_f32 v82, v82, -2.0, 1.0
	v_lshlrev_b32_e32 v83, 16, v8
	v_mul_f32_e32 v6, 0x3d372713, v83
	v_mul_f32_e32 v6, v6, v83
	v_fma_f32 v6, v6, v83, v83
	v_mul_f32_e32 v84, 0x3f4c422a, v6
	v_add_f32_e64 v85, |v84|, |v84|
	v_mul_f32_e32 v85, 0x3fb8aa3b, v85
	v_exp_f32_e32 v85, v85
	s_nop 0
	v_add_f32_e32 v85, 1.0, v85
	v_rcp_f32_e32 v85, v85
	s_nop 0
	v_fma_f32 v85, v85, -2.0, 1.0
	v_and_b32_e32 v8, 0xffff0000, v8
	v_mul_f32_e32 v6, 0x3d372713, v8
	v_mul_f32_e32 v6, v6, v8
	v_fma_f32 v6, v6, v8, v8
	v_mul_f32_e32 v86, 0x3f4c422a, v6
	v_add_f32_e64 v87, |v86|, |v86|
	v_mul_f32_e32 v87, 0x3fb8aa3b, v87
	v_exp_f32_e32 v87, v87
	s_nop 0
	v_add_f32_e32 v87, 1.0, v87
	v_rcp_f32_e32 v87, v87
	s_nop 0
	v_fma_f32 v87, v87, -2.0, 1.0
	v_lshlrev_b32_e32 v88, 16, v9
	v_mul_f32_e32 v6, 0x3d372713, v88
	v_mul_f32_e32 v6, v6, v88
	v_fma_f32 v6, v6, v88, v88
	v_mul_f32_e32 v89, 0x3f4c422a, v6
	v_add_f32_e64 v90, |v89|, |v89|
	v_mul_f32_e32 v90, 0x3fb8aa3b, v90
	v_exp_f32_e32 v90, v90
	s_nop 0
	v_add_f32_e32 v90, 1.0, v90
	v_rcp_f32_e32 v90, v90
	s_nop 0
	v_fma_f32 v90, v90, -2.0, 1.0
	v_and_b32_e32 v9, 0xffff0000, v9
	v_mul_f32_e32 v6, 0x3d372713, v9
	v_mul_f32_e32 v6, v6, v9
	v_fma_f32 v6, v6, v9, v9
	v_mul_f32_e32 v91, 0x3f4c422a, v6
	v_add_f32_e64 v92, |v91|, |v91|
	v_mul_f32_e32 v92, 0x3fb8aa3b, v92
	v_exp_f32_e32 v92, v92
	s_nop 0
	v_add_f32_e32 v92, 1.0, v92
	v_rcp_f32_e32 v92, v92
	s_nop 0
	v_fma_f32 v92, v92, -2.0, 1.0
	v_lshlrev_b32_e32 v6, 16, v2
	v_mul_f32_e32 v7, 0x3d372713, v6
	v_mul_f32_e32 v7, v7, v6
	v_fma_f32 v7, v7, v6, v6
	v_mul_f32_e32 v7, 0x3f4c422a, v7
	v_add_f32_e64 v93, |v7|, |v7|
	v_mul_f32_e32 v93, 0x3fb8aa3b, v93
	v_exp_f32_e32 v93, v93
	s_nop 0
	v_add_f32_e32 v93, 1.0, v93
	v_rcp_f32_e32 v93, v93
	s_nop 0
	v_fma_f32 v93, v93, -2.0, 1.0
	v_and_b32_e32 v94, 0xffff0000, v2
	v_mul_f32_e32 v2, 0x3d372713, v94
	v_mul_f32_e32 v2, v2, v94
	v_fma_f32 v2, v2, v94, v94
	v_mul_f32_e32 v95, 0x3f4c422a, v2
	v_add_f32_e64 v96, |v95|, |v95|
	v_mul_f32_e32 v96, 0x3fb8aa3b, v96
	v_exp_f32_e32 v96, v96
	s_nop 0
	v_add_f32_e32 v96, 1.0, v96
	v_rcp_f32_e32 v96, v96
	s_nop 0
	v_fma_f32 v96, v96, -2.0, 1.0
	v_lshlrev_b32_e32 v97, 16, v3
	v_mul_f32_e32 v2, 0x3d372713, v97
	v_mul_f32_e32 v2, v2, v97
	v_fma_f32 v2, v2, v97, v97
	v_mul_f32_e32 v98, 0x3f4c422a, v2
	v_add_f32_e64 v99, |v98|, |v98|
	v_mul_f32_e32 v99, 0x3fb8aa3b, v99
	v_exp_f32_e32 v99, v99
	s_nop 0
	v_add_f32_e32 v99, 1.0, v99
	v_rcp_f32_e32 v99, v99
	s_nop 0
	v_fma_f32 v99, v99, -2.0, 1.0
	v_and_b32_e32 v100, 0xffff0000, v3
	v_mul_f32_e32 v2, 0x3d372713, v100
	v_mul_f32_e32 v2, v2, v100
	v_fma_f32 v2, v2, v100, v100
	v_mul_f32_e32 v101, 0x3f4c422a, v2
	v_add_f32_e64 v102, |v101|, |v101|
	v_mul_f32_e32 v102, 0x3fb8aa3b, v102
	v_exp_f32_e32 v102, v102
	s_nop 0
	v_add_f32_e32 v102, 1.0, v102
	v_rcp_f32_e32 v102, v102
	s_nop 0
	v_fma_f32 v102, v102, -2.0, 1.0
	v_lshlrev_b32_e32 v103, 16, v4
	v_mul_f32_e32 v2, 0x3d372713, v103
	v_mul_f32_e32 v2, v2, v103
	v_fma_f32 v2, v2, v103, v103
	v_mul_f32_e32 v104, 0x3f4c422a, v2
	v_add_f32_e64 v107, |v104|, |v104|
	v_mul_f32_e32 v107, 0x3fb8aa3b, v107
	v_exp_f32_e32 v107, v107
	s_nop 0
	v_add_f32_e32 v107, 1.0, v107
	v_rcp_f32_e32 v107, v107
	s_nop 0
	v_fma_f32 v107, v107, -2.0, 1.0
	v_and_b32_e32 v109, 0xffff0000, v4
	v_mul_f32_e32 v2, 0x3d372713, v109
	v_mul_f32_e32 v2, v2, v109
	v_fma_f32 v2, v2, v109, v109
	v_mul_f32_e32 v110, 0x3f4c422a, v2
	v_add_f32_e64 v111, |v110|, |v110|
	v_mul_f32_e32 v111, 0x3fb8aa3b, v111
	v_exp_f32_e32 v111, v111
	s_nop 0
	v_add_f32_e32 v111, 1.0, v111
	v_rcp_f32_e32 v111, v111
	s_nop 0
	v_fma_f32 v111, v111, -2.0, 1.0
	v_lshlrev_b32_e32 v112, 16, v5
	v_mul_f32_e32 v2, 0x3d372713, v112
	v_mul_f32_e32 v2, v2, v112
	v_fma_f32 v2, v2, v112, v112
	v_mul_f32_e32 v113, 0x3f4c422a, v2
	v_add_f32_e64 v114, |v113|, |v113|
	v_mul_f32_e32 v114, 0x3fb8aa3b, v114
	v_exp_f32_e32 v114, v114
	s_nop 0
	v_add_f32_e32 v114, 1.0, v114
	v_rcp_f32_e32 v114, v114
	s_nop 0
	v_fma_f32 v114, v114, -2.0, 1.0
	v_and_b32_e32 v105, 0xffff0000, v5
	v_mul_f32_e32 v2, 0x3d372713, v105
	v_mul_f32_e32 v2, v2, v105
	v_fma_f32 v2, v2, v105, v105
	v_mul_f32_e32 v106, 0x3f4c422a, v2
	v_add_f32_e64 v108, |v106|, |v106|
	v_mul_f32_e32 v108, 0x3fb8aa3b, v108
	v_exp_f32_e32 v108, v108
	s_nop 0
	v_add_f32_e32 v108, 1.0, v108
	v_rcp_f32_e32 v108, v108
	s_nop 0
	v_fma_f32 v108, v108, -2.0, 1.0
	v_bfi_b32 v72, s17, v73, v72
	v_mul_f32_e32 v71, 0.5, v71
	v_add_f32_e32 v73, 1.0, v72
	v_mul_f32_e32 v72, v71, v73
	v_fma_f32 v71, v71, v73, 0
	v_bfi_b32 v73, s17, v76, v75
	v_mul_f32_e32 v74, 0.5, v74
	v_add_f32_e32 v75, 1.0, v73
	v_mul_f32_e32 v73, v74, v75
	v_fmac_f32_e32 v71, v74, v75
	v_bfi_b32 v74, s17, v79, v78
	v_mul_f32_e32 v75, 0.5, v77
	v_add_f32_e32 v76, 1.0, v74
	v_mul_f32_e32 v74, v75, v76
	v_fmac_f32_e32 v71, v75, v76
	v_bfi_b32 v75, s17, v82, v81
	v_mul_f32_e32 v76, 0.5, v80
	v_add_f32_e32 v77, 1.0, v75
	v_mul_f32_e32 v75, v76, v77
	v_fmac_f32_e32 v71, v76, v77
	v_bfi_b32 v76, s17, v85, v84
	v_mul_f32_e32 v77, 0.5, v83
	v_add_f32_e32 v78, 1.0, v76
	v_mul_f32_e32 v76, v77, v78
	v_fmac_f32_e32 v71, v77, v78
	v_bfi_b32 v77, s17, v87, v86
	v_mul_f32_e32 v8, 0.5, v8
	v_add_f32_e32 v78, 1.0, v77
	v_mul_f32_e32 v77, v8, v78
	v_fmac_f32_e32 v71, v8, v78
	v_bfi_b32 v8, s17, v90, v89
	v_mul_f32_e32 v78, 0.5, v88
	v_add_f32_e32 v79, 1.0, v8
	v_mul_f32_e32 v8, v78, v79
	v_fmac_f32_e32 v71, v78, v79
	v_mul_f32_e32 v78, 0.5, v9
	v_bfi_b32 v9, s17, v92, v91
	v_add_f32_e32 v79, 1.0, v9
	v_mul_f32_e32 v9, v78, v79
	v_fmac_f32_e32 v71, v78, v79
	v_mul_f32_e32 v78, 0.5, v46
	v_bfi_b32 v46, s17, v48, v47
	v_add_f32_e32 v47, 1.0, v46
	v_mul_f32_e32 v46, v78, v47
	v_fma_f32 v78, v78, v47, 0
	v_bfi_b32 v47, s17, v55, v49
	v_mul_f32_e32 v10, 0.5, v10
	v_add_f32_e32 v48, 1.0, v47
	v_mul_f32_e32 v47, v10, v48
	v_fmac_f32_e32 v78, v10, v48
	v_bfi_b32 v10, s17, v58, v57
	v_mul_f32_e32 v48, 0.5, v56
	v_add_f32_e32 v49, 1.0, v10
	v_mul_f32_e32 v10, v48, v49
	v_fmac_f32_e32 v78, v48, v49
	v_mul_f32_e32 v48, 0.5, v11
	v_bfi_b32 v11, s17, v60, v59
	v_add_f32_e32 v49, 1.0, v11
	v_mul_f32_e32 v11, v48, v49
	v_fmac_f32_e32 v78, v48, v49
	v_bfi_b32 v48, s17, v63, v62
	v_mul_f32_e32 v49, 0.5, v61
	v_add_f32_e32 v55, 1.0, v48
	v_mul_f32_e32 v48, v49, v55
	v_fmac_f32_e32 v78, v49, v55
	v_bfi_b32 v49, s17, v65, v64
	v_mul_f32_e32 v12, 0.5, v12
	v_add_f32_e32 v55, 1.0, v49
	v_mul_f32_e32 v49, v12, v55
	v_fmac_f32_e32 v78, v12, v55
	v_bfi_b32 v12, s17, v68, v67
	v_mul_f32_e32 v55, 0.5, v66
	v_add_f32_e32 v56, 1.0, v12
	v_mul_f32_e32 v12, v55, v56
	v_fmac_f32_e32 v78, v55, v56
	v_mul_f32_e32 v55, 0.5, v13
	v_bfi_b32 v13, s17, v70, v69
	v_bfi_b32 v27, s17, v28, v27
	v_add_f32_e32 v56, 1.0, v13
	v_mul_f32_e32 v26, 0.5, v26
	v_add_f32_e32 v27, 1.0, v27
	v_bfi_b32 v2, s17, v93, v7
	v_mul_f32_e32 v13, v55, v56
	v_fmac_f32_e32 v78, v55, v56
	v_mul_f32_e32 v56, v26, v27
	v_fma_f32 v26, v26, v27, 0
	v_bfi_b32 v27, s17, v30, v29
	v_mul_f32_e32 v3, 0.5, v6
	v_add_f32_e32 v4, 1.0, v2
	v_mul_f32_e32 v14, 0.5, v14
	v_add_f32_e32 v27, 1.0, v27
	v_mul_f32_e32 v2, v3, v4
	v_fma_f32 v93, v3, v4, 0
	v_bfi_b32 v3, s17, v96, v95
	v_mul_f32_e32 v57, v14, v27
	v_fmac_f32_e32 v26, v14, v27
	v_bfi_b32 v27, s17, v33, v32
	v_mul_f32_e32 v4, 0.5, v94
	v_add_f32_e32 v5, 1.0, v3
	v_mul_f32_e32 v14, 0.5, v31
	v_add_f32_e32 v27, 1.0, v27
	v_mul_f32_e32 v3, v4, v5
	v_fmac_f32_e32 v93, v4, v5
	v_bfi_b32 v4, s17, v99, v98
	v_mul_f32_e32 v58, v14, v27
	v_fmac_f32_e32 v26, v14, v27
	v_mul_f32_e32 v14, 0.5, v15
	v_bfi_b32 v15, s17, v35, v34
	v_mul_f32_e32 v5, 0.5, v97
	v_add_f32_e32 v6, 1.0, v4
	v_add_f32_e32 v15, 1.0, v15
	v_mul_f32_e32 v4, v5, v6
	v_fmac_f32_e32 v93, v5, v6
	v_bfi_b32 v5, s17, v102, v101
	v_mul_f32_e32 v59, v14, v15
	v_fmac_f32_e32 v26, v14, v15
	v_bfi_b32 v15, s17, v38, v37
	v_mul_f32_e32 v6, 0.5, v100
	v_add_f32_e32 v7, 1.0, v5
	v_mul_f32_e32 v14, 0.5, v36
	v_add_f32_e32 v15, 1.0, v15
	v_mul_f32_e32 v5, v6, v7
	v_fmac_f32_e32 v93, v6, v7
	v_bfi_b32 v6, s17, v107, v104
	v_mul_f32_e32 v60, v14, v15
	v_fmac_f32_e32 v26, v14, v15
	v_bfi_b32 v15, s17, v40, v39
	v_mul_f32_e32 v7, 0.5, v103
	v_add_f32_e32 v94, 1.0, v6
	v_mul_f32_e32 v14, 0.5, v16
	v_add_f32_e32 v15, 1.0, v15
	v_mul_f32_e32 v6, v7, v94
	v_fmac_f32_e32 v93, v7, v94
	v_bfi_b32 v7, s17, v111, v110
	v_mul_f32_e32 v61, v14, v15
	v_fmac_f32_e32 v26, v14, v15
	v_bfi_b32 v15, s17, v43, v42
	v_mul_f32_e32 v94, 0.5, v109
	v_add_f32_e32 v95, 1.0, v7
	v_mul_f32_e32 v14, 0.5, v41
	v_add_f32_e32 v15, 1.0, v15
	v_mul_f32_e32 v7, v94, v95
	v_fmac_f32_e32 v93, v94, v95
	v_bfi_b32 v94, s17, v114, v113
	v_mul_f32_e32 v62, v14, v15
	v_fmac_f32_e32 v26, v14, v15
	v_bfi_b32 v15, s17, v45, v44
	v_mul_f32_e32 v95, 0.5, v112
	v_add_f32_e32 v96, 1.0, v94
	v_mul_f32_e32 v14, 0.5, v17
	v_add_f32_e32 v15, 1.0, v15
	v_bfi_b32 v17, s17, v108, v106
	v_fmac_f32_e32 v93, v95, v96
	v_fmac_f32_e32 v26, v14, v15
	v_mul_f32_e32 v16, 0.5, v105
	v_add_f32_e32 v17, 1.0, v17
	v_fmac_f32_e32 v93, v16, v17
	v_add_f32_dpp v26, v26, v26 quad_perm:[1,0,3,2] row_mask:0xf bank_mask:0xf bound_ctrl:1
	v_add_f32_dpp v27, v78, v78 quad_perm:[1,0,3,2] row_mask:0xf bank_mask:0xf bound_ctrl:1
	v_add_f32_dpp v28, v71, v71 quad_perm:[1,0,3,2] row_mask:0xf bank_mask:0xf bound_ctrl:1
	v_add_f32_dpp v26, v26, v26 quad_perm:[2,3,0,1] row_mask:0xf bank_mask:0xf bound_ctrl:1
	v_add_f32_dpp v27, v27, v27 quad_perm:[2,3,0,1] row_mask:0xf bank_mask:0xf bound_ctrl:1
	v_add_f32_dpp v29, v93, v93 quad_perm:[1,0,3,2] row_mask:0xf bank_mask:0xf bound_ctrl:1
	v_add_f32_dpp v26, v26, v26 row_ror:4 row_mask:0xf bank_mask:0xf bound_ctrl:1
	v_add_f32_dpp v27, v27, v27 row_ror:4 row_mask:0xf bank_mask:0xf bound_ctrl:1
	v_add_f32_dpp v28, v28, v28 quad_perm:[2,3,0,1] row_mask:0xf bank_mask:0xf bound_ctrl:1
	v_add_f32_dpp v29, v29, v29 quad_perm:[2,3,0,1] row_mask:0xf bank_mask:0xf bound_ctrl:1
	v_add_f32_dpp v26, v26, v26 row_ror:8 row_mask:0xf bank_mask:0xf bound_ctrl:1
	v_add_f32_dpp v27, v27, v27 row_ror:8 row_mask:0xf bank_mask:0xf bound_ctrl:1
	v_add_f32_dpp v28, v28, v28 row_ror:4 row_mask:0xf bank_mask:0xf bound_ctrl:1
	v_add_f32_dpp v29, v29, v29 row_ror:4 row_mask:0xf bank_mask:0xf bound_ctrl:1
	ds_bpermute_b32 v30, v1, v26
	v_add_f32_dpp v28, v28, v28 row_ror:8 row_mask:0xf bank_mask:0xf bound_ctrl:1
	v_add_f32_dpp v29, v29, v29 row_ror:8 row_mask:0xf bank_mask:0xf bound_ctrl:1
	ds_bpermute_b32 v31, v1, v27
	ds_bpermute_b32 v32, v1, v28
	ds_bpermute_b32 v33, v1, v29
	v_mul_f32_e32 v63, v14, v15
	s_waitcnt lgkmcnt(3)
	v_add_f32_e32 v14, v26, v30
	s_waitcnt lgkmcnt(2)
	v_add_f32_e32 v15, v27, v31
	s_waitcnt lgkmcnt(1)
	v_add_f32_e32 v26, v28, v32
	s_waitcnt lgkmcnt(0)
	v_add_f32_e32 v27, v29, v33
	ds_bpermute_b32 v28, v50, v14
	ds_bpermute_b32 v29, v50, v15
	ds_bpermute_b32 v30, v50, v26
	ds_bpermute_b32 v31, v50, v27
	v_mul_f32_e32 v94, v95, v96
	s_waitcnt lgkmcnt(3)
	v_add_f32_e32 v14, v14, v28
	s_waitcnt lgkmcnt(2)
	v_add_f32_e32 v15, v15, v29
	v_mul_f32_e32 v64, 0x3b000000, v14
	v_mul_f32_e32 v14, 0x3b000000, v15
	v_pk_add_f32 v[42:43], v[46:47], v[14:15] op_sel_hi:[1,0] neg_lo:[0,1] neg_hi:[0,1]
	v_mul_f32_e32 v95, v16, v17
	v_pk_mul_f32 v[16:17], v[42:43], v[42:43]
	v_pk_add_f32 v[44:45], v[10:11], v[14:15] op_sel_hi:[1,0] neg_lo:[0,1] neg_hi:[0,1]
	v_pk_add_f32 v[46:47], v[48:49], v[14:15] op_sel_hi:[1,0] neg_lo:[0,1] neg_hi:[0,1]
	v_pk_mul_f32 v[10:11], v[44:45], v[44:45]
	v_pk_add_f32 v[48:49], v[12:13], v[14:15] op_sel_hi:[1,0] neg_lo:[0,1] neg_hi:[0,1]
	v_add_f32_e32 v14, v16, v17
	v_add_f32_e32 v10, v10, v14
	s_waitcnt lgkmcnt(1)
	v_add_f32_e32 v28, v26, v30
	s_waitcnt lgkmcnt(0)
	v_add_f32_e32 v29, v27, v31
	v_pk_mul_f32 v[26:27], v[46:47], v[46:47]
	v_add_f32_e32 v10, v11, v10
	v_add_f32_e32 v10, v26, v10
	v_pk_mul_f32 v[12:13], v[48:49], v[48:49]
	v_add_f32_e32 v10, v27, v10
	v_add_f32_e32 v10, v12, v10
	v_add_f32_e32 v55, v13, v10
	v_mul_f32_e32 v10, 0x3b000000, v28
	v_pk_add_f32 v[34:35], v[72:73], v[10:11] op_sel_hi:[1,0] neg_lo:[0,1] neg_hi:[0,1]
	v_pk_add_f32 v[36:37], v[74:75], v[10:11] op_sel_hi:[1,0] neg_lo:[0,1] neg_hi:[0,1]
	v_pk_mul_f32 v[12:13], v[34:35], v[34:35]
	v_pk_mul_f32 v[14:15], v[36:37], v[36:37]
	v_pk_add_f32 v[38:39], v[76:77], v[10:11] op_sel_hi:[1,0] neg_lo:[0,1] neg_hi:[0,1]
	v_pk_add_f32 v[40:41], v[8:9], v[10:11] op_sel_hi:[1,0] neg_lo:[0,1] neg_hi:[0,1]
	v_add_f32_e32 v10, v12, v13
	v_add_f32_e32 v10, v14, v10
	v_pk_mul_f32 v[16:17], v[38:39], v[38:39]
	v_add_f32_e32 v10, v15, v10
	v_add_f32_e32 v10, v16, v10
	v_pk_mul_f32 v[8:9], v[40:41], v[40:41]
	v_add_f32_e32 v10, v17, v10
	v_add_f32_e32 v8, v8, v10
	v_add_f32_e32 v65, v9, v8
	v_mul_f32_e32 v8, 0x3b000000, v29
	v_pk_add_f32 v[26:27], v[2:3], v[8:9] op_sel_hi:[1,0] neg_lo:[0,1] neg_hi:[0,1]
	v_pk_add_f32 v[28:29], v[4:5], v[8:9] op_sel_hi:[1,0] neg_lo:[0,1] neg_hi:[0,1]
	v_pk_mul_f32 v[2:3], v[26:27], v[26:27]
	v_pk_mul_f32 v[4:5], v[28:29], v[28:29]
	v_add_f32_e32 v2, v2, v3
	v_pk_add_f32 v[30:31], v[6:7], v[8:9] op_sel_hi:[1,0] neg_lo:[0,1] neg_hi:[0,1]
	v_add_f32_e32 v2, v4, v2
	v_pk_mul_f32 v[66:67], v[30:31], v[30:31]
	v_add_f32_e32 v2, v5, v2
	v_pk_add_f32 v[32:33], v[94:95], v[8:9] op_sel_hi:[1,0] neg_lo:[0,1] neg_hi:[0,1]
	v_add_f32_e32 v66, v66, v2
	global_load_dwordx4 v[2:5], v[20:21], off
	global_load_dwordx4 v[10:13], v[20:21], off offset:16
	global_load_dwordx4 v[6:9], v[22:23], off
	global_load_dwordx4 v[14:17], v[22:23], off offset:16
	v_pk_mul_f32 v[68:69], v[32:33], v[32:33]
	v_add_f32_e32 v66, v67, v66
	v_add_f32_dpp v65, v65, v65 quad_perm:[1,0,3,2] row_mask:0xf bank_mask:0xf bound_ctrl:1
	v_add_f32_e32 v66, v68, v66
	v_add_f32_e32 v72, v69, v66
	v_add_f32_dpp v65, v65, v65 quad_perm:[2,3,0,1] row_mask:0xf bank_mask:0xf bound_ctrl:1
	v_pk_add_f32 v[66:67], v[56:57], v[64:65] op_sel_hi:[1,0] neg_lo:[0,1] neg_hi:[0,1]
	v_pk_add_f32 v[68:69], v[58:59], v[64:65] op_sel_hi:[1,0] neg_lo:[0,1] neg_hi:[0,1]
	v_pk_mul_f32 v[56:57], v[66:67], v[66:67]
	v_pk_mul_f32 v[58:59], v[68:69], v[68:69]
	v_add_f32_e32 v56, v56, v57
	v_pk_add_f32 v[70:71], v[60:61], v[64:65] op_sel_hi:[1,0] neg_lo:[0,1] neg_hi:[0,1]
	v_add_f32_e32 v56, v58, v56
	v_pk_mul_f32 v[60:61], v[70:71], v[70:71]
	v_add_f32_e32 v56, v59, v56
	v_pk_add_f32 v[62:63], v[62:63], v[64:65] op_sel_hi:[1,0] neg_lo:[0,1] neg_hi:[0,1]
	v_add_f32_e32 v56, v60, v56
	v_add_f32_dpp v73, v65, v65 row_ror:4 row_mask:0xf bank_mask:0xf bound_ctrl:1
	v_pk_mul_f32 v[64:65], v[62:63], v[62:63]
	v_add_f32_e32 v56, v61, v56
	v_add_f32_e32 v56, v64, v56
	v_add_f32_e32 v56, v65, v56
	v_add_f32_dpp v55, v55, v55 quad_perm:[1,0,3,2] row_mask:0xf bank_mask:0xf bound_ctrl:1
	v_add_f32_dpp v59, v72, v72 quad_perm:[1,0,3,2] row_mask:0xf bank_mask:0xf bound_ctrl:1
	v_add_f32_dpp v56, v56, v56 quad_perm:[1,0,3,2] row_mask:0xf bank_mask:0xf bound_ctrl:1
	v_add_f32_dpp v55, v55, v55 quad_perm:[2,3,0,1] row_mask:0xf bank_mask:0xf bound_ctrl:1
	v_add_f32_dpp v59, v59, v59 quad_perm:[2,3,0,1] row_mask:0xf bank_mask:0xf bound_ctrl:1
	v_add_f32_dpp v56, v56, v56 quad_perm:[2,3,0,1] row_mask:0xf bank_mask:0xf bound_ctrl:1
	v_add_f32_dpp v55, v55, v55 row_ror:4 row_mask:0xf bank_mask:0xf bound_ctrl:1
	v_add_f32_dpp v58, v73, v73 row_ror:8 row_mask:0xf bank_mask:0xf bound_ctrl:1
	v_add_f32_dpp v56, v56, v56 row_ror:4 row_mask:0xf bank_mask:0xf bound_ctrl:1
	v_add_f32_dpp v59, v59, v59 row_ror:4 row_mask:0xf bank_mask:0xf bound_ctrl:1
	v_add_f32_dpp v55, v55, v55 row_ror:8 row_mask:0xf bank_mask:0xf bound_ctrl:1
	v_add_f32_dpp v56, v56, v56 row_ror:8 row_mask:0xf bank_mask:0xf bound_ctrl:1
	ds_bpermute_b32 v57, v1, v56
	v_add_f32_dpp v60, v59, v59 row_ror:8 row_mask:0xf bank_mask:0xf bound_ctrl:1
	ds_bpermute_b32 v61, v1, v58
	ds_bpermute_b32 v59, v1, v55
	ds_bpermute_b32 v64, v1, v60
	s_waitcnt lgkmcnt(3)
	v_add_f32_e32 v56, v56, v57
	ds_bpermute_b32 v57, v50, v56
	s_mov_b64 s[0:1], 0x2380
	s_waitcnt lgkmcnt(2)
	v_add_f32_e32 v59, v55, v59
	s_waitcnt lgkmcnt(1)
	v_add_f32_e32 v55, v60, v64
	v_lshl_add_u64 v[24:25], v[24:25], 0, s[0:1]
	s_waitcnt lgkmcnt(0)
	v_add_f32_e32 v56, v56, v57
	v_fmamk_f32 v56, v56, 0x3b000000, v52
	v_mul_f32_e32 v57, 0x4f800000, v56
	v_cmp_gt_f32_e32 vcc, s18, v56
	s_nop 1
	v_cndmask_b32_e32 v56, v56, v57, vcc
	v_sqrt_f32_e32 v65, v56
	v_add_f32_e32 v57, v58, v61
	v_add_u32_e32 v58, -1, v65
	v_fma_f32 v60, -v58, v65, v56
	v_cmp_ge_f32_e64 s[0:1], 0, v60
	v_add_u32_e32 v60, 1, v65
	v_fma_f32 v61, -v60, v65, v56
	v_cndmask_b32_e64 v58, v65, v58, s[0:1]
	v_cmp_lt_f32_e64 s[0:1], 0, v61
	s_nop 1
	v_cndmask_b32_e64 v58, v58, v60, s[0:1]
	v_mul_f32_e32 v60, 0x37800000, v58
	v_cndmask_b32_e32 v58, v58, v60, vcc
	v_cmp_class_f32_e32 vcc, v56, v53
	ds_bpermute_b32 v60, v50, v59
	s_nop 0
	v_cndmask_b32_e32 v61, v58, v56, vcc
	v_div_scale_f32 v64, s[0:1], v61, v61, 1.0
	v_rcp_f32_e32 v65, v64
	ds_bpermute_b32 v58, v50, v57
	ds_bpermute_b32 v56, v50, v55
	v_fma_f32 v72, -v64, v65, 1.0
	v_fmac_f32_e32 v65, v72, v65
	v_div_scale_f32 v72, vcc, 1.0, v61, 1.0
	v_mul_f32_e32 v73, v72, v65
	v_fma_f32 v74, -v64, v73, v72
	v_fmac_f32_e32 v73, v74, v65
	v_fma_f32 v64, -v64, v73, v72
	v_div_fmas_f32 v64, v64, v65, v73
	v_div_fixup_f32 v64, v64, v61, 1.0
	v_pk_mul_f32 v[62:63], v[62:63], v[64:65] op_sel_hi:[1,0]
	s_andn2_b64 vcc, exec, s[10:11]
	s_waitcnt vmcnt(0)
	v_pk_fma_f32 v[72:73], v[12:13], v[62:63], v[16:17]
	v_pk_mul_f32 v[62:63], v[70:71], v[64:65] op_sel_hi:[1,0]
	s_nop 0
	v_pk_fma_f32 v[70:71], v[10:11], v[62:63], v[14:15]
	v_pk_mul_f32 v[62:63], v[68:69], v[64:65] op_sel_hi:[1,0]
	s_nop 0
	v_pk_fma_f32 v[68:69], v[4:5], v[62:63], v[8:9]
	v_pk_mul_f32 v[62:63], v[66:67], v[64:65] op_sel_hi:[1,0]
	v_cvt_pk_bf16_f32 v64, v70, v71
	v_pk_fma_f32 v[62:63], v[2:3], v[62:63], v[6:7]
	v_cvt_pk_bf16_f32 v65, v72, v73
	v_cvt_pk_bf16_f32 v62, v62, v63
	v_cvt_pk_bf16_f32 v63, v68, v69
	global_store_dwordx4 v[24:25], v[62:65], off
	s_cbranch_vccz .LBB0_925
	s_andn2_b64 vcc, exec, s[8:9]
	s_cbranch_vccz .LBB0_926

.LBB0_1006:
	ds_read_b64_tr_b16 v[82:83], v154
	ds_read_b64_tr_b16 v[86:87], v154 offset:32
	ds_read_b64_tr_b16 v[84:85], v145 offset:576
	ds_read_b64_tr_b16 v[88:89], v145 offset:608
	ds_read_b64_tr_b16 v[90:91], v154 offset:64
	ds_read_b64_tr_b16 v[92:93], v145 offset:640
	ds_read_b64_tr_b16 v[94:95], v154 offset:96
	ds_read_b64_tr_b16 v[96:97], v145 offset:672
	ds_read_b128 v[98:101], v155 offset:18432
	ds_read_b128 v[134:137], v155 offset:22784
	s_add_i32 s2, s22, s14
	s_ashr_i32 s3, s2, 31
	s_lshr_b32 s3, s3, 25
	s_waitcnt lgkmcnt(1)
	v_mfma_f32_16x16x32_bf16 v[102:105], v[82:85], v[98:101], 0
	s_add_i32 s3, s2, s3
	s_and_b32 s16, s3, 0xffffff80
	s_sub_i32 s14, s2, s16
	v_mfma_f32_16x16x32_bf16 v[106:109], v[86:89], v[98:101], 0
	s_ashr_i32 s15, s14, 31
	s_lshl_b64 s[14:15], s[14:15], 7
	s_ashr_i32 s17, s3, 7
	v_mfma_f32_16x16x32_bf16 v[110:113], v[90:93], v[98:101], 0
	s_lshl_b32 s18, s17, 6
	s_ashr_i32 s19, s18, 31
	v_mfma_f32_16x16x32_bf16 v[98:101], v[94:97], v[98:101], 0
	s_waitcnt lgkmcnt(0)
	v_mfma_f32_16x16x32_bf16 v[82:85], v[82:85], v[134:137], 0
	v_mfma_f32_16x16x32_bf16 v[86:89], v[86:89], v[134:137], 0
	v_mfma_f32_16x16x32_bf16 v[90:93], v[90:93], v[134:137], 0
	v_mfma_f32_16x16x32_bf16 v[94:97], v[94:97], v[134:137], 0
	ds_read_b64_tr_b16 v[134:135], v154 offset:4608
	ds_read_b64_tr_b16 v[136:137], v145 offset:5184
	ds_read_b64_tr_b16 v[138:139], v154 offset:4640
	ds_read_b64_tr_b16 v[140:141], v145 offset:5216
	ds_read_b64_tr_b16 v[160:161], v154 offset:4672
	ds_read_b64_tr_b16 v[162:163], v145 offset:5248
	ds_read_b64_tr_b16 v[164:165], v154 offset:4704
	ds_read_b64_tr_b16 v[166:167], v145 offset:5280
	ds_read_b128 v[168:171], v155 offset:18496
	s_waitcnt lgkmcnt(0)
	v_mfma_f32_16x16x32_bf16 v[102:105], v[134:137], v[168:171], v[102:105]
	v_mfma_f32_16x16x32_bf16 v[106:109], v[138:141], v[168:171], v[106:109]
	v_mfma_f32_16x16x32_bf16 v[110:113], v[160:163], v[168:171], v[110:113]
	v_mfma_f32_16x16x32_bf16 v[98:101], v[164:167], v[168:171], v[98:101]
	ds_read_b128 v[168:171], v155 offset:22848
	s_waitcnt lgkmcnt(0)
	v_mfma_f32_16x16x32_bf16 v[82:85], v[134:137], v[168:171], v[82:85]
	v_mfma_f32_16x16x32_bf16 v[86:89], v[138:141], v[168:171], v[86:89]
	v_mfma_f32_16x16x32_bf16 v[90:93], v[160:163], v[168:171], v[90:93]
	v_mfma_f32_16x16x32_bf16 v[94:97], v[164:167], v[168:171], v[94:97]
	ds_read_b64_tr_b16 v[134:135], v154 offset:9216
	ds_read_b64_tr_b16 v[136:137], v145 offset:9792
	ds_read_b64_tr_b16 v[138:139], v154 offset:9248
	ds_read_b64_tr_b16 v[140:141], v145 offset:9824
	ds_read_b64_tr_b16 v[160:161], v154 offset:9280
	ds_read_b64_tr_b16 v[162:163], v145 offset:9856
	ds_read_b64_tr_b16 v[164:165], v154 offset:9312
	ds_read_b64_tr_b16 v[166:167], v145 offset:9888
	ds_read_b128 v[168:171], v155 offset:18560
	s_waitcnt lgkmcnt(0)
	v_mfma_f32_16x16x32_bf16 v[172:175], v[160:163], v[168:171], v[110:113]
	s_nop 2
	ds_read_b128 v[110:113], v155 offset:22912
	v_mfma_f32_16x16x32_bf16 v[102:105], v[134:137], v[168:171], v[102:105]
	v_mfma_f32_16x16x32_bf16 v[106:109], v[138:141], v[168:171], v[106:109]
	v_mfma_f32_16x16x32_bf16 v[98:101], v[164:167], v[168:171], v[98:101]
	s_waitcnt lgkmcnt(0)
	v_mfma_f32_16x16x32_bf16 v[82:85], v[134:137], v[110:113], v[82:85]
	v_mfma_f32_16x16x32_bf16 v[86:89], v[138:141], v[110:113], v[86:89]
	v_mfma_f32_16x16x32_bf16 v[134:137], v[160:163], v[110:113], v[90:93]
	v_mfma_f32_16x16x32_bf16 v[138:141], v[164:167], v[110:113], v[94:97]
	s_nop 1
	ds_read_b64_tr_b16 v[90:91], v154 offset:13824
	ds_read_b64_tr_b16 v[92:93], v145 offset:14400
	ds_read_b64_tr_b16 v[160:161], v154 offset:13856
	ds_read_b64_tr_b16 v[162:163], v145 offset:14432
	ds_read_b64_tr_b16 v[164:165], v154 offset:13888
	ds_read_b64_tr_b16 v[166:167], v145 offset:14464
	ds_read_b64_tr_b16 v[168:169], v154 offset:13920
	ds_read_b64_tr_b16 v[170:171], v145 offset:14496
	ds_read_b128 v[94:97], v155 offset:18624
	s_waitcnt lgkmcnt(0)
	v_mfma_f32_16x16x32_bf16 v[110:113], v[90:93], v[94:97], v[102:105]
	v_mfma_f32_16x16x32_bf16 v[102:105], v[164:167], v[94:97], v[172:175]
	s_nop 2
	ds_read_b128 v[172:175], v155 offset:22976
	v_mfma_f32_16x16x32_bf16 v[106:109], v[160:163], v[94:97], v[106:109]
	v_mfma_f32_16x16x32_bf16 v[98:101], v[168:171], v[94:97], v[98:101]
	s_waitcnt lgkmcnt(0)
	v_mfma_f32_16x16x32_bf16 v[94:97], v[90:93], v[172:175], v[82:85]
	v_mfma_f32_16x16x32_bf16 v[90:93], v[160:163], v[172:175], v[86:89]
	v_mfma_f32_16x16x32_bf16 v[86:89], v[164:167], v[172:175], v[134:137]
	v_mfma_f32_16x16x32_bf16 v[82:85], v[168:171], v[172:175], v[138:141]
	s_nop 1
	v_mov_b64_e32 v[136:137], s[0:1]
	v_or_b32_e32 v134, s16, v116
	v_ashrrev_i32_e32 v135, 31, v134
	v_or_b32_e32 v138, s14, v116
	v_mad_u64_u32 v[136:137], s[20:21], v138, s25, v[136:137]
	v_mad_i32_i24 v137, s15, v157, v137
	v_lshl_add_u64 v[136:137], s[18:19], 1, v[136:137]
	v_lshl_add_u64 v[136:137], v[136:137], 0, v[114:115]
	v_add_co_u32_e32 v140, vcc, 0x1000, v136
	v_lshl_add_u64 v[134:135], v[134:135], 2, s[4:5]
	s_nop 0
	v_addc_co_u32_e32 v141, vcc, 0, v137, vcc
	global_load_dwordx2 v[140:141], v[140:141], off offset:3968
	v_mov_b32_e32 v139, s15
	global_load_dword v134, v[134:135], off
	s_waitcnt vmcnt(1)
	v_lshlrev_b32_e32 v123, 16, v140
	v_mul_f32_e32 v125, 0x3d372713, v123
	v_mul_f32_e32 v125, v125, v123
	v_fma_f32 v125, v125, v123, v123
	v_mul_f32_e32 v125, 0x3f4c422a, v125
	v_add_f32_e64 v127, |v125|, |v125|
	v_mul_f32_e32 v127, 0x3fb8aa3b, v127
	v_exp_f32_e32 v127, v127
	s_nop 0
	v_add_f32_e32 v127, 1.0, v127
	v_rcp_f32_e32 v127, v127
	s_nop 0
	v_fma_f32 v127, v127, -2.0, 1.0
	v_and_b32_e32 v129, 0xffff0000, v140
	v_mul_f32_e32 v131, 0x3d372713, v129
	v_mul_f32_e32 v131, v131, v129
	v_fma_f32 v131, v131, v129, v129
	v_mul_f32_e32 v131, 0x3f4c422a, v131
	v_add_f32_e64 v132, |v131|, |v131|
	v_mul_f32_e32 v132, 0x3fb8aa3b, v132
	v_exp_f32_e32 v132, v132
	s_nop 0
	v_add_f32_e32 v132, 1.0, v132
	v_rcp_f32_e32 v132, v132
	s_nop 0
	v_fma_f32 v132, v132, -2.0, 1.0
	v_lshlrev_b32_e32 v135, 16, v141
	v_mul_f32_e32 v140, 0x3d372713, v135
	v_mul_f32_e32 v140, v140, v135
	v_fma_f32 v140, v140, v135, v135
	v_mul_f32_e32 v140, 0x3f4c422a, v140
	v_add_f32_e64 v159, |v140|, |v140|
	v_mul_f32_e32 v159, 0x3fb8aa3b, v159
	v_exp_f32_e32 v159, v159
	s_nop 0
	v_add_f32_e32 v159, 1.0, v159
	v_rcp_f32_e32 v159, v159
	s_nop 0
	v_fma_f32 v159, v159, -2.0, 1.0
	v_and_b32_e32 v141, 0xffff0000, v141
	v_mul_f32_e32 v160, 0x3d372713, v141
	v_mul_f32_e32 v160, v160, v141
	v_fma_f32 v160, v160, v141, v141
	v_mul_f32_e32 v160, 0x3f4c422a, v160
	v_add_f32_e64 v161, |v160|, |v160|
	v_mul_f32_e32 v161, 0x3fb8aa3b, v161
	v_exp_f32_e32 v161, v161
	s_nop 0
	v_add_f32_e32 v161, 1.0, v161
	v_rcp_f32_e32 v161, v161
	s_nop 0
	v_fma_f32 v161, v161, -2.0, 1.0
	v_bfi_b32 v140, s30, v159, v140
	v_mul_f32_e32 v135, 0.5, v135
	v_add_f32_e32 v140, 1.0, v140
	v_mul_f32_e32 v135, v135, v140
	s_waitcnt vmcnt(0)
	v_add_f32_e32 v112, v112, v134
	v_mul_f32_e32 v140, v112, v135
	v_mul_f32_e32 v112, 0.5, v123
	v_bfi_b32 v123, s30, v127, v125
	v_add_f32_e32 v123, 1.0, v123
	v_mul_f32_e32 v112, v112, v123
	v_add_f32_e32 v110, v110, v134
	v_bfi_b32 v135, s30, v132, v131
	v_mov_b32_e32 v132, v111
	v_mul_f32_e32 v112, v110, v112
	v_mul_f32_e32 v123, 0.5, v129
	v_pk_add_f32 v[110:111], v[132:133], v[134:135]
	v_bfi_b32 v135, s30, v161, v160
	v_mul_f32_e32 v111, v123, v111
	v_mul_f32_e32 v110, v110, v111
	v_mov_b32_e32 v132, v113
	v_cvt_pk_bf16_f32 v112, v112, v110
	v_lshlrev_b64 v[110:111], 12, v[138:139]
	v_mul_f32_e32 v123, 0.5, v141
	v_pk_add_f32 v[138:139], v[132:133], v[134:135]
	v_lshl_add_u64 v[110:111], s[8:9], 0, v[110:111]
	v_mul_f32_e32 v113, v123, v139
	v_lshl_add_u64 v[110:111], s[18:19], 1, v[110:111]
	v_mul_f32_e32 v113, v138, v113
	v_lshl_add_u64 v[136:137], v[136:137], 0, s[10:11]
	v_lshl_add_u64 v[110:111], v[110:111], 0, v[114:115]
	v_cvt_pk_bf16_f32 v113, v140, v113
	global_store_dwordx2 v[110:111], v[112:113], off offset:2048
	global_load_dwordx2 v[112:113], v[136:137], off offset:32
	s_waitcnt vmcnt(0)
	v_lshlrev_b32_e32 v123, 16, v112
	v_mul_f32_e32 v125, 0x3d372713, v123
	v_mul_f32_e32 v125, v125, v123
	v_fma_f32 v125, v125, v123, v123
	v_mul_f32_e32 v125, 0x3f4c422a, v125
	v_add_f32_e64 v127, |v125|, |v125|
	v_mul_f32_e32 v127, 0x3fb8aa3b, v127
	v_exp_f32_e32 v127, v127
	s_nop 0
	v_add_f32_e32 v127, 1.0, v127
	v_rcp_f32_e32 v127, v127
	s_nop 0
	v_fma_f32 v127, v127, -2.0, 1.0
	v_and_b32_e32 v112, 0xffff0000, v112
	v_mul_f32_e32 v129, 0x3d372713, v112
	v_mul_f32_e32 v129, v129, v112
	v_fma_f32 v129, v129, v112, v112
	v_mul_f32_e32 v129, 0x3f4c422a, v129
	v_add_f32_e64 v131, |v129|, |v129|
	v_mul_f32_e32 v131, 0x3fb8aa3b, v131
	v_exp_f32_e32 v131, v131
	s_nop 0
	v_add_f32_e32 v131, 1.0, v131
	v_rcp_f32_e32 v131, v131
	s_nop 0
	v_fma_f32 v131, v131, -2.0, 1.0
	v_lshlrev_b32_e32 v132, 16, v113
	v_mul_f32_e32 v135, 0x3d372713, v132
	v_mul_f32_e32 v135, v135, v132
	v_fma_f32 v135, v135, v132, v132
	v_mul_f32_e32 v135, 0x3f4c422a, v135
	v_add_f32_e64 v138, |v135|, |v135|
	v_mul_f32_e32 v138, 0x3fb8aa3b, v138
	v_exp_f32_e32 v138, v138
	s_nop 0
	v_add_f32_e32 v138, 1.0, v138
	v_rcp_f32_e32 v138, v138
	s_nop 0
	v_fma_f32 v138, v138, -2.0, 1.0
	v_and_b32_e32 v113, 0xffff0000, v113
	v_mul_f32_e32 v139, 0x3d372713, v113
	v_mul_f32_e32 v139, v139, v113
	v_fma_f32 v139, v139, v113, v113
	v_mul_f32_e32 v139, 0x3f4c422a, v139
	v_add_f32_e64 v140, |v139|, |v139|
	v_mul_f32_e32 v140, 0x3fb8aa3b, v140
	v_exp_f32_e32 v140, v140
	s_nop 0
	v_add_f32_e32 v140, 1.0, v140
	v_rcp_f32_e32 v140, v140
	s_nop 0
	v_fma_f32 v140, v140, -2.0, 1.0
	v_bfi_b32 v135, s30, v138, v135
	v_mul_f32_e32 v132, 0.5, v132
	v_add_f32_e32 v135, 1.0, v135
	v_mul_f32_e32 v132, v132, v135
	v_add_f32_e32 v108, v108, v134
	v_mul_f32_e32 v138, v108, v132
	v_mul_f32_e32 v108, 0.5, v123
	v_bfi_b32 v123, s30, v127, v125
	v_add_f32_e32 v123, 1.0, v123
	v_mul_f32_e32 v108, v108, v123
	v_add_f32_e32 v106, v106, v134
	v_bfi_b32 v135, s30, v131, v129
	v_mov_b32_e32 v132, v107
	v_mul_f32_e32 v108, v106, v108
	v_mul_f32_e32 v112, 0.5, v112
	v_pk_add_f32 v[106:107], v[132:133], v[134:135]
	v_bfi_b32 v135, s30, v140, v139
	v_mul_f32_e32 v107, v112, v107
	v_mul_f32_e32 v106, v106, v107
	v_mov_b32_e32 v132, v109
	v_cvt_pk_bf16_f32 v106, v108, v106
	v_mul_f32_e32 v107, 0.5, v113
	v_pk_add_f32 v[108:109], v[132:133], v[134:135]
	s_nop 0
	v_mul_f32_e32 v107, v107, v109
	v_mul_f32_e32 v107, v108, v107
	v_cvt_pk_bf16_f32 v107, v138, v107
	global_store_dwordx2 v[110:111], v[106:107], off offset:2080
	global_load_dwordx2 v[106:107], v[136:137], off offset:64
	s_waitcnt vmcnt(0)
	v_lshlrev_b32_e32 v108, 16, v106
	v_mul_f32_e32 v109, 0x3d372713, v108
	v_mul_f32_e32 v109, v109, v108
	v_fma_f32 v109, v109, v108, v108
	v_mul_f32_e32 v109, 0x3f4c422a, v109
	v_add_f32_e64 v112, |v109|, |v109|
	v_mul_f32_e32 v112, 0x3fb8aa3b, v112
	v_exp_f32_e32 v112, v112
	s_nop 0
	v_add_f32_e32 v112, 1.0, v112
	v_rcp_f32_e32 v112, v112
	s_nop 0
	v_fma_f32 v112, v112, -2.0, 1.0
	v_and_b32_e32 v106, 0xffff0000, v106
	v_mul_f32_e32 v113, 0x3d372713, v106
	v_mul_f32_e32 v113, v113, v106
	v_fma_f32 v113, v113, v106, v106
	v_mul_f32_e32 v113, 0x3f4c422a, v113
	v_add_f32_e64 v123, |v113|, |v113|
	v_mul_f32_e32 v123, 0x3fb8aa3b, v123
	v_exp_f32_e32 v123, v123
	s_nop 0
	v_add_f32_e32 v123, 1.0, v123
	v_rcp_f32_e32 v123, v123
	s_nop 0
	v_fma_f32 v123, v123, -2.0, 1.0
	v_lshlrev_b32_e32 v125, 16, v107
	v_mul_f32_e32 v127, 0x3d372713, v125
	v_mul_f32_e32 v127, v127, v125
	v_fma_f32 v127, v127, v125, v125
	v_mul_f32_e32 v127, 0x3f4c422a, v127
	v_add_f32_e64 v129, |v127|, |v127|
	v_mul_f32_e32 v129, 0x3fb8aa3b, v129
	v_exp_f32_e32 v129, v129
	s_nop 0
	v_add_f32_e32 v129, 1.0, v129
	v_rcp_f32_e32 v129, v129
	s_nop 0
	v_fma_f32 v129, v129, -2.0, 1.0
	v_and_b32_e32 v107, 0xffff0000, v107
	v_mul_f32_e32 v131, 0x3d372713, v107
	v_mul_f32_e32 v131, v131, v107
	v_fma_f32 v131, v131, v107, v107
	v_mul_f32_e32 v131, 0x3f4c422a, v131
	v_add_f32_e64 v138, |v131|, |v131|
	v_mul_f32_e32 v138, 0x3fb8aa3b, v138
	v_exp_f32_e32 v138, v138
	s_nop 0
	v_add_f32_e32 v138, 1.0, v138
	v_rcp_f32_e32 v138, v138
	s_nop 0
	v_fma_f32 v138, v138, -2.0, 1.0
	v_bfi_b32 v127, s30, v129, v127
	v_mul_f32_e32 v125, 0.5, v125
	v_add_f32_e32 v127, 1.0, v127
	v_mul_f32_e32 v125, v125, v127
	v_add_f32_e32 v104, v104, v134
	v_mul_f32_e32 v125, v104, v125
	v_mul_f32_e32 v104, 0.5, v108
	v_bfi_b32 v108, s30, v112, v109
	v_add_f32_e32 v108, 1.0, v108
	v_mul_f32_e32 v104, v104, v108
	v_add_f32_e32 v102, v102, v134
	v_bfi_b32 v135, s30, v123, v113
	v_mov_b32_e32 v132, v103
	v_mul_f32_e32 v104, v102, v104
	v_mul_f32_e32 v106, 0.5, v106
	v_pk_add_f32 v[102:103], v[132:133], v[134:135]
	v_bfi_b32 v135, s30, v138, v131
	v_mul_f32_e32 v103, v106, v103
	v_mul_f32_e32 v102, v102, v103
	v_mov_b32_e32 v132, v105
	v_cvt_pk_bf16_f32 v102, v104, v102
	v_mul_f32_e32 v103, 0.5, v107
	v_pk_add_f32 v[104:105], v[132:133], v[134:135]
	s_nop 0
	v_mul_f32_e32 v103, v103, v105
	v_mul_f32_e32 v103, v104, v103
	v_cvt_pk_bf16_f32 v103, v125, v103
	global_store_dwordx2 v[110:111], v[102:103], off offset:2112
	global_load_dwordx2 v[102:103], v[136:137], off offset:96
	s_waitcnt vmcnt(0)
	v_lshlrev_b32_e32 v104, 16, v102
	v_mul_f32_e32 v105, 0x3d372713, v104
	v_mul_f32_e32 v105, v105, v104
	v_fma_f32 v105, v105, v104, v104
	v_mul_f32_e32 v105, 0x3f4c422a, v105
	v_add_f32_e64 v106, |v105|, |v105|
	v_mul_f32_e32 v106, 0x3fb8aa3b, v106
	v_exp_f32_e32 v106, v106
	s_nop 0
	v_add_f32_e32 v106, 1.0, v106
	v_rcp_f32_e32 v106, v106
	s_nop 0
	v_fma_f32 v106, v106, -2.0, 1.0
	v_and_b32_e32 v102, 0xffff0000, v102
	v_mul_f32_e32 v107, 0x3d372713, v102
	v_mul_f32_e32 v107, v107, v102
	v_fma_f32 v107, v107, v102, v102
	v_mul_f32_e32 v107, 0x3f4c422a, v107
	v_add_f32_e64 v108, |v107|, |v107|
	v_mul_f32_e32 v108, 0x3fb8aa3b, v108
	v_exp_f32_e32 v108, v108
	s_nop 0
	v_add_f32_e32 v108, 1.0, v108
	v_rcp_f32_e32 v108, v108
	s_nop 0
	v_fma_f32 v108, v108, -2.0, 1.0
	v_lshlrev_b32_e32 v109, 16, v103
	v_mul_f32_e32 v112, 0x3d372713, v109
	v_mul_f32_e32 v112, v112, v109
	v_fma_f32 v112, v112, v109, v109
	v_mul_f32_e32 v112, 0x3f4c422a, v112
	v_add_f32_e64 v113, |v112|, |v112|
	v_mul_f32_e32 v113, 0x3fb8aa3b, v113
	v_exp_f32_e32 v113, v113
	s_nop 0
	v_add_f32_e32 v113, 1.0, v113
	v_rcp_f32_e32 v113, v113
	s_nop 0
	v_fma_f32 v113, v113, -2.0, 1.0
	v_and_b32_e32 v103, 0xffff0000, v103
	v_mul_f32_e32 v123, 0x3d372713, v103
	v_mul_f32_e32 v123, v123, v103
	v_fma_f32 v123, v123, v103, v103
	v_mul_f32_e32 v123, 0x3f4c422a, v123
	v_add_f32_e64 v125, |v123|, |v123|
	v_mul_f32_e32 v125, 0x3fb8aa3b, v125
	v_exp_f32_e32 v125, v125
	s_nop 0
	v_add_f32_e32 v125, 1.0, v125
	v_rcp_f32_e32 v125, v125
	s_nop 0
	v_fma_f32 v125, v125, -2.0, 1.0
	v_bfi_b32 v112, s30, v113, v112
	v_mul_f32_e32 v109, 0.5, v109
	v_add_f32_e32 v112, 1.0, v112
	v_mul_f32_e32 v109, v109, v112
	v_add_f32_e32 v100, v100, v134
	v_mul_f32_e32 v109, v100, v109
	v_mul_f32_e32 v100, 0.5, v104
	v_bfi_b32 v104, s30, v106, v105
	v_add_f32_e32 v104, 1.0, v104
	v_mul_f32_e32 v100, v100, v104
	v_add_f32_e32 v98, v98, v134
	v_bfi_b32 v135, s30, v108, v107
	v_mov_b32_e32 v132, v99
	v_mul_f32_e32 v100, v98, v100
	v_mul_f32_e32 v102, 0.5, v102
	v_pk_add_f32 v[98:99], v[132:133], v[134:135]
	v_bfi_b32 v135, s30, v125, v123
	v_mul_f32_e32 v99, v102, v99
	v_mul_f32_e32 v98, v98, v99
	v_mov_b32_e32 v132, v101
	v_cvt_pk_bf16_f32 v98, v100, v98
	v_mul_f32_e32 v99, 0.5, v103
	v_pk_add_f32 v[100:101], v[132:133], v[134:135]
	s_ashr_i32 s17, s16, 31
	v_mul_f32_e32 v99, v99, v101
	v_mul_f32_e32 v99, v100, v99
	v_cvt_pk_bf16_f32 v99, v109, v99
	v_or_b32_e32 v102, s14, v118
	v_mov_b64_e32 v[100:101], s[0:1]
	global_store_dwordx2 v[110:111], v[98:99], off offset:2144
	v_lshl_add_u64 v[98:99], s[16:17], 0, v[116:117]
	v_mad_u64_u32 v[100:101], s[16:17], v102, s25, v[100:101]
	v_mad_i32_i24 v101, s15, v157, v101
	v_lshl_add_u64 v[100:101], s[18:19], 1, v[100:101]
	v_lshl_add_u64 v[100:101], v[100:101], 0, v[114:115]
	v_add_co_u32_e32 v104, vcc, 0x1000, v100
	v_lshl_add_u64 v[98:99], v[98:99], 2, s[4:5]
	s_nop 0
	v_addc_co_u32_e32 v105, vcc, 0, v101, vcc
	global_load_dwordx2 v[104:105], v[104:105], off offset:3968
	v_mov_b32_e32 v103, s15
	global_load_dword v98, v[98:99], off offset:64
	s_waitcnt vmcnt(1)
	v_lshlrev_b32_e32 v99, 16, v104
	v_mul_f32_e32 v106, 0x3d372713, v99
	v_mul_f32_e32 v106, v106, v99
	v_fma_f32 v106, v106, v99, v99
	v_mul_f32_e32 v106, 0x3f4c422a, v106
	v_add_f32_e64 v107, |v106|, |v106|
	v_mul_f32_e32 v107, 0x3fb8aa3b, v107
	v_exp_f32_e32 v107, v107
	s_nop 0
	v_add_f32_e32 v107, 1.0, v107
	v_rcp_f32_e32 v107, v107
	s_nop 0
	v_fma_f32 v107, v107, -2.0, 1.0
	v_and_b32_e32 v104, 0xffff0000, v104
	v_mul_f32_e32 v108, 0x3d372713, v104
	v_mul_f32_e32 v108, v108, v104
	v_fma_f32 v108, v108, v104, v104
	v_mul_f32_e32 v108, 0x3f4c422a, v108
	v_add_f32_e64 v109, |v108|, |v108|
	v_mul_f32_e32 v109, 0x3fb8aa3b, v109
	v_exp_f32_e32 v109, v109
	s_nop 0
	v_add_f32_e32 v109, 1.0, v109
	v_rcp_f32_e32 v109, v109
	s_nop 0
	v_fma_f32 v109, v109, -2.0, 1.0
	v_lshlrev_b32_e32 v110, 16, v105
	v_mul_f32_e32 v111, 0x3d372713, v110
	v_mul_f32_e32 v111, v111, v110
	v_fma_f32 v111, v111, v110, v110
	v_mul_f32_e32 v111, 0x3f4c422a, v111
	v_add_f32_e64 v112, |v111|, |v111|
	v_mul_f32_e32 v112, 0x3fb8aa3b, v112
	v_exp_f32_e32 v112, v112
	s_nop 0
	v_add_f32_e32 v112, 1.0, v112
	v_rcp_f32_e32 v112, v112
	s_nop 0
	v_fma_f32 v112, v112, -2.0, 1.0
	v_and_b32_e32 v105, 0xffff0000, v105
	v_mul_f32_e32 v113, 0x3d372713, v105
	v_mul_f32_e32 v113, v113, v105
	v_fma_f32 v113, v113, v105, v105
	v_mul_f32_e32 v113, 0x3f4c422a, v113
	v_add_f32_e64 v123, |v113|, |v113|
	v_mul_f32_e32 v123, 0x3fb8aa3b, v123
	v_exp_f32_e32 v123, v123
	s_nop 0
	v_add_f32_e32 v123, 1.0, v123
	v_rcp_f32_e32 v123, v123
	s_nop 0
	v_fma_f32 v123, v123, -2.0, 1.0
	v_bfi_b32 v111, s30, v112, v111
	v_mul_f32_e32 v110, 0.5, v110
	v_add_f32_e32 v111, 1.0, v111
	v_mul_f32_e32 v110, v110, v111
	s_waitcnt vmcnt(0)
	v_add_f32_e32 v96, v96, v98
	v_mul_f32_e32 v110, v96, v110
	v_mul_f32_e32 v96, 0.5, v99
	v_bfi_b32 v99, s30, v107, v106
	v_add_f32_e32 v99, 1.0, v99
	v_mul_f32_e32 v96, v96, v99
	v_add_f32_e32 v94, v94, v98
	v_bfi_b32 v99, s30, v109, v108
	v_mov_b32_e32 v132, v95
	v_mul_f32_e32 v96, v94, v96
	v_mul_f32_e32 v104, 0.5, v104
	v_pk_add_f32 v[94:95], v[132:133], v[98:99]
	v_bfi_b32 v99, s30, v123, v113
	v_mul_f32_e32 v95, v104, v95
	v_mul_f32_e32 v94, v94, v95
	v_mov_b32_e32 v132, v97
	v_cvt_pk_bf16_f32 v96, v96, v94
	v_lshlrev_b64 v[94:95], 12, v[102:103]
	v_mul_f32_e32 v104, 0.5, v105
	v_pk_add_f32 v[102:103], v[132:133], v[98:99]
	v_lshl_add_u64 v[94:95], s[8:9], 0, v[94:95]
	v_mul_f32_e32 v97, v104, v103
	v_lshl_add_u64 v[94:95], s[18:19], 1, v[94:95]
	v_mul_f32_e32 v97, v102, v97
	v_lshl_add_u64 v[100:101], v[100:101], 0, s[10:11]
	v_lshl_add_u64 v[94:95], v[94:95], 0, v[114:115]
	v_cvt_pk_bf16_f32 v97, v110, v97
	global_store_dwordx2 v[94:95], v[96:97], off offset:2048
	global_load_dwordx2 v[96:97], v[100:101], off offset:32
	s_waitcnt vmcnt(0)
	v_lshlrev_b32_e32 v99, 16, v96
	v_mul_f32_e32 v102, 0x3d372713, v99
	v_mul_f32_e32 v102, v102, v99
	v_fma_f32 v102, v102, v99, v99
	v_mul_f32_e32 v102, 0x3f4c422a, v102
	v_add_f32_e64 v103, |v102|, |v102|
	v_mul_f32_e32 v103, 0x3fb8aa3b, v103
	v_exp_f32_e32 v103, v103
	s_nop 0
	v_add_f32_e32 v103, 1.0, v103
	v_rcp_f32_e32 v103, v103
	s_nop 0
	v_fma_f32 v103, v103, -2.0, 1.0
	v_and_b32_e32 v96, 0xffff0000, v96
	v_mul_f32_e32 v104, 0x3d372713, v96
	v_mul_f32_e32 v104, v104, v96
	v_fma_f32 v104, v104, v96, v96
	v_mul_f32_e32 v104, 0x3f4c422a, v104
	v_add_f32_e64 v105, |v104|, |v104|
	v_mul_f32_e32 v105, 0x3fb8aa3b, v105
	v_exp_f32_e32 v105, v105
	s_nop 0
	v_add_f32_e32 v105, 1.0, v105
	v_rcp_f32_e32 v105, v105
	s_nop 0
	v_fma_f32 v105, v105, -2.0, 1.0
	v_lshlrev_b32_e32 v106, 16, v97
	v_mul_f32_e32 v107, 0x3d372713, v106
	v_mul_f32_e32 v107, v107, v106
	v_fma_f32 v107, v107, v106, v106
	v_mul_f32_e32 v107, 0x3f4c422a, v107
	v_add_f32_e64 v108, |v107|, |v107|
	v_mul_f32_e32 v108, 0x3fb8aa3b, v108
	v_exp_f32_e32 v108, v108
	s_nop 0
	v_add_f32_e32 v108, 1.0, v108
	v_rcp_f32_e32 v108, v108
	s_nop 0
	v_fma_f32 v108, v108, -2.0, 1.0
	v_and_b32_e32 v97, 0xffff0000, v97
	v_mul_f32_e32 v109, 0x3d372713, v97
	v_mul_f32_e32 v109, v109, v97
	v_fma_f32 v109, v109, v97, v97
	v_mul_f32_e32 v109, 0x3f4c422a, v109
	v_add_f32_e64 v110, |v109|, |v109|
	v_mul_f32_e32 v110, 0x3fb8aa3b, v110
	v_exp_f32_e32 v110, v110
	s_nop 0
	v_add_f32_e32 v110, 1.0, v110
	v_rcp_f32_e32 v110, v110
	s_nop 0
	v_fma_f32 v110, v110, -2.0, 1.0
	v_bfi_b32 v107, s30, v108, v107
	v_mul_f32_e32 v106, 0.5, v106
	v_add_f32_e32 v107, 1.0, v107
	v_mul_f32_e32 v106, v106, v107
	v_add_f32_e32 v92, v92, v98
	v_mul_f32_e32 v106, v92, v106
	v_mul_f32_e32 v92, 0.5, v99
	v_bfi_b32 v99, s30, v103, v102
	v_add_f32_e32 v99, 1.0, v99
	v_mul_f32_e32 v92, v92, v99
	v_add_f32_e32 v90, v90, v98
	v_bfi_b32 v99, s30, v105, v104
	v_mov_b32_e32 v132, v91
	v_mul_f32_e32 v92, v90, v92
	v_mul_f32_e32 v96, 0.5, v96
	v_pk_add_f32 v[90:91], v[132:133], v[98:99]
	v_bfi_b32 v99, s30, v110, v109
	v_mul_f32_e32 v91, v96, v91
	v_mul_f32_e32 v90, v90, v91
	v_mov_b32_e32 v132, v93
	v_cvt_pk_bf16_f32 v90, v92, v90
	v_mul_f32_e32 v91, 0.5, v97
	v_pk_add_f32 v[92:93], v[132:133], v[98:99]
	s_nop 0
	v_mul_f32_e32 v91, v91, v93
	v_mul_f32_e32 v91, v92, v91
	v_cvt_pk_bf16_f32 v91, v106, v91
	global_store_dwordx2 v[94:95], v[90:91], off offset:2080
	global_load_dwordx2 v[90:91], v[100:101], off offset:64
	s_waitcnt vmcnt(0)
	v_lshlrev_b32_e32 v92, 16, v90
	v_mul_f32_e32 v93, 0x3d372713, v92
	v_mul_f32_e32 v93, v93, v92
	v_fma_f32 v93, v93, v92, v92
	v_mul_f32_e32 v93, 0x3f4c422a, v93
	v_add_f32_e64 v96, |v93|, |v93|
	v_mul_f32_e32 v96, 0x3fb8aa3b, v96
	v_exp_f32_e32 v96, v96
	s_nop 0
	v_add_f32_e32 v96, 1.0, v96
	v_rcp_f32_e32 v96, v96
	s_nop 0
	v_fma_f32 v96, v96, -2.0, 1.0
	v_and_b32_e32 v90, 0xffff0000, v90
	v_mul_f32_e32 v97, 0x3d372713, v90
	v_mul_f32_e32 v97, v97, v90
	v_fma_f32 v97, v97, v90, v90
	v_mul_f32_e32 v97, 0x3f4c422a, v97
	v_add_f32_e64 v99, |v97|, |v97|
	v_mul_f32_e32 v99, 0x3fb8aa3b, v99
	v_exp_f32_e32 v99, v99
	s_nop 0
	v_add_f32_e32 v99, 1.0, v99
	v_rcp_f32_e32 v99, v99
	s_nop 0
	v_fma_f32 v99, v99, -2.0, 1.0
	v_lshlrev_b32_e32 v102, 16, v91
	v_mul_f32_e32 v103, 0x3d372713, v102
	v_mul_f32_e32 v103, v103, v102
	v_fma_f32 v103, v103, v102, v102
	v_mul_f32_e32 v103, 0x3f4c422a, v103
	v_add_f32_e64 v104, |v103|, |v103|
	v_mul_f32_e32 v104, 0x3fb8aa3b, v104
	v_exp_f32_e32 v104, v104
	s_nop 0
	v_add_f32_e32 v104, 1.0, v104
	v_rcp_f32_e32 v104, v104
	s_nop 0
	v_fma_f32 v104, v104, -2.0, 1.0
	v_and_b32_e32 v91, 0xffff0000, v91
	v_mul_f32_e32 v105, 0x3d372713, v91
	v_mul_f32_e32 v105, v105, v91
	v_fma_f32 v105, v105, v91, v91
	v_mul_f32_e32 v105, 0x3f4c422a, v105
	v_add_f32_e64 v106, |v105|, |v105|
	v_mul_f32_e32 v106, 0x3fb8aa3b, v106
	v_exp_f32_e32 v106, v106
	s_nop 0
	v_add_f32_e32 v106, 1.0, v106
	v_rcp_f32_e32 v106, v106
	s_nop 0
	v_fma_f32 v106, v106, -2.0, 1.0
	v_bfi_b32 v103, s30, v104, v103
	v_mul_f32_e32 v102, 0.5, v102
	v_add_f32_e32 v103, 1.0, v103
	v_mul_f32_e32 v102, v102, v103
	v_add_f32_e32 v88, v88, v98
	v_mul_f32_e32 v102, v88, v102
	v_mul_f32_e32 v88, 0.5, v92
	v_bfi_b32 v92, s30, v96, v93
	v_add_f32_e32 v92, 1.0, v92
	v_mul_f32_e32 v88, v88, v92
	v_add_f32_e32 v86, v86, v98
	v_bfi_b32 v99, s30, v99, v97
	v_mov_b32_e32 v132, v87
	v_mul_f32_e32 v88, v86, v88
	v_mul_f32_e32 v90, 0.5, v90
	v_pk_add_f32 v[86:87], v[132:133], v[98:99]
	v_bfi_b32 v99, s30, v106, v105
	v_mul_f32_e32 v87, v90, v87
	v_mul_f32_e32 v86, v86, v87
	v_mov_b32_e32 v132, v89
	v_cvt_pk_bf16_f32 v86, v88, v86
	v_mul_f32_e32 v87, 0.5, v91
	v_pk_add_f32 v[88:89], v[132:133], v[98:99]
	s_nop 0
	v_mul_f32_e32 v87, v87, v89
	v_mul_f32_e32 v87, v88, v87
	v_cvt_pk_bf16_f32 v87, v102, v87
	global_store_dwordx2 v[94:95], v[86:87], off offset:2112
	global_load_dwordx2 v[86:87], v[100:101], off offset:96
	s_waitcnt vmcnt(0)
	v_lshlrev_b32_e32 v88, 16, v86
	v_mul_f32_e32 v89, 0x3d372713, v88
	v_mul_f32_e32 v89, v89, v88
	v_fma_f32 v89, v89, v88, v88
	v_mul_f32_e32 v89, 0x3f4c422a, v89
	v_add_f32_e64 v90, |v89|, |v89|
	v_mul_f32_e32 v90, 0x3fb8aa3b, v90
	v_exp_f32_e32 v90, v90
	s_nop 0
	v_add_f32_e32 v90, 1.0, v90
	v_rcp_f32_e32 v90, v90
	s_nop 0
	v_fma_f32 v90, v90, -2.0, 1.0
	v_and_b32_e32 v86, 0xffff0000, v86
	v_mul_f32_e32 v91, 0x3d372713, v86
	v_mul_f32_e32 v91, v91, v86
	v_fma_f32 v91, v91, v86, v86
	v_mul_f32_e32 v91, 0x3f4c422a, v91
	v_add_f32_e64 v92, |v91|, |v91|
	v_mul_f32_e32 v92, 0x3fb8aa3b, v92
	v_exp_f32_e32 v92, v92
	s_nop 0
	v_add_f32_e32 v92, 1.0, v92
	v_rcp_f32_e32 v92, v92
	s_nop 0
	v_fma_f32 v92, v92, -2.0, 1.0
	v_lshlrev_b32_e32 v93, 16, v87
	v_mul_f32_e32 v96, 0x3d372713, v93
	v_mul_f32_e32 v96, v96, v93
	v_fma_f32 v96, v96, v93, v93
	v_mul_f32_e32 v96, 0x3f4c422a, v96
	v_add_f32_e64 v97, |v96|, |v96|
	v_mul_f32_e32 v97, 0x3fb8aa3b, v97
	v_exp_f32_e32 v97, v97
	s_nop 0
	v_add_f32_e32 v97, 1.0, v97
	v_rcp_f32_e32 v97, v97
	s_nop 0
	v_fma_f32 v97, v97, -2.0, 1.0
	v_and_b32_e32 v87, 0xffff0000, v87
	v_mul_f32_e32 v99, 0x3d372713, v87
	v_mul_f32_e32 v99, v99, v87
	v_fma_f32 v99, v99, v87, v87
	v_mul_f32_e32 v100, 0x3f4c422a, v99
	v_cmp_nlt_f32_e64 s[14:15], |v100|, s26
	s_and_saveexec_b64 s[16:17], s[14:15]
	s_xor_b64 s[14:15], exec, s[16:17]
	s_cbranch_execz .LBB0_1132
	v_add_f32_e64 v99, |v100|, |v100|
	v_mul_f32_e32 v101, 0x3fb8aa3b, v99
	v_rndne_f32_e32 v102, v101
	v_sub_f32_e32 v103, v101, v102
	v_fma_f32 v101, v99, s27, -v101
	v_fmac_f32_e32 v101, 0x32a5705f, v99
	v_add_f32_e32 v101, v103, v101
	v_cvt_i32_f32_e32 v102, v102
	v_exp_f32_e32 v101, v101
	v_cmp_ngt_f32_e32 vcc, s28, v99
	v_ldexp_f32 v101, v101, v102
	s_nop 0
	v_cndmask_b32_e32 v101, 0, v101, vcc
	v_cmp_nlt_f32_e32 vcc, s29, v99
	s_nop 1
	v_cndmask_b32_e32 v99, v158, v101, vcc
	v_add_f32_e32 v99, 1.0, v99
	v_rcp_f32_e32 v99, v99
	s_nop 0
	v_fma_f32 v101, v99, -2.0, 1.0

.LBB0_2697:
	s_andn2_saveexec_b64 s[50:51], s[50:51]
	s_cbranch_execz .LBB0_2731
	v_add_f32_e64 v120, |v126|, |v126|
	v_mul_f32_e32 v120, 0x3fb8aa3b, v120
	v_exp_f32_e32 v120, v120
	s_nop 0
	v_add_f32_e32 v120, 1.0, v120
	v_rcp_f32_e32 v120, v120
	s_nop 0
	v_fma_f32 v120, v120, -2.0, 1.0
	v_add_f32_e64 v121, |v127|, |v127|
	v_mul_f32_e32 v121, 0x3fb8aa3b, v121
	v_exp_f32_e32 v121, v121
	s_nop 0
	v_add_f32_e32 v121, 1.0, v121
	v_rcp_f32_e32 v121, v121
	s_nop 0
	v_fma_f32 v121, v121, -2.0, 1.0
	v_add_f32_e64 v122, |v114|, |v114|
	v_mul_f32_e32 v122, 0x3fb8aa3b, v122
	v_exp_f32_e32 v122, v122
	s_nop 0
	v_add_f32_e32 v122, 1.0, v122
	v_rcp_f32_e32 v122, v122
	s_nop 0
	v_fma_f32 v122, v122, -2.0, 1.0
	v_add_f32_e64 v123, |v115|, |v115|
	v_mul_f32_e32 v123, 0x3fb8aa3b, v123
	v_exp_f32_e32 v123, v123
	s_nop 0
	v_add_f32_e32 v123, 1.0, v123
	v_rcp_f32_e32 v123, v123
	s_nop 0
	v_fma_f32 v123, v123, -2.0, 1.0
	v_add_f32_e64 v124, |v118|, |v118|
	v_mul_f32_e32 v124, 0x3fb8aa3b, v124
	v_exp_f32_e32 v124, v124
	s_nop 0
	v_add_f32_e32 v124, 1.0, v124
	v_rcp_f32_e32 v124, v124
	s_nop 0
	v_fma_f32 v124, v124, -2.0, 1.0
	v_add_f32_e64 v125, |v119|, |v119|
	v_mul_f32_e32 v125, 0x3fb8aa3b, v125
	v_exp_f32_e32 v125, v125
	s_nop 0
	v_add_f32_e32 v125, 1.0, v125
	v_rcp_f32_e32 v125, v125
	s_nop 0
	v_fma_f32 v125, v125, -2.0, 1.0
	v_add_f32_e64 v128, |v116|, |v116|
	v_mul_f32_e32 v128, 0x3fb8aa3b, v128
	v_exp_f32_e32 v128, v128
	s_nop 0
	v_add_f32_e32 v128, 1.0, v128
	v_rcp_f32_e32 v128, v128
	s_nop 0
	v_fma_f32 v128, v128, -2.0, 1.0
	v_add_f32_e64 v129, |v117|, |v117|
	v_mul_f32_e32 v129, 0x3fb8aa3b, v129
	v_exp_f32_e32 v129, v129
	s_nop 0
	v_add_f32_e32 v129, 1.0, v129
	v_rcp_f32_e32 v129, v129
	s_nop 0
	v_fma_f32 v129, v129, -2.0, 1.0
	v_bfi_b32 v126, s91, v120, v126
	v_bfi_b32 v127, s91, v121, v127
	v_bfi_b32 v114, s91, v122, v114
	v_bfi_b32 v115, s91, v123, v115
	v_bfi_b32 v118, s91, v124, v118
	v_bfi_b32 v119, s91, v125, v119
	v_bfi_b32 v116, s91, v128, v116
	v_bfi_b32 v117, s91, v129, v117

.LBB0_2754:
	s_andn2_saveexec_b64 s[50:51], s[50:51]
	s_cbranch_execz .LBB0_2788
	v_add_f32_e64 v118, |v114|, |v114|
	v_mul_f32_e32 v118, 0x3fb8aa3b, v118
	v_exp_f32_e32 v118, v118
	s_nop 0
	v_add_f32_e32 v118, 1.0, v118
	v_rcp_f32_e32 v118, v118
	s_nop 0
	v_fma_f32 v118, v118, -2.0, 1.0
	v_add_f32_e64 v119, |v115|, |v115|
	v_mul_f32_e32 v119, 0x3fb8aa3b, v119
	v_exp_f32_e32 v119, v119
	s_nop 0
	v_add_f32_e32 v119, 1.0, v119
	v_rcp_f32_e32 v119, v119
	s_nop 0
	v_fma_f32 v119, v119, -2.0, 1.0
	v_add_f32_e64 v122, |v110|, |v110|
	v_mul_f32_e32 v122, 0x3fb8aa3b, v122
	v_exp_f32_e32 v122, v122
	s_nop 0
	v_add_f32_e32 v122, 1.0, v122
	v_rcp_f32_e32 v122, v122
	s_nop 0
	v_fma_f32 v122, v122, -2.0, 1.0
	v_add_f32_e64 v123, |v111|, |v111|
	v_mul_f32_e32 v123, 0x3fb8aa3b, v123
	v_exp_f32_e32 v123, v123
	s_nop 0
	v_add_f32_e32 v123, 1.0, v123
	v_rcp_f32_e32 v123, v123
	s_nop 0
	v_fma_f32 v123, v123, -2.0, 1.0
	v_add_f32_e64 v124, |v116|, |v116|
	v_mul_f32_e32 v124, 0x3fb8aa3b, v124
	v_exp_f32_e32 v124, v124
	s_nop 0
	v_add_f32_e32 v124, 1.0, v124
	v_rcp_f32_e32 v124, v124
	s_nop 0
	v_fma_f32 v124, v124, -2.0, 1.0
	v_add_f32_e64 v125, |v117|, |v117|
	v_mul_f32_e32 v125, 0x3fb8aa3b, v125
	v_exp_f32_e32 v125, v125
	s_nop 0
	v_add_f32_e32 v125, 1.0, v125
	v_rcp_f32_e32 v125, v125
	s_nop 0
	v_fma_f32 v125, v125, -2.0, 1.0
	v_add_f32_e64 v126, |v112|, |v112|
	v_mul_f32_e32 v126, 0x3fb8aa3b, v126
	v_exp_f32_e32 v126, v126
	s_nop 0
	v_add_f32_e32 v126, 1.0, v126
	v_rcp_f32_e32 v126, v126
	s_nop 0
	v_fma_f32 v126, v126, -2.0, 1.0
	v_add_f32_e64 v127, |v113|, |v113|
	v_mul_f32_e32 v127, 0x3fb8aa3b, v127
	v_exp_f32_e32 v127, v127
	s_nop 0
	v_add_f32_e32 v127, 1.0, v127
	v_rcp_f32_e32 v127, v127
	s_nop 0
	v_fma_f32 v127, v127, -2.0, 1.0
	v_bfi_b32 v114, s91, v118, v114
	v_bfi_b32 v115, s91, v119, v115
	v_bfi_b32 v110, s91, v122, v110
	v_bfi_b32 v111, s91, v123, v111
	v_bfi_b32 v116, s91, v124, v116
	v_bfi_b32 v117, s91, v125, v117
	v_bfi_b32 v112, s91, v126, v112
	v_bfi_b32 v113, s91, v127, v113

.LBB0_2805:
	s_andn2_saveexec_b64 s[48:49], s[48:49]
	s_cbranch_execz .LBB0_2839
	v_add_f32_e64 v114, |v110|, |v110|
	v_mul_f32_e32 v114, 0x3fb8aa3b, v114
	v_exp_f32_e32 v114, v114
	s_nop 0
	v_add_f32_e32 v114, 1.0, v114
	v_rcp_f32_e32 v114, v114
	s_nop 0
	v_fma_f32 v114, v114, -2.0, 1.0
	v_add_f32_e64 v115, |v111|, |v111|
	v_mul_f32_e32 v115, 0x3fb8aa3b, v115
	v_exp_f32_e32 v115, v115
	s_nop 0
	v_add_f32_e32 v115, 1.0, v115
	v_rcp_f32_e32 v115, v115
	s_nop 0
	v_fma_f32 v115, v115, -2.0, 1.0
	v_add_f32_e64 v117, |v106|, |v106|
	v_mul_f32_e32 v117, 0x3fb8aa3b, v117
	v_exp_f32_e32 v117, v117
	s_nop 0
	v_add_f32_e32 v117, 1.0, v117
	v_rcp_f32_e32 v117, v117
	s_nop 0
	v_fma_f32 v117, v117, -2.0, 1.0
	v_add_f32_e64 v118, |v107|, |v107|
	v_mul_f32_e32 v118, 0x3fb8aa3b, v118
	v_exp_f32_e32 v118, v118
	s_nop 0
	v_add_f32_e32 v118, 1.0, v118
	v_rcp_f32_e32 v118, v118
	s_nop 0
	v_fma_f32 v118, v118, -2.0, 1.0
	v_add_f32_e64 v119, |v112|, |v112|
	v_mul_f32_e32 v119, 0x3fb8aa3b, v119
	v_exp_f32_e32 v119, v119
	s_nop 0
	v_add_f32_e32 v119, 1.0, v119
	v_rcp_f32_e32 v119, v119
	s_nop 0
	v_fma_f32 v119, v119, -2.0, 1.0
	v_add_f32_e64 v121, |v113|, |v113|
	v_mul_f32_e32 v121, 0x3fb8aa3b, v121
	v_exp_f32_e32 v121, v121
	s_nop 0
	v_add_f32_e32 v121, 1.0, v121
	v_rcp_f32_e32 v121, v121
	s_nop 0
	v_fma_f32 v121, v121, -2.0, 1.0
	v_add_f32_e64 v122, |v108|, |v108|
	v_mul_f32_e32 v122, 0x3fb8aa3b, v122
	v_exp_f32_e32 v122, v122
	s_nop 0
	v_add_f32_e32 v122, 1.0, v122
	v_rcp_f32_e32 v122, v122
	s_nop 0
	v_fma_f32 v122, v122, -2.0, 1.0
	v_add_f32_e64 v123, |v109|, |v109|
	v_mul_f32_e32 v123, 0x3fb8aa3b, v123
	v_exp_f32_e32 v123, v123
	s_nop 0
	v_add_f32_e32 v123, 1.0, v123
	v_rcp_f32_e32 v123, v123
	s_nop 0
	v_fma_f32 v123, v123, -2.0, 1.0
	v_bfi_b32 v110, s91, v114, v110
	v_bfi_b32 v111, s91, v115, v111
	v_bfi_b32 v106, s91, v117, v106
	v_bfi_b32 v107, s91, v118, v107
	v_bfi_b32 v112, s91, v119, v112
	v_bfi_b32 v113, s91, v121, v113
	v_bfi_b32 v108, s91, v122, v108
	v_bfi_b32 v109, s91, v123, v109

.LBB0_2856:
	s_andn2_saveexec_b64 s[46:47], s[46:47]
	s_cbranch_execz .LBB0_2890
	v_add_f32_e64 v110, |v106|, |v106|
	v_mul_f32_e32 v110, 0x3fb8aa3b, v110
	v_exp_f32_e32 v110, v110
	s_nop 0
	v_add_f32_e32 v110, 1.0, v110
	v_rcp_f32_e32 v110, v110
	s_nop 0
	v_fma_f32 v110, v110, -2.0, 1.0
	v_add_f32_e64 v111, |v107|, |v107|
	v_mul_f32_e32 v111, 0x3fb8aa3b, v111
	v_exp_f32_e32 v111, v111
	s_nop 0
	v_add_f32_e32 v111, 1.0, v111
	v_rcp_f32_e32 v111, v111
	s_nop 0
	v_fma_f32 v111, v111, -2.0, 1.0
	v_add_f32_e64 v113, |v102|, |v102|
	v_mul_f32_e32 v113, 0x3fb8aa3b, v113
	v_exp_f32_e32 v113, v113
	s_nop 0
	v_add_f32_e32 v113, 1.0, v113
	v_rcp_f32_e32 v113, v113
	s_nop 0
	v_fma_f32 v113, v113, -2.0, 1.0
	v_add_f32_e64 v114, |v103|, |v103|
	v_mul_f32_e32 v114, 0x3fb8aa3b, v114
	v_exp_f32_e32 v114, v114
	s_nop 0
	v_add_f32_e32 v114, 1.0, v114
	v_rcp_f32_e32 v114, v114
	s_nop 0
	v_fma_f32 v114, v114, -2.0, 1.0
	v_add_f32_e64 v115, |v108|, |v108|
	v_mul_f32_e32 v115, 0x3fb8aa3b, v115
	v_exp_f32_e32 v115, v115
	s_nop 0
	v_add_f32_e32 v115, 1.0, v115
	v_rcp_f32_e32 v115, v115
	s_nop 0
	v_fma_f32 v115, v115, -2.0, 1.0
	v_add_f32_e64 v116, |v109|, |v109|
	v_mul_f32_e32 v116, 0x3fb8aa3b, v116
	v_exp_f32_e32 v116, v116
	s_nop 0
	v_add_f32_e32 v116, 1.0, v116
	v_rcp_f32_e32 v116, v116
	s_nop 0
	v_fma_f32 v116, v116, -2.0, 1.0
	v_add_f32_e64 v117, |v104|, |v104|
	v_mul_f32_e32 v117, 0x3fb8aa3b, v117
	v_exp_f32_e32 v117, v117
	s_nop 0
	v_add_f32_e32 v117, 1.0, v117
	v_rcp_f32_e32 v117, v117
	s_nop 0
	v_fma_f32 v117, v117, -2.0, 1.0
	v_add_f32_e64 v118, |v105|, |v105|
	v_mul_f32_e32 v118, 0x3fb8aa3b, v118
	v_exp_f32_e32 v118, v118
	s_nop 0
	v_add_f32_e32 v118, 1.0, v118
	v_rcp_f32_e32 v118, v118
	s_nop 0
	v_fma_f32 v118, v118, -2.0, 1.0
	v_bfi_b32 v106, s91, v110, v106
	v_bfi_b32 v107, s91, v111, v107
	v_bfi_b32 v102, s91, v113, v102
	v_bfi_b32 v103, s91, v114, v103
	v_bfi_b32 v108, s91, v115, v108
	v_bfi_b32 v109, s91, v116, v109
	v_bfi_b32 v104, s91, v117, v104
	v_bfi_b32 v105, s91, v118, v105

.LBB0_2907:
	s_andn2_saveexec_b64 s[22:23], s[22:23]
	s_cbranch_execz .LBB0_2941
	v_add_f32_e64 v106, |v102|, |v102|
	v_mul_f32_e32 v106, 0x3fb8aa3b, v106
	v_exp_f32_e32 v106, v106
	s_nop 0
	v_add_f32_e32 v106, 1.0, v106
	v_rcp_f32_e32 v106, v106
	s_nop 0
	v_fma_f32 v106, v106, -2.0, 1.0
	v_add_f32_e64 v107, |v103|, |v103|
	v_mul_f32_e32 v107, 0x3fb8aa3b, v107
	v_exp_f32_e32 v107, v107
	s_nop 0
	v_add_f32_e32 v107, 1.0, v107
	v_rcp_f32_e32 v107, v107
	s_nop 0
	v_fma_f32 v107, v107, -2.0, 1.0
	v_add_f32_e64 v109, |v98|, |v98|
	v_mul_f32_e32 v109, 0x3fb8aa3b, v109
	v_exp_f32_e32 v109, v109
	s_nop 0
	v_add_f32_e32 v109, 1.0, v109
	v_rcp_f32_e32 v109, v109
	s_nop 0
	v_fma_f32 v109, v109, -2.0, 1.0
	v_add_f32_e64 v110, |v99|, |v99|
	v_mul_f32_e32 v110, 0x3fb8aa3b, v110
	v_exp_f32_e32 v110, v110
	s_nop 0
	v_add_f32_e32 v110, 1.0, v110
	v_rcp_f32_e32 v110, v110
	s_nop 0
	v_fma_f32 v110, v110, -2.0, 1.0
	v_add_f32_e64 v111, |v104|, |v104|
	v_mul_f32_e32 v111, 0x3fb8aa3b, v111
	v_exp_f32_e32 v111, v111
	s_nop 0
	v_add_f32_e32 v111, 1.0, v111
	v_rcp_f32_e32 v111, v111
	s_nop 0
	v_fma_f32 v111, v111, -2.0, 1.0
	v_add_f32_e64 v112, |v105|, |v105|
	v_mul_f32_e32 v112, 0x3fb8aa3b, v112
	v_exp_f32_e32 v112, v112
	s_nop 0
	v_add_f32_e32 v112, 1.0, v112
	v_rcp_f32_e32 v112, v112
	s_nop 0
	v_fma_f32 v112, v112, -2.0, 1.0
	v_add_f32_e64 v113, |v100|, |v100|
	v_mul_f32_e32 v113, 0x3fb8aa3b, v113
	v_exp_f32_e32 v113, v113
	s_nop 0
	v_add_f32_e32 v113, 1.0, v113
	v_rcp_f32_e32 v113, v113
	s_nop 0
	v_fma_f32 v113, v113, -2.0, 1.0
	v_add_f32_e64 v114, |v101|, |v101|
	v_mul_f32_e32 v114, 0x3fb8aa3b, v114
	v_exp_f32_e32 v114, v114
	s_nop 0
	v_add_f32_e32 v114, 1.0, v114
	v_rcp_f32_e32 v114, v114
	s_nop 0
	v_fma_f32 v114, v114, -2.0, 1.0
	v_bfi_b32 v102, s91, v106, v102
	v_bfi_b32 v103, s91, v107, v103
	v_bfi_b32 v98, s91, v109, v98
	v_bfi_b32 v99, s91, v110, v99
	v_bfi_b32 v104, s91, v111, v104
	v_bfi_b32 v105, s91, v112, v105
	v_bfi_b32 v100, s91, v113, v100
	v_bfi_b32 v101, s91, v114, v101

.LBB0_2958:
	s_andn2_saveexec_b64 s[20:21], s[20:21]
	s_cbranch_execz .LBB0_2992
	v_add_f32_e64 v102, |v98|, |v98|
	v_mul_f32_e32 v102, 0x3fb8aa3b, v102
	v_exp_f32_e32 v102, v102
	s_nop 0
	v_add_f32_e32 v102, 1.0, v102
	v_rcp_f32_e32 v102, v102
	s_nop 0
	v_fma_f32 v102, v102, -2.0, 1.0
	v_add_f32_e64 v103, |v99|, |v99|
	v_mul_f32_e32 v103, 0x3fb8aa3b, v103
	v_exp_f32_e32 v103, v103
	s_nop 0
	v_add_f32_e32 v103, 1.0, v103
	v_rcp_f32_e32 v103, v103
	s_nop 0
	v_fma_f32 v103, v103, -2.0, 1.0
	v_add_f32_e64 v105, |v94|, |v94|
	v_mul_f32_e32 v105, 0x3fb8aa3b, v105
	v_exp_f32_e32 v105, v105
	s_nop 0
	v_add_f32_e32 v105, 1.0, v105
	v_rcp_f32_e32 v105, v105
	s_nop 0
	v_fma_f32 v105, v105, -2.0, 1.0
	v_add_f32_e64 v106, |v95|, |v95|
	v_mul_f32_e32 v106, 0x3fb8aa3b, v106
	v_exp_f32_e32 v106, v106
	s_nop 0
	v_add_f32_e32 v106, 1.0, v106
	v_rcp_f32_e32 v106, v106
	s_nop 0
	v_fma_f32 v106, v106, -2.0, 1.0
	v_add_f32_e64 v107, |v100|, |v100|
	v_mul_f32_e32 v107, 0x3fb8aa3b, v107
	v_exp_f32_e32 v107, v107
	s_nop 0
	v_add_f32_e32 v107, 1.0, v107
	v_rcp_f32_e32 v107, v107
	s_nop 0
	v_fma_f32 v107, v107, -2.0, 1.0
	v_add_f32_e64 v108, |v101|, |v101|
	v_mul_f32_e32 v108, 0x3fb8aa3b, v108
	v_exp_f32_e32 v108, v108
	s_nop 0
	v_add_f32_e32 v108, 1.0, v108
	v_rcp_f32_e32 v108, v108
	s_nop 0
	v_fma_f32 v108, v108, -2.0, 1.0
	v_add_f32_e64 v109, |v96|, |v96|
	v_mul_f32_e32 v109, 0x3fb8aa3b, v109
	v_exp_f32_e32 v109, v109
	s_nop 0
	v_add_f32_e32 v109, 1.0, v109
	v_rcp_f32_e32 v109, v109
	s_nop 0
	v_fma_f32 v109, v109, -2.0, 1.0
	v_add_f32_e64 v110, |v97|, |v97|
	v_mul_f32_e32 v110, 0x3fb8aa3b, v110
	v_exp_f32_e32 v110, v110
	s_nop 0
	v_add_f32_e32 v110, 1.0, v110
	v_rcp_f32_e32 v110, v110
	s_nop 0
	v_fma_f32 v110, v110, -2.0, 1.0
	v_bfi_b32 v98, s91, v102, v98
	v_bfi_b32 v99, s91, v103, v99
	v_bfi_b32 v94, s91, v105, v94
	v_bfi_b32 v95, s91, v106, v95
	v_bfi_b32 v100, s91, v107, v100
	v_bfi_b32 v101, s91, v108, v101
	v_bfi_b32 v96, s91, v109, v96
	v_bfi_b32 v97, s91, v110, v97

.LBB0_3009:
	s_andn2_saveexec_b64 s[18:19], s[18:19]
	s_cbranch_execz .LBB0_3043
	v_add_f32_e64 v98, |v94|, |v94|
	v_mul_f32_e32 v98, 0x3fb8aa3b, v98
	v_exp_f32_e32 v98, v98
	s_nop 0
	v_add_f32_e32 v98, 1.0, v98
	v_rcp_f32_e32 v98, v98
	s_nop 0
	v_fma_f32 v98, v98, -2.0, 1.0
	v_add_f32_e64 v99, |v95|, |v95|
	v_mul_f32_e32 v99, 0x3fb8aa3b, v99
	v_exp_f32_e32 v99, v99
	s_nop 0
	v_add_f32_e32 v99, 1.0, v99
	v_rcp_f32_e32 v99, v99
	s_nop 0
	v_fma_f32 v99, v99, -2.0, 1.0
	v_add_f32_e64 v101, |v90|, |v90|
	v_mul_f32_e32 v101, 0x3fb8aa3b, v101
	v_exp_f32_e32 v101, v101
	s_nop 0
	v_add_f32_e32 v101, 1.0, v101
	v_rcp_f32_e32 v101, v101
	s_nop 0
	v_fma_f32 v101, v101, -2.0, 1.0
	v_add_f32_e64 v102, |v91|, |v91|
	v_mul_f32_e32 v102, 0x3fb8aa3b, v102
	v_exp_f32_e32 v102, v102
	s_nop 0
	v_add_f32_e32 v102, 1.0, v102
	v_rcp_f32_e32 v102, v102
	s_nop 0
	v_fma_f32 v102, v102, -2.0, 1.0
	v_add_f32_e64 v103, |v96|, |v96|
	v_mul_f32_e32 v103, 0x3fb8aa3b, v103
	v_exp_f32_e32 v103, v103
	s_nop 0
	v_add_f32_e32 v103, 1.0, v103
	v_rcp_f32_e32 v103, v103
	s_nop 0
	v_fma_f32 v103, v103, -2.0, 1.0
	v_add_f32_e64 v104, |v97|, |v97|
	v_mul_f32_e32 v104, 0x3fb8aa3b, v104
	v_exp_f32_e32 v104, v104
	s_nop 0
	v_add_f32_e32 v104, 1.0, v104
	v_rcp_f32_e32 v104, v104
	s_nop 0
	v_fma_f32 v104, v104, -2.0, 1.0
	v_add_f32_e64 v105, |v92|, |v92|
	v_mul_f32_e32 v105, 0x3fb8aa3b, v105
	v_exp_f32_e32 v105, v105
	s_nop 0
	v_add_f32_e32 v105, 1.0, v105
	v_rcp_f32_e32 v105, v105
	s_nop 0
	v_fma_f32 v105, v105, -2.0, 1.0
	v_add_f32_e64 v106, |v93|, |v93|
	v_mul_f32_e32 v106, 0x3fb8aa3b, v106
	v_exp_f32_e32 v106, v106
	s_nop 0
	v_add_f32_e32 v106, 1.0, v106
	v_rcp_f32_e32 v106, v106
	s_nop 0
	v_fma_f32 v106, v106, -2.0, 1.0
	v_bfi_b32 v94, s91, v98, v94
	v_bfi_b32 v95, s91, v99, v95
	v_bfi_b32 v90, s91, v101, v90
	v_bfi_b32 v91, s91, v102, v91
	v_bfi_b32 v96, s91, v103, v96
	v_bfi_b32 v97, s91, v104, v97
	v_bfi_b32 v92, s91, v105, v92
	v_bfi_b32 v93, s91, v106, v93

.LBB0_3060:
	s_andn2_saveexec_b64 s[16:17], s[16:17]
	s_cbranch_execz .LBB0_3094
	v_add_f32_e64 v94, |v90|, |v90|
	v_mul_f32_e32 v94, 0x3fb8aa3b, v94
	v_exp_f32_e32 v94, v94
	s_nop 0
	v_add_f32_e32 v94, 1.0, v94
	v_rcp_f32_e32 v94, v94
	s_nop 0
	v_fma_f32 v94, v94, -2.0, 1.0
	v_add_f32_e64 v95, |v91|, |v91|
	v_mul_f32_e32 v95, 0x3fb8aa3b, v95
	v_exp_f32_e32 v95, v95
	s_nop 0
	v_add_f32_e32 v95, 1.0, v95
	v_rcp_f32_e32 v95, v95
	s_nop 0
	v_fma_f32 v95, v95, -2.0, 1.0
	v_add_f32_e64 v97, |v86|, |v86|
	v_mul_f32_e32 v97, 0x3fb8aa3b, v97
	v_exp_f32_e32 v97, v97
	s_nop 0
	v_add_f32_e32 v97, 1.0, v97
	v_rcp_f32_e32 v97, v97
	s_nop 0
	v_fma_f32 v97, v97, -2.0, 1.0
	v_add_f32_e64 v98, |v87|, |v87|
	v_mul_f32_e32 v98, 0x3fb8aa3b, v98
	v_exp_f32_e32 v98, v98
	s_nop 0
	v_add_f32_e32 v98, 1.0, v98
	v_rcp_f32_e32 v98, v98
	s_nop 0
	v_fma_f32 v98, v98, -2.0, 1.0
	v_add_f32_e64 v99, |v92|, |v92|
	v_mul_f32_e32 v99, 0x3fb8aa3b, v99
	v_exp_f32_e32 v99, v99
	s_nop 0
	v_add_f32_e32 v99, 1.0, v99
	v_rcp_f32_e32 v99, v99
	s_nop 0
	v_fma_f32 v99, v99, -2.0, 1.0
	v_add_f32_e64 v100, |v93|, |v93|
	v_mul_f32_e32 v100, 0x3fb8aa3b, v100
	v_exp_f32_e32 v100, v100
	s_nop 0
	v_add_f32_e32 v100, 1.0, v100
	v_rcp_f32_e32 v100, v100
	s_nop 0
	v_fma_f32 v100, v100, -2.0, 1.0
	v_add_f32_e64 v101, |v88|, |v88|
	v_mul_f32_e32 v101, 0x3fb8aa3b, v101
	v_exp_f32_e32 v101, v101
	s_nop 0
	v_add_f32_e32 v101, 1.0, v101
	v_rcp_f32_e32 v101, v101
	s_nop 0
	v_fma_f32 v101, v101, -2.0, 1.0
	v_add_f32_e64 v102, |v89|, |v89|
	v_mul_f32_e32 v102, 0x3fb8aa3b, v102
	v_exp_f32_e32 v102, v102
	s_nop 0
	v_add_f32_e32 v102, 1.0, v102
	v_rcp_f32_e32 v102, v102
	s_nop 0
	v_fma_f32 v102, v102, -2.0, 1.0
	v_bfi_b32 v90, s91, v94, v90
	v_bfi_b32 v91, s91, v95, v91
	v_bfi_b32 v86, s91, v97, v86
	v_bfi_b32 v87, s91, v98, v87
	v_bfi_b32 v92, s91, v99, v92
	v_bfi_b32 v93, s91, v100, v93
	v_bfi_b32 v88, s91, v101, v88
	v_bfi_b32 v89, s91, v102, v89

.LBB0_3112:
	s_waitcnt vmcnt(0)
	v_lshlrev_b32_e32 v26, 16, v14
	v_mul_f32_e32 v27, 0x3d372713, v26
	v_mul_f32_e32 v27, v27, v26
	v_fma_f32 v27, v27, v26, v26
	v_mul_f32_e32 v27, 0x3f4c422a, v27
	v_add_f32_e64 v28, |v27|, |v27|
	v_mul_f32_e32 v28, 0x3fb8aa3b, v28
	v_exp_f32_e32 v28, v28
	s_nop 0
	v_add_f32_e32 v28, 1.0, v28
	v_rcp_f32_e32 v28, v28
	s_nop 0
	v_fma_f32 v28, v28, -2.0, 1.0
	v_and_b32_e32 v14, 0xffff0000, v14
	v_mul_f32_e32 v29, 0x3d372713, v14
	v_mul_f32_e32 v29, v29, v14
	v_fma_f32 v29, v29, v14, v14
	v_mul_f32_e32 v29, 0x3f4c422a, v29
	v_add_f32_e64 v30, |v29|, |v29|
	v_mul_f32_e32 v30, 0x3fb8aa3b, v30
	v_exp_f32_e32 v30, v30
	s_nop 0
	v_add_f32_e32 v30, 1.0, v30
	v_rcp_f32_e32 v30, v30
	s_nop 0
	v_fma_f32 v30, v30, -2.0, 1.0
	v_lshlrev_b32_e32 v31, 16, v15
	v_mul_f32_e32 v32, 0x3d372713, v31
	v_mul_f32_e32 v32, v32, v31
	v_fma_f32 v32, v32, v31, v31
	v_mul_f32_e32 v32, 0x3f4c422a, v32
	v_add_f32_e64 v33, |v32|, |v32|
	v_mul_f32_e32 v33, 0x3fb8aa3b, v33
	v_exp_f32_e32 v33, v33
	s_nop 0
	v_add_f32_e32 v33, 1.0, v33
	v_rcp_f32_e32 v33, v33
	s_nop 0
	v_fma_f32 v33, v33, -2.0, 1.0
	v_and_b32_e32 v15, 0xffff0000, v15
	v_mul_f32_e32 v34, 0x3d372713, v15
	v_mul_f32_e32 v34, v34, v15
	v_fma_f32 v34, v34, v15, v15
	v_mul_f32_e32 v34, 0x3f4c422a, v34
	v_add_f32_e64 v35, |v34|, |v34|
	v_mul_f32_e32 v35, 0x3fb8aa3b, v35
	v_exp_f32_e32 v35, v35
	s_nop 0
	v_add_f32_e32 v35, 1.0, v35
	v_rcp_f32_e32 v35, v35
	s_nop 0
	v_fma_f32 v35, v35, -2.0, 1.0
	v_lshlrev_b32_e32 v36, 16, v16
	v_mul_f32_e32 v37, 0x3d372713, v36
	v_mul_f32_e32 v37, v37, v36
	v_fma_f32 v37, v37, v36, v36
	v_mul_f32_e32 v37, 0x3f4c422a, v37
	v_add_f32_e64 v38, |v37|, |v37|
	v_mul_f32_e32 v38, 0x3fb8aa3b, v38
	v_exp_f32_e32 v38, v38
	s_nop 0
	v_add_f32_e32 v38, 1.0, v38
	v_rcp_f32_e32 v38, v38
	s_nop 0
	v_fma_f32 v38, v38, -2.0, 1.0
	v_and_b32_e32 v16, 0xffff0000, v16
	v_mul_f32_e32 v39, 0x3d372713, v16
	v_mul_f32_e32 v39, v39, v16
	v_fma_f32 v39, v39, v16, v16
	v_mul_f32_e32 v39, 0x3f4c422a, v39
	v_add_f32_e64 v40, |v39|, |v39|
	v_mul_f32_e32 v40, 0x3fb8aa3b, v40
	v_exp_f32_e32 v40, v40
	s_nop 0
	v_add_f32_e32 v40, 1.0, v40
	v_rcp_f32_e32 v40, v40
	s_nop 0
	v_fma_f32 v40, v40, -2.0, 1.0
	v_lshlrev_b32_e32 v41, 16, v17
	v_mul_f32_e32 v42, 0x3d372713, v41
	v_mul_f32_e32 v42, v42, v41
	v_fma_f32 v42, v42, v41, v41
	v_mul_f32_e32 v42, 0x3f4c422a, v42
	v_add_f32_e64 v43, |v42|, |v42|
	v_mul_f32_e32 v43, 0x3fb8aa3b, v43
	v_exp_f32_e32 v43, v43
	s_nop 0
	v_add_f32_e32 v43, 1.0, v43
	v_rcp_f32_e32 v43, v43
	s_nop 0
	v_fma_f32 v43, v43, -2.0, 1.0
	v_and_b32_e32 v17, 0xffff0000, v17
	v_mul_f32_e32 v44, 0x3d372713, v17
	v_mul_f32_e32 v44, v44, v17
	v_fma_f32 v44, v44, v17, v17
	v_mul_f32_e32 v44, 0x3f4c422a, v44
	v_add_f32_e64 v45, |v44|, |v44|
	v_mul_f32_e32 v45, 0x3fb8aa3b, v45
	v_exp_f32_e32 v45, v45
	s_nop 0
	v_add_f32_e32 v45, 1.0, v45
	v_rcp_f32_e32 v45, v45
	s_nop 0
	v_fma_f32 v45, v45, -2.0, 1.0
	v_lshlrev_b32_e32 v46, 16, v10
	v_mul_f32_e32 v47, 0x3d372713, v46
	v_mul_f32_e32 v47, v47, v46
	v_fma_f32 v47, v47, v46, v46
	v_mul_f32_e32 v47, 0x3f4c422a, v47
	s_waitcnt lgkmcnt(0)
	v_add_f32_e64 v48, |v47|, |v47|
	v_mul_f32_e32 v48, 0x3fb8aa3b, v48
	v_exp_f32_e32 v48, v48
	s_nop 0
	v_add_f32_e32 v48, 1.0, v48
	v_rcp_f32_e32 v48, v48
	s_nop 0
	v_fma_f32 v48, v48, -2.0, 1.0
	v_and_b32_e32 v10, 0xffff0000, v10
	v_mul_f32_e32 v49, 0x3d372713, v10
	v_mul_f32_e32 v49, v49, v10
	v_fma_f32 v49, v49, v10, v10
	v_mul_f32_e32 v49, 0x3f4c422a, v49
	s_waitcnt lgkmcnt(0)
	s_waitcnt lgkmcnt(0)
	v_add_f32_e64 v55, |v49|, |v49|
	v_mul_f32_e32 v55, 0x3fb8aa3b, v55
	v_exp_f32_e32 v55, v55
	s_nop 0
	v_add_f32_e32 v55, 1.0, v55
	v_rcp_f32_e32 v55, v55
	s_nop 0
	v_fma_f32 v55, v55, -2.0, 1.0
	s_waitcnt lgkmcnt(0)
	v_lshlrev_b32_e32 v56, 16, v11
	v_mul_f32_e32 v57, 0x3d372713, v56
	v_mul_f32_e32 v57, v57, v56
	v_fma_f32 v57, v57, v56, v56
	v_mul_f32_e32 v57, 0x3f4c422a, v57
	v_add_f32_e64 v58, |v57|, |v57|
	v_mul_f32_e32 v58, 0x3fb8aa3b, v58
	v_exp_f32_e32 v58, v58
	s_nop 0
	v_add_f32_e32 v58, 1.0, v58
	v_rcp_f32_e32 v58, v58
	s_nop 0
	v_fma_f32 v58, v58, -2.0, 1.0
	v_and_b32_e32 v11, 0xffff0000, v11
	v_mul_f32_e32 v59, 0x3d372713, v11
	v_mul_f32_e32 v59, v59, v11
	v_fma_f32 v59, v59, v11, v11
	v_mul_f32_e32 v59, 0x3f4c422a, v59
	v_add_f32_e64 v60, |v59|, |v59|
	v_mul_f32_e32 v60, 0x3fb8aa3b, v60
	v_exp_f32_e32 v60, v60
	s_nop 0
	v_add_f32_e32 v60, 1.0, v60
	v_rcp_f32_e32 v60, v60
	s_nop 0
	v_fma_f32 v60, v60, -2.0, 1.0
	v_lshlrev_b32_e32 v61, 16, v12
	v_mul_f32_e32 v62, 0x3d372713, v61
	v_mul_f32_e32 v62, v62, v61
	v_fma_f32 v62, v62, v61, v61
	v_mul_f32_e32 v62, 0x3f4c422a, v62
	v_add_f32_e64 v63, |v62|, |v62|
	v_mul_f32_e32 v63, 0x3fb8aa3b, v63
	v_exp_f32_e32 v63, v63
	s_nop 0
	v_add_f32_e32 v63, 1.0, v63
	v_rcp_f32_e32 v63, v63
	s_nop 0
	v_fma_f32 v63, v63, -2.0, 1.0
	v_and_b32_e32 v12, 0xffff0000, v12
	v_mul_f32_e32 v64, 0x3d372713, v12
	v_mul_f32_e32 v64, v64, v12
	v_fma_f32 v64, v64, v12, v12
	v_mul_f32_e32 v64, 0x3f4c422a, v64
	v_add_f32_e64 v65, |v64|, |v64|
	v_mul_f32_e32 v65, 0x3fb8aa3b, v65
	v_exp_f32_e32 v65, v65
	s_nop 0
	v_add_f32_e32 v65, 1.0, v65
	v_rcp_f32_e32 v65, v65
	s_nop 0
	v_fma_f32 v65, v65, -2.0, 1.0
	v_lshlrev_b32_e32 v66, 16, v13
	v_mul_f32_e32 v67, 0x3d372713, v66
	v_mul_f32_e32 v67, v67, v66
	v_fma_f32 v67, v67, v66, v66
	v_mul_f32_e32 v67, 0x3f4c422a, v67
	v_add_f32_e64 v68, |v67|, |v67|
	v_mul_f32_e32 v68, 0x3fb8aa3b, v68
	v_exp_f32_e32 v68, v68
	s_nop 0
	v_add_f32_e32 v68, 1.0, v68
	v_rcp_f32_e32 v68, v68
	s_nop 0
	v_fma_f32 v68, v68, -2.0, 1.0
	v_and_b32_e32 v13, 0xffff0000, v13
	v_mul_f32_e32 v69, 0x3d372713, v13
	v_mul_f32_e32 v69, v69, v13
	v_fma_f32 v69, v69, v13, v13
	v_mul_f32_e32 v69, 0x3f4c422a, v69
	v_add_f32_e64 v70, |v69|, |v69|
	v_mul_f32_e32 v70, 0x3fb8aa3b, v70
	v_exp_f32_e32 v70, v70
	s_nop 0
	v_add_f32_e32 v70, 1.0, v70
	v_rcp_f32_e32 v70, v70
	s_nop 0
	v_fma_f32 v70, v70, -2.0, 1.0
	v_lshlrev_b32_e32 v71, 16, v6
	v_mul_f32_e32 v72, 0x3d372713, v71
	v_mul_f32_e32 v72, v72, v71
	v_fma_f32 v72, v72, v71, v71
	v_mul_f32_e32 v72, 0x3f4c422a, v72
	v_add_f32_e64 v73, |v72|, |v72|
	v_mul_f32_e32 v73, 0x3fb8aa3b, v73
	v_exp_f32_e32 v73, v73
	s_nop 0
	v_add_f32_e32 v73, 1.0, v73
	v_rcp_f32_e32 v73, v73
	s_nop 0
	v_fma_f32 v73, v73, -2.0, 1.0
	v_and_b32_e32 v74, 0xffff0000, v6
	v_mul_f32_e32 v6, 0x3d372713, v74
	v_mul_f32_e32 v6, v6, v74
	v_fma_f32 v6, v6, v74, v74
	v_mul_f32_e32 v75, 0x3f4c422a, v6
	v_add_f32_e64 v76, |v75|, |v75|
	v_mul_f32_e32 v76, 0x3fb8aa3b, v76
	v_exp_f32_e32 v76, v76
	s_nop 0
	v_add_f32_e32 v76, 1.0, v76
	v_rcp_f32_e32 v76, v76
	s_nop 0
	v_fma_f32 v76, v76, -2.0, 1.0
	v_lshlrev_b32_e32 v77, 16, v7
	v_mul_f32_e32 v6, 0x3d372713, v77
	v_mul_f32_e32 v6, v6, v77
	v_fma_f32 v6, v6, v77, v77
	v_mul_f32_e32 v78, 0x3f4c422a, v6
	v_add_f32_e64 v79, |v78|, |v78|
	v_mul_f32_e32 v79, 0x3fb8aa3b, v79
	v_exp_f32_e32 v79, v79
	s_nop 0
	v_add_f32_e32 v79, 1.0, v79
	v_rcp_f32_e32 v79, v79
	s_nop 0
	v_fma_f32 v79, v79, -2.0, 1.0
	v_and_b32_e32 v80, 0xffff0000, v7
	v_mul_f32_e32 v6, 0x3d372713, v80
	v_mul_f32_e32 v6, v6, v80
	v_fma_f32 v6, v6, v80, v80
	v_mul_f32_e32 v81, 0x3f4c422a, v6
	v_add_f32_e64 v82, |v81|, |v81|
	v_mul_f32_e32 v82, 0x3fb8aa3b, v82
	v_exp_f32_e32 v82, v82
	s_nop 0
	v_add_f32_e32 v82, 1.0, v82
	v_rcp_f32_e32 v82, v82
	s_nop 0
	v_fma_f32 v82, v82, -2.0, 1.0
	v_lshlrev_b32_e32 v83, 16, v8
	v_mul_f32_e32 v6, 0x3d372713, v83
	v_mul_f32_e32 v6, v6, v83
	v_fma_f32 v6, v6, v83, v83
	v_mul_f32_e32 v84, 0x3f4c422a, v6
	v_add_f32_e64 v85, |v84|, |v84|
	v_mul_f32_e32 v85, 0x3fb8aa3b, v85
	v_exp_f32_e32 v85, v85
	s_nop 0
	v_add_f32_e32 v85, 1.0, v85
	v_rcp_f32_e32 v85, v85
	s_nop 0
	v_fma_f32 v85, v85, -2.0, 1.0
	v_and_b32_e32 v8, 0xffff0000, v8
	v_mul_f32_e32 v6, 0x3d372713, v8
	v_mul_f32_e32 v6, v6, v8
	v_fma_f32 v6, v6, v8, v8
	v_mul_f32_e32 v86, 0x3f4c422a, v6
	v_add_f32_e64 v87, |v86|, |v86|
	v_mul_f32_e32 v87, 0x3fb8aa3b, v87
	v_exp_f32_e32 v87, v87
	s_nop 0
	v_add_f32_e32 v87, 1.0, v87
	v_rcp_f32_e32 v87, v87
	s_nop 0
	v_fma_f32 v87, v87, -2.0, 1.0
	v_lshlrev_b32_e32 v88, 16, v9
	v_mul_f32_e32 v6, 0x3d372713, v88
	v_mul_f32_e32 v6, v6, v88
	v_fma_f32 v6, v6, v88, v88
	v_mul_f32_e32 v89, 0x3f4c422a, v6
	v_add_f32_e64 v90, |v89|, |v89|
	v_mul_f32_e32 v90, 0x3fb8aa3b, v90
	v_exp_f32_e32 v90, v90
	s_nop 0
	v_add_f32_e32 v90, 1.0, v90
	v_rcp_f32_e32 v90, v90
	s_nop 0
	v_fma_f32 v90, v90, -2.0, 1.0
	v_and_b32_e32 v9, 0xffff0000, v9
	v_mul_f32_e32 v6, 0x3d372713, v9
	v_mul_f32_e32 v6, v6, v9
	v_fma_f32 v6, v6, v9, v9
	v_mul_f32_e32 v91, 0x3f4c422a, v6
	v_add_f32_e64 v92, |v91|, |v91|
	v_mul_f32_e32 v92, 0x3fb8aa3b, v92
	v_exp_f32_e32 v92, v92
	s_nop 0
	v_add_f32_e32 v92, 1.0, v92
	v_rcp_f32_e32 v92, v92
	s_nop 0
	v_fma_f32 v92, v92, -2.0, 1.0
	v_lshlrev_b32_e32 v6, 16, v2
	v_mul_f32_e32 v7, 0x3d372713, v6
	v_mul_f32_e32 v7, v7, v6
	v_fma_f32 v7, v7, v6, v6
	v_mul_f32_e32 v7, 0x3f4c422a, v7
	v_add_f32_e64 v93, |v7|, |v7|
	v_mul_f32_e32 v93, 0x3fb8aa3b, v93
	v_exp_f32_e32 v93, v93
	s_nop 0
	v_add_f32_e32 v93, 1.0, v93
	v_rcp_f32_e32 v93, v93
	s_nop 0
	v_fma_f32 v93, v93, -2.0, 1.0
	v_and_b32_e32 v94, 0xffff0000, v2
	v_mul_f32_e32 v2, 0x3d372713, v94
	v_mul_f32_e32 v2, v2, v94
	v_fma_f32 v2, v2, v94, v94
	v_mul_f32_e32 v95, 0x3f4c422a, v2
	v_add_f32_e64 v96, |v95|, |v95|
	v_mul_f32_e32 v96, 0x3fb8aa3b, v96
	v_exp_f32_e32 v96, v96
	s_nop 0
	v_add_f32_e32 v96, 1.0, v96
	v_rcp_f32_e32 v96, v96
	s_nop 0
	v_fma_f32 v96, v96, -2.0, 1.0
	v_lshlrev_b32_e32 v97, 16, v3
	v_mul_f32_e32 v2, 0x3d372713, v97
	v_mul_f32_e32 v2, v2, v97
	v_fma_f32 v2, v2, v97, v97
	v_mul_f32_e32 v98, 0x3f4c422a, v2
	v_add_f32_e64 v99, |v98|, |v98|
	v_mul_f32_e32 v99, 0x3fb8aa3b, v99
	v_exp_f32_e32 v99, v99
	s_nop 0
	v_add_f32_e32 v99, 1.0, v99
	v_rcp_f32_e32 v99, v99
	s_nop 0
	v_fma_f32 v99, v99, -2.0, 1.0
	v_and_b32_e32 v100, 0xffff0000, v3
	v_mul_f32_e32 v2, 0x3d372713, v100
	v_mul_f32_e32 v2, v2, v100
	v_fma_f32 v2, v2, v100, v100
	v_mul_f32_e32 v101, 0x3f4c422a, v2
	v_add_f32_e64 v102, |v101|, |v101|
	v_mul_f32_e32 v102, 0x3fb8aa3b, v102
	v_exp_f32_e32 v102, v102
	s_nop 0
	v_add_f32_e32 v102, 1.0, v102
	v_rcp_f32_e32 v102, v102
	s_nop 0
	v_fma_f32 v102, v102, -2.0, 1.0
	v_lshlrev_b32_e32 v103, 16, v4
	v_mul_f32_e32 v2, 0x3d372713, v103
	v_mul_f32_e32 v2, v2, v103
	v_fma_f32 v2, v2, v103, v103
	v_mul_f32_e32 v104, 0x3f4c422a, v2
	v_add_f32_e64 v107, |v104|, |v104|
	v_mul_f32_e32 v107, 0x3fb8aa3b, v107
	v_exp_f32_e32 v107, v107
	s_nop 0
	v_add_f32_e32 v107, 1.0, v107
	v_rcp_f32_e32 v107, v107
	s_nop 0
	v_fma_f32 v107, v107, -2.0, 1.0
	v_and_b32_e32 v109, 0xffff0000, v4
	v_mul_f32_e32 v2, 0x3d372713, v109
	v_mul_f32_e32 v2, v2, v109
	v_fma_f32 v2, v2, v109, v109
	v_mul_f32_e32 v110, 0x3f4c422a, v2
	v_add_f32_e64 v111, |v110|, |v110|
	v_mul_f32_e32 v111, 0x3fb8aa3b, v111
	v_exp_f32_e32 v111, v111
	s_nop 0
	v_add_f32_e32 v111, 1.0, v111
	v_rcp_f32_e32 v111, v111
	s_nop 0
	v_fma_f32 v111, v111, -2.0, 1.0
	v_lshlrev_b32_e32 v112, 16, v5
	v_mul_f32_e32 v2, 0x3d372713, v112
	v_mul_f32_e32 v2, v2, v112
	v_fma_f32 v2, v2, v112, v112
	v_mul_f32_e32 v113, 0x3f4c422a, v2
	v_add_f32_e64 v114, |v113|, |v113|
	v_mul_f32_e32 v114, 0x3fb8aa3b, v114
	v_exp_f32_e32 v114, v114
	s_nop 0
	v_add_f32_e32 v114, 1.0, v114
	v_rcp_f32_e32 v114, v114
	s_nop 0
	v_fma_f32 v114, v114, -2.0, 1.0
	v_and_b32_e32 v105, 0xffff0000, v5
	v_mul_f32_e32 v2, 0x3d372713, v105
	v_mul_f32_e32 v2, v2, v105
	v_fma_f32 v2, v2, v105, v105
	v_mul_f32_e32 v106, 0x3f4c422a, v2
	v_add_f32_e64 v108, |v106|, |v106|
	v_mul_f32_e32 v108, 0x3fb8aa3b, v108
	v_exp_f32_e32 v108, v108
	s_nop 0
	v_add_f32_e32 v108, 1.0, v108
	v_rcp_f32_e32 v108, v108
	s_nop 0
	v_fma_f32 v108, v108, -2.0, 1.0
	v_bfi_b32 v72, s15, v73, v72
	v_mul_f32_e32 v71, 0.5, v71
	v_add_f32_e32 v73, 1.0, v72
	v_mul_f32_e32 v72, v71, v73
	v_fma_f32 v71, v71, v73, 0
	v_bfi_b32 v73, s15, v76, v75
	v_mul_f32_e32 v74, 0.5, v74
	v_add_f32_e32 v75, 1.0, v73
	v_mul_f32_e32 v73, v74, v75
	v_fmac_f32_e32 v71, v74, v75
	v_bfi_b32 v74, s15, v79, v78
	v_mul_f32_e32 v75, 0.5, v77
	v_add_f32_e32 v76, 1.0, v74
	v_mul_f32_e32 v74, v75, v76
	v_fmac_f32_e32 v71, v75, v76
	v_bfi_b32 v75, s15, v82, v81
	v_mul_f32_e32 v76, 0.5, v80
	v_add_f32_e32 v77, 1.0, v75
	v_mul_f32_e32 v75, v76, v77
	v_fmac_f32_e32 v71, v76, v77
	v_bfi_b32 v76, s15, v85, v84
	v_mul_f32_e32 v77, 0.5, v83
	v_add_f32_e32 v78, 1.0, v76
	v_mul_f32_e32 v76, v77, v78
	v_fmac_f32_e32 v71, v77, v78
	v_bfi_b32 v77, s15, v87, v86
	v_mul_f32_e32 v8, 0.5, v8
	v_add_f32_e32 v78, 1.0, v77
	v_mul_f32_e32 v77, v8, v78
	v_fmac_f32_e32 v71, v8, v78
	v_bfi_b32 v8, s15, v90, v89
	v_mul_f32_e32 v78, 0.5, v88
	v_add_f32_e32 v79, 1.0, v8
	v_mul_f32_e32 v8, v78, v79
	v_fmac_f32_e32 v71, v78, v79
	v_mul_f32_e32 v78, 0.5, v9
	v_bfi_b32 v9, s15, v92, v91
	v_add_f32_e32 v79, 1.0, v9
	v_mul_f32_e32 v9, v78, v79
	v_fmac_f32_e32 v71, v78, v79
	v_mul_f32_e32 v78, 0.5, v46
	v_bfi_b32 v46, s15, v48, v47
	v_add_f32_e32 v47, 1.0, v46
	v_mul_f32_e32 v46, v78, v47
	v_fma_f32 v78, v78, v47, 0
	v_bfi_b32 v47, s15, v55, v49
	v_mul_f32_e32 v10, 0.5, v10
	v_add_f32_e32 v48, 1.0, v47
	v_mul_f32_e32 v47, v10, v48
	v_fmac_f32_e32 v78, v10, v48
	v_bfi_b32 v10, s15, v58, v57
	v_mul_f32_e32 v48, 0.5, v56
	v_add_f32_e32 v49, 1.0, v10
	v_mul_f32_e32 v10, v48, v49
	v_fmac_f32_e32 v78, v48, v49
	v_mul_f32_e32 v48, 0.5, v11
	v_bfi_b32 v11, s15, v60, v59
	v_add_f32_e32 v49, 1.0, v11
	v_mul_f32_e32 v11, v48, v49
	v_fmac_f32_e32 v78, v48, v49
	v_bfi_b32 v48, s15, v63, v62
	v_mul_f32_e32 v49, 0.5, v61
	v_add_f32_e32 v55, 1.0, v48
	v_mul_f32_e32 v48, v49, v55
	v_fmac_f32_e32 v78, v49, v55
	v_bfi_b32 v49, s15, v65, v64
	v_mul_f32_e32 v12, 0.5, v12
	v_add_f32_e32 v55, 1.0, v49
	v_mul_f32_e32 v49, v12, v55
	v_fmac_f32_e32 v78, v12, v55
	v_bfi_b32 v12, s15, v68, v67
	v_mul_f32_e32 v55, 0.5, v66
	v_add_f32_e32 v56, 1.0, v12
	v_mul_f32_e32 v12, v55, v56
	v_fmac_f32_e32 v78, v55, v56
	v_mul_f32_e32 v55, 0.5, v13
	v_bfi_b32 v13, s15, v70, v69
	v_bfi_b32 v27, s15, v28, v27
	v_add_f32_e32 v56, 1.0, v13
	v_mul_f32_e32 v26, 0.5, v26
	v_add_f32_e32 v27, 1.0, v27
	v_bfi_b32 v2, s15, v93, v7
	v_mul_f32_e32 v13, v55, v56
	v_fmac_f32_e32 v78, v55, v56
	v_mul_f32_e32 v56, v26, v27
	v_fma_f32 v26, v26, v27, 0
	v_bfi_b32 v27, s15, v30, v29
	v_mul_f32_e32 v3, 0.5, v6
	v_add_f32_e32 v4, 1.0, v2
	v_mul_f32_e32 v14, 0.5, v14
	v_add_f32_e32 v27, 1.0, v27
	v_mul_f32_e32 v2, v3, v4
	v_fma_f32 v93, v3, v4, 0
	v_bfi_b32 v3, s15, v96, v95
	v_mul_f32_e32 v57, v14, v27
	v_fmac_f32_e32 v26, v14, v27
	v_bfi_b32 v27, s15, v33, v32
	v_mul_f32_e32 v4, 0.5, v94
	v_add_f32_e32 v5, 1.0, v3
	v_mul_f32_e32 v14, 0.5, v31
	v_add_f32_e32 v27, 1.0, v27
	v_mul_f32_e32 v3, v4, v5
	v_fmac_f32_e32 v93, v4, v5
	v_bfi_b32 v4, s15, v99, v98
	v_mul_f32_e32 v58, v14, v27
	v_fmac_f32_e32 v26, v14, v27
	v_mul_f32_e32 v14, 0.5, v15
	v_bfi_b32 v15, s15, v35, v34
	v_mul_f32_e32 v5, 0.5, v97
	v_add_f32_e32 v6, 1.0, v4
	v_add_f32_e32 v15, 1.0, v15
	v_mul_f32_e32 v4, v5, v6
	v_fmac_f32_e32 v93, v5, v6
	v_bfi_b32 v5, s15, v102, v101
	v_mul_f32_e32 v59, v14, v15
	v_fmac_f32_e32 v26, v14, v15
	v_bfi_b32 v15, s15, v38, v37
	v_mul_f32_e32 v6, 0.5, v100
	v_add_f32_e32 v7, 1.0, v5
	v_mul_f32_e32 v14, 0.5, v36
	v_add_f32_e32 v15, 1.0, v15
	v_mul_f32_e32 v5, v6, v7
	v_fmac_f32_e32 v93, v6, v7
	v_bfi_b32 v6, s15, v107, v104
	v_mul_f32_e32 v60, v14, v15
	v_fmac_f32_e32 v26, v14, v15
	v_bfi_b32 v15, s15, v40, v39
	v_mul_f32_e32 v7, 0.5, v103
	v_add_f32_e32 v94, 1.0, v6
	v_mul_f32_e32 v14, 0.5, v16
	v_add_f32_e32 v15, 1.0, v15
	v_mul_f32_e32 v6, v7, v94
	v_fmac_f32_e32 v93, v7, v94
	v_bfi_b32 v7, s15, v111, v110
	v_mul_f32_e32 v61, v14, v15
	v_fmac_f32_e32 v26, v14, v15
	v_bfi_b32 v15, s15, v43, v42
	v_mul_f32_e32 v94, 0.5, v109
	v_add_f32_e32 v95, 1.0, v7
	v_mul_f32_e32 v14, 0.5, v41
	v_add_f32_e32 v15, 1.0, v15
	v_mul_f32_e32 v7, v94, v95
	v_fmac_f32_e32 v93, v94, v95
	v_bfi_b32 v94, s15, v114, v113
	v_mul_f32_e32 v62, v14, v15
	v_fmac_f32_e32 v26, v14, v15
	v_bfi_b32 v15, s15, v45, v44
	v_mul_f32_e32 v95, 0.5, v112
	v_add_f32_e32 v96, 1.0, v94
	v_mul_f32_e32 v14, 0.5, v17
	v_add_f32_e32 v15, 1.0, v15
	v_bfi_b32 v17, s15, v108, v106
	v_fmac_f32_e32 v93, v95, v96
	v_fmac_f32_e32 v26, v14, v15
	v_mul_f32_e32 v16, 0.5, v105
	v_add_f32_e32 v17, 1.0, v17
	v_fmac_f32_e32 v93, v16, v17
	v_add_f32_dpp v26, v26, v26 quad_perm:[1,0,3,2] row_mask:0xf bank_mask:0xf bound_ctrl:1
	v_add_f32_dpp v27, v78, v78 quad_perm:[1,0,3,2] row_mask:0xf bank_mask:0xf bound_ctrl:1
	v_add_f32_dpp v28, v71, v71 quad_perm:[1,0,3,2] row_mask:0xf bank_mask:0xf bound_ctrl:1
	v_add_f32_dpp v26, v26, v26 quad_perm:[2,3,0,1] row_mask:0xf bank_mask:0xf bound_ctrl:1
	v_add_f32_dpp v27, v27, v27 quad_perm:[2,3,0,1] row_mask:0xf bank_mask:0xf bound_ctrl:1
	v_add_f32_dpp v29, v93, v93 quad_perm:[1,0,3,2] row_mask:0xf bank_mask:0xf bound_ctrl:1
	v_add_f32_dpp v26, v26, v26 row_ror:4 row_mask:0xf bank_mask:0xf bound_ctrl:1
	v_add_f32_dpp v27, v27, v27 row_ror:4 row_mask:0xf bank_mask:0xf bound_ctrl:1
	v_add_f32_dpp v28, v28, v28 quad_perm:[2,3,0,1] row_mask:0xf bank_mask:0xf bound_ctrl:1
	v_add_f32_dpp v29, v29, v29 quad_perm:[2,3,0,1] row_mask:0xf bank_mask:0xf bound_ctrl:1
	v_add_f32_dpp v26, v26, v26 row_ror:8 row_mask:0xf bank_mask:0xf bound_ctrl:1
	v_add_f32_dpp v27, v27, v27 row_ror:8 row_mask:0xf bank_mask:0xf bound_ctrl:1
	v_add_f32_dpp v28, v28, v28 row_ror:4 row_mask:0xf bank_mask:0xf bound_ctrl:1
	v_add_f32_dpp v29, v29, v29 row_ror:4 row_mask:0xf bank_mask:0xf bound_ctrl:1
	ds_bpermute_b32 v30, v1, v26
	v_add_f32_dpp v28, v28, v28 row_ror:8 row_mask:0xf bank_mask:0xf bound_ctrl:1
	v_add_f32_dpp v29, v29, v29 row_ror:8 row_mask:0xf bank_mask:0xf bound_ctrl:1
	ds_bpermute_b32 v31, v1, v27
	ds_bpermute_b32 v32, v1, v28
	ds_bpermute_b32 v33, v1, v29
	v_mul_f32_e32 v63, v14, v15
	s_waitcnt lgkmcnt(3)
	v_add_f32_e32 v14, v26, v30
	s_waitcnt lgkmcnt(2)
	v_add_f32_e32 v15, v27, v31
	s_waitcnt lgkmcnt(1)
	v_add_f32_e32 v26, v28, v32
	s_waitcnt lgkmcnt(0)
	v_add_f32_e32 v27, v29, v33
	ds_bpermute_b32 v28, v50, v14
	ds_bpermute_b32 v29, v50, v15
	ds_bpermute_b32 v30, v50, v26
	ds_bpermute_b32 v31, v50, v27
	v_mul_f32_e32 v94, v95, v96
	s_waitcnt lgkmcnt(3)
	v_add_f32_e32 v14, v14, v28
	s_waitcnt lgkmcnt(2)
	v_add_f32_e32 v15, v15, v29
	v_mul_f32_e32 v64, 0x3b000000, v14
	v_mul_f32_e32 v14, 0x3b000000, v15
	v_pk_add_f32 v[42:43], v[46:47], v[14:15] op_sel_hi:[1,0] neg_lo:[0,1] neg_hi:[0,1]
	v_mul_f32_e32 v95, v16, v17
	v_pk_mul_f32 v[16:17], v[42:43], v[42:43]
	v_pk_add_f32 v[44:45], v[10:11], v[14:15] op_sel_hi:[1,0] neg_lo:[0,1] neg_hi:[0,1]
	v_pk_add_f32 v[46:47], v[48:49], v[14:15] op_sel_hi:[1,0] neg_lo:[0,1] neg_hi:[0,1]
	v_pk_mul_f32 v[10:11], v[44:45], v[44:45]
	v_pk_add_f32 v[48:49], v[12:13], v[14:15] op_sel_hi:[1,0] neg_lo:[0,1] neg_hi:[0,1]
	v_add_f32_e32 v14, v16, v17
	v_add_f32_e32 v10, v10, v14
	s_waitcnt lgkmcnt(1)
	v_add_f32_e32 v28, v26, v30
	s_waitcnt lgkmcnt(0)
	v_add_f32_e32 v29, v27, v31
	v_pk_mul_f32 v[26:27], v[46:47], v[46:47]
	v_add_f32_e32 v10, v11, v10
	v_add_f32_e32 v10, v26, v10
	v_pk_mul_f32 v[12:13], v[48:49], v[48:49]
	v_add_f32_e32 v10, v27, v10
	v_add_f32_e32 v10, v12, v10
	v_add_f32_e32 v55, v13, v10
	v_mul_f32_e32 v10, 0x3b000000, v28
	v_pk_add_f32 v[34:35], v[72:73], v[10:11] op_sel_hi:[1,0] neg_lo:[0,1] neg_hi:[0,1]
	v_pk_add_f32 v[36:37], v[74:75], v[10:11] op_sel_hi:[1,0] neg_lo:[0,1] neg_hi:[0,1]
	v_pk_mul_f32 v[12:13], v[34:35], v[34:35]
	v_pk_mul_f32 v[14:15], v[36:37], v[36:37]
	v_pk_add_f32 v[38:39], v[76:77], v[10:11] op_sel_hi:[1,0] neg_lo:[0,1] neg_hi:[0,1]
	v_pk_add_f32 v[40:41], v[8:9], v[10:11] op_sel_hi:[1,0] neg_lo:[0,1] neg_hi:[0,1]
	v_add_f32_e32 v10, v12, v13
	v_add_f32_e32 v10, v14, v10
	v_pk_mul_f32 v[16:17], v[38:39], v[38:39]
	v_add_f32_e32 v10, v15, v10
	v_add_f32_e32 v10, v16, v10
	v_pk_mul_f32 v[8:9], v[40:41], v[40:41]
	v_add_f32_e32 v10, v17, v10
	v_add_f32_e32 v8, v8, v10
	v_add_f32_e32 v65, v9, v8
	v_mul_f32_e32 v8, 0x3b000000, v29
	v_pk_add_f32 v[26:27], v[2:3], v[8:9] op_sel_hi:[1,0] neg_lo:[0,1] neg_hi:[0,1]
	v_pk_add_f32 v[28:29], v[4:5], v[8:9] op_sel_hi:[1,0] neg_lo:[0,1] neg_hi:[0,1]
	v_pk_mul_f32 v[2:3], v[26:27], v[26:27]
	v_pk_mul_f32 v[4:5], v[28:29], v[28:29]
	v_add_f32_e32 v2, v2, v3
	v_pk_add_f32 v[30:31], v[6:7], v[8:9] op_sel_hi:[1,0] neg_lo:[0,1] neg_hi:[0,1]
	v_add_f32_e32 v2, v4, v2
	v_pk_mul_f32 v[66:67], v[30:31], v[30:31]
	v_add_f32_e32 v2, v5, v2
	v_pk_add_f32 v[32:33], v[94:95], v[8:9] op_sel_hi:[1,0] neg_lo:[0,1] neg_hi:[0,1]
	v_add_f32_e32 v66, v66, v2
	global_load_dwordx4 v[2:5], v[20:21], off
	global_load_dwordx4 v[10:13], v[20:21], off offset:16
	global_load_dwordx4 v[6:9], v[22:23], off
	global_load_dwordx4 v[14:17], v[22:23], off offset:16
	v_pk_mul_f32 v[68:69], v[32:33], v[32:33]
	v_add_f32_e32 v66, v67, v66
	v_add_f32_dpp v65, v65, v65 quad_perm:[1,0,3,2] row_mask:0xf bank_mask:0xf bound_ctrl:1
	v_add_f32_e32 v66, v68, v66
	v_add_f32_e32 v72, v69, v66
	v_add_f32_dpp v65, v65, v65 quad_perm:[2,3,0,1] row_mask:0xf bank_mask:0xf bound_ctrl:1
	v_pk_add_f32 v[66:67], v[56:57], v[64:65] op_sel_hi:[1,0] neg_lo:[0,1] neg_hi:[0,1]
	v_pk_add_f32 v[68:69], v[58:59], v[64:65] op_sel_hi:[1,0] neg_lo:[0,1] neg_hi:[0,1]
	v_pk_mul_f32 v[56:57], v[66:67], v[66:67]
	v_pk_mul_f32 v[58:59], v[68:69], v[68:69]
	v_add_f32_e32 v56, v56, v57
	v_pk_add_f32 v[70:71], v[60:61], v[64:65] op_sel_hi:[1,0] neg_lo:[0,1] neg_hi:[0,1]
	v_add_f32_e32 v56, v58, v56
	v_pk_mul_f32 v[60:61], v[70:71], v[70:71]
	v_add_f32_e32 v56, v59, v56
	v_pk_add_f32 v[62:63], v[62:63], v[64:65] op_sel_hi:[1,0] neg_lo:[0,1] neg_hi:[0,1]
	v_add_f32_e32 v56, v60, v56
	v_add_f32_dpp v73, v65, v65 row_ror:4 row_mask:0xf bank_mask:0xf bound_ctrl:1
	v_pk_mul_f32 v[64:65], v[62:63], v[62:63]
	v_add_f32_e32 v56, v61, v56
	v_add_f32_e32 v56, v64, v56
	v_add_f32_e32 v56, v65, v56
	v_add_f32_dpp v55, v55, v55 quad_perm:[1,0,3,2] row_mask:0xf bank_mask:0xf bound_ctrl:1
	v_add_f32_dpp v59, v72, v72 quad_perm:[1,0,3,2] row_mask:0xf bank_mask:0xf bound_ctrl:1
	v_add_f32_dpp v56, v56, v56 quad_perm:[1,0,3,2] row_mask:0xf bank_mask:0xf bound_ctrl:1
	v_add_f32_dpp v55, v55, v55 quad_perm:[2,3,0,1] row_mask:0xf bank_mask:0xf bound_ctrl:1
	v_add_f32_dpp v59, v59, v59 quad_perm:[2,3,0,1] row_mask:0xf bank_mask:0xf bound_ctrl:1
	v_add_f32_dpp v56, v56, v56 quad_perm:[2,3,0,1] row_mask:0xf bank_mask:0xf bound_ctrl:1
	v_add_f32_dpp v55, v55, v55 row_ror:4 row_mask:0xf bank_mask:0xf bound_ctrl:1
	v_add_f32_dpp v58, v73, v73 row_ror:8 row_mask:0xf bank_mask:0xf bound_ctrl:1
	v_add_f32_dpp v56, v56, v56 row_ror:4 row_mask:0xf bank_mask:0xf bound_ctrl:1
	v_add_f32_dpp v59, v59, v59 row_ror:4 row_mask:0xf bank_mask:0xf bound_ctrl:1
	v_add_f32_dpp v55, v55, v55 row_ror:8 row_mask:0xf bank_mask:0xf bound_ctrl:1
	v_add_f32_dpp v56, v56, v56 row_ror:8 row_mask:0xf bank_mask:0xf bound_ctrl:1
	ds_bpermute_b32 v57, v1, v56
	v_add_f32_dpp v60, v59, v59 row_ror:8 row_mask:0xf bank_mask:0xf bound_ctrl:1
	ds_bpermute_b32 v61, v1, v58
	ds_bpermute_b32 v59, v1, v55
	ds_bpermute_b32 v64, v1, v60
	s_waitcnt lgkmcnt(3)
	v_add_f32_e32 v56, v56, v57
	ds_bpermute_b32 v57, v50, v56
	s_mov_b64 s[0:1], 0x2380
	s_waitcnt lgkmcnt(2)
	v_add_f32_e32 v59, v55, v59
	s_waitcnt lgkmcnt(1)
	v_add_f32_e32 v55, v60, v64
	v_lshl_add_u64 v[24:25], v[24:25], 0, s[0:1]
	s_waitcnt lgkmcnt(0)
	v_add_f32_e32 v56, v56, v57
	v_fmamk_f32 v56, v56, 0x3b000000, v52
	v_mul_f32_e32 v57, 0x4f800000, v56
	v_cmp_gt_f32_e32 vcc, s16, v56
	s_nop 1
	v_cndmask_b32_e32 v56, v56, v57, vcc
	v_sqrt_f32_e32 v65, v56
	v_add_f32_e32 v57, v58, v61
	v_add_u32_e32 v58, -1, v65
	v_fma_f32 v60, -v58, v65, v56
	v_cmp_ge_f32_e64 s[0:1], 0, v60
	v_add_u32_e32 v60, 1, v65
	v_fma_f32 v61, -v60, v65, v56
	v_cndmask_b32_e64 v58, v65, v58, s[0:1]
	v_cmp_lt_f32_e64 s[0:1], 0, v61
	s_nop 1
	v_cndmask_b32_e64 v58, v58, v60, s[0:1]
	v_mul_f32_e32 v60, 0x37800000, v58
	v_cndmask_b32_e32 v58, v58, v60, vcc
	v_cmp_class_f32_e32 vcc, v56, v53
	ds_bpermute_b32 v60, v50, v59
	s_nop 0
	v_cndmask_b32_e32 v61, v58, v56, vcc
	v_div_scale_f32 v64, s[0:1], v61, v61, 1.0
	v_rcp_f32_e32 v65, v64
	ds_bpermute_b32 v58, v50, v57
	ds_bpermute_b32 v56, v50, v55
	v_fma_f32 v72, -v64, v65, 1.0
	v_fmac_f32_e32 v65, v72, v65
	v_div_scale_f32 v72, vcc, 1.0, v61, 1.0
	v_mul_f32_e32 v73, v72, v65
	v_fma_f32 v74, -v64, v73, v72
	v_fmac_f32_e32 v73, v74, v65
	v_fma_f32 v64, -v64, v73, v72
	v_div_fmas_f32 v64, v64, v65, v73
	v_div_fixup_f32 v64, v64, v61, 1.0
	v_pk_mul_f32 v[62:63], v[62:63], v[64:65] op_sel_hi:[1,0]
	s_andn2_b64 vcc, exec, s[12:13]
	s_waitcnt vmcnt(0)
	v_pk_fma_f32 v[72:73], v[12:13], v[62:63], v[16:17]
	v_pk_mul_f32 v[62:63], v[70:71], v[64:65] op_sel_hi:[1,0]
	s_nop 0
	v_pk_fma_f32 v[70:71], v[10:11], v[62:63], v[14:15]
	v_pk_mul_f32 v[62:63], v[68:69], v[64:65] op_sel_hi:[1,0]
	s_nop 0
	v_pk_fma_f32 v[68:69], v[4:5], v[62:63], v[8:9]
	v_pk_mul_f32 v[62:63], v[66:67], v[64:65] op_sel_hi:[1,0]
	v_cvt_pk_bf16_f32 v64, v70, v71
	v_pk_fma_f32 v[62:63], v[2:3], v[62:63], v[6:7]
	v_cvt_pk_bf16_f32 v65, v72, v73
	v_cvt_pk_bf16_f32 v62, v62, v63
	v_cvt_pk_bf16_f32 v63, v68, v69
	global_store_dwordx4 v[24:25], v[62:65], off
	s_cbranch_vccz .LBB0_3243
	s_andn2_b64 vcc, exec, s[6:7]
	s_cbranch_vccz .LBB0_3244

.LBB0_3324:
	ds_read_b64_tr_b16 v[82:83], v154
	ds_read_b64_tr_b16 v[86:87], v154 offset:32
	ds_read_b64_tr_b16 v[84:85], v145 offset:576
	ds_read_b64_tr_b16 v[88:89], v145 offset:608
	ds_read_b64_tr_b16 v[90:91], v154 offset:64
	ds_read_b64_tr_b16 v[92:93], v145 offset:640
	ds_read_b64_tr_b16 v[94:95], v154 offset:96
	ds_read_b64_tr_b16 v[96:97], v145 offset:672
	ds_read_b128 v[98:101], v155 offset:18432
	ds_read_b128 v[134:137], v155 offset:22784
	s_add_i32 s2, s8, s18
	s_ashr_i32 s3, s2, 31
	s_lshr_b32 s3, s3, 25
	s_waitcnt lgkmcnt(1)
	v_mfma_f32_16x16x32_bf16 v[102:105], v[82:85], v[98:101], 0
	s_add_i32 s3, s2, s3
	s_and_b32 s20, s3, 0xffffff80
	s_sub_i32 s2, s2, s20
	v_mfma_f32_16x16x32_bf16 v[106:109], v[86:89], v[98:101], 0
	s_ashr_i32 s21, s3, 7
	s_ashr_i32 s3, s2, 31
	s_lshl_b64 s[18:19], s[2:3], 7
	v_mfma_f32_16x16x32_bf16 v[110:113], v[90:93], v[98:101], 0
	s_lshl_b32 s22, s21, 6
	s_ashr_i32 s23, s22, 31
	v_mfma_f32_16x16x32_bf16 v[98:101], v[94:97], v[98:101], 0
	s_waitcnt lgkmcnt(0)
	v_mfma_f32_16x16x32_bf16 v[82:85], v[82:85], v[134:137], 0
	v_mfma_f32_16x16x32_bf16 v[86:89], v[86:89], v[134:137], 0
	v_mfma_f32_16x16x32_bf16 v[90:93], v[90:93], v[134:137], 0
	v_mfma_f32_16x16x32_bf16 v[94:97], v[94:97], v[134:137], 0
	ds_read_b64_tr_b16 v[134:135], v154 offset:4608
	ds_read_b64_tr_b16 v[136:137], v145 offset:5184
	ds_read_b64_tr_b16 v[138:139], v154 offset:4640
	ds_read_b64_tr_b16 v[140:141], v145 offset:5216
	ds_read_b64_tr_b16 v[160:161], v154 offset:4672
	ds_read_b64_tr_b16 v[162:163], v145 offset:5248
	ds_read_b64_tr_b16 v[164:165], v154 offset:4704
	ds_read_b64_tr_b16 v[166:167], v145 offset:5280
	ds_read_b128 v[168:171], v155 offset:18496
	s_waitcnt lgkmcnt(0)
	v_mfma_f32_16x16x32_bf16 v[102:105], v[134:137], v[168:171], v[102:105]
	v_mfma_f32_16x16x32_bf16 v[106:109], v[138:141], v[168:171], v[106:109]
	v_mfma_f32_16x16x32_bf16 v[110:113], v[160:163], v[168:171], v[110:113]
	v_mfma_f32_16x16x32_bf16 v[98:101], v[164:167], v[168:171], v[98:101]
	ds_read_b128 v[168:171], v155 offset:22848
	s_waitcnt lgkmcnt(0)
	v_mfma_f32_16x16x32_bf16 v[82:85], v[134:137], v[168:171], v[82:85]
	v_mfma_f32_16x16x32_bf16 v[86:89], v[138:141], v[168:171], v[86:89]
	v_mfma_f32_16x16x32_bf16 v[90:93], v[160:163], v[168:171], v[90:93]
	v_mfma_f32_16x16x32_bf16 v[94:97], v[164:167], v[168:171], v[94:97]
	ds_read_b64_tr_b16 v[134:135], v154 offset:9216
	ds_read_b64_tr_b16 v[136:137], v145 offset:9792
	ds_read_b64_tr_b16 v[138:139], v154 offset:9248
	ds_read_b64_tr_b16 v[140:141], v145 offset:9824
	ds_read_b64_tr_b16 v[160:161], v154 offset:9280
	ds_read_b64_tr_b16 v[162:163], v145 offset:9856
	ds_read_b64_tr_b16 v[164:165], v154 offset:9312
	ds_read_b64_tr_b16 v[166:167], v145 offset:9888
	ds_read_b128 v[168:171], v155 offset:18560
	s_waitcnt lgkmcnt(0)
	v_mfma_f32_16x16x32_bf16 v[172:175], v[160:163], v[168:171], v[110:113]
	s_nop 2
	ds_read_b128 v[110:113], v155 offset:22912
	v_mfma_f32_16x16x32_bf16 v[102:105], v[134:137], v[168:171], v[102:105]
	v_mfma_f32_16x16x32_bf16 v[106:109], v[138:141], v[168:171], v[106:109]
	v_mfma_f32_16x16x32_bf16 v[98:101], v[164:167], v[168:171], v[98:101]
	s_waitcnt lgkmcnt(0)
	v_mfma_f32_16x16x32_bf16 v[82:85], v[134:137], v[110:113], v[82:85]
	v_mfma_f32_16x16x32_bf16 v[86:89], v[138:141], v[110:113], v[86:89]
	v_mfma_f32_16x16x32_bf16 v[134:137], v[160:163], v[110:113], v[90:93]
	v_mfma_f32_16x16x32_bf16 v[138:141], v[164:167], v[110:113], v[94:97]
	s_nop 1
	ds_read_b64_tr_b16 v[90:91], v154 offset:13824
	ds_read_b64_tr_b16 v[92:93], v145 offset:14400
	ds_read_b64_tr_b16 v[160:161], v154 offset:13856
	ds_read_b64_tr_b16 v[162:163], v145 offset:14432
	ds_read_b64_tr_b16 v[164:165], v154 offset:13888
	ds_read_b64_tr_b16 v[166:167], v145 offset:14464
	ds_read_b64_tr_b16 v[168:169], v154 offset:13920
	ds_read_b64_tr_b16 v[170:171], v145 offset:14496
	ds_read_b128 v[94:97], v155 offset:18624
	s_waitcnt lgkmcnt(0)
	v_mfma_f32_16x16x32_bf16 v[110:113], v[90:93], v[94:97], v[102:105]
	v_mfma_f32_16x16x32_bf16 v[102:105], v[164:167], v[94:97], v[172:175]
	s_nop 2
	ds_read_b128 v[172:175], v155 offset:22976
	v_mfma_f32_16x16x32_bf16 v[106:109], v[160:163], v[94:97], v[106:109]
	v_mfma_f32_16x16x32_bf16 v[98:101], v[168:171], v[94:97], v[98:101]
	s_waitcnt lgkmcnt(0)
	v_mfma_f32_16x16x32_bf16 v[94:97], v[90:93], v[172:175], v[82:85]
	v_mfma_f32_16x16x32_bf16 v[90:93], v[160:163], v[172:175], v[86:89]
	v_mfma_f32_16x16x32_bf16 v[86:89], v[164:167], v[172:175], v[134:137]
	v_mfma_f32_16x16x32_bf16 v[82:85], v[168:171], v[172:175], v[138:141]
	s_nop 1
	v_mov_b64_e32 v[136:137], s[0:1]
	v_or_b32_e32 v134, s20, v116
	v_ashrrev_i32_e32 v135, 31, v134
	v_or_b32_e32 v138, s18, v116
	v_mad_u64_u32 v[136:137], s[2:3], v138, s11, v[136:137]
	v_mad_i32_i24 v137, s19, v157, v137
	v_lshl_add_u64 v[136:137], s[22:23], 1, v[136:137]
	v_lshl_add_u64 v[136:137], v[136:137], 0, v[114:115]
	v_add_co_u32_e32 v140, vcc, 0x1000, v136
	v_lshl_add_u64 v[134:135], v[134:135], 2, s[6:7]
	s_nop 0
	v_addc_co_u32_e32 v141, vcc, 0, v137, vcc
	global_load_dwordx2 v[140:141], v[140:141], off offset:3968
	v_mov_b32_e32 v139, s19
	global_load_dword v134, v[134:135], off
	s_waitcnt vmcnt(1)
	v_lshlrev_b32_e32 v123, 16, v140
	v_mul_f32_e32 v125, 0x3d372713, v123
	v_mul_f32_e32 v125, v125, v123
	v_fma_f32 v125, v125, v123, v123
	v_mul_f32_e32 v125, 0x3f4c422a, v125
	v_add_f32_e64 v127, |v125|, |v125|
	v_mul_f32_e32 v127, 0x3fb8aa3b, v127
	v_exp_f32_e32 v127, v127
	s_nop 0
	v_add_f32_e32 v127, 1.0, v127
	v_rcp_f32_e32 v127, v127
	s_nop 0
	v_fma_f32 v127, v127, -2.0, 1.0
	v_and_b32_e32 v129, 0xffff0000, v140
	v_mul_f32_e32 v131, 0x3d372713, v129
	v_mul_f32_e32 v131, v131, v129
	v_fma_f32 v131, v131, v129, v129
	v_mul_f32_e32 v131, 0x3f4c422a, v131
	v_add_f32_e64 v132, |v131|, |v131|
	v_mul_f32_e32 v132, 0x3fb8aa3b, v132
	v_exp_f32_e32 v132, v132
	s_nop 0
	v_add_f32_e32 v132, 1.0, v132
	v_rcp_f32_e32 v132, v132
	s_nop 0
	v_fma_f32 v132, v132, -2.0, 1.0
	v_lshlrev_b32_e32 v135, 16, v141
	v_mul_f32_e32 v140, 0x3d372713, v135
	v_mul_f32_e32 v140, v140, v135
	v_fma_f32 v140, v140, v135, v135
	v_mul_f32_e32 v140, 0x3f4c422a, v140
	v_add_f32_e64 v159, |v140|, |v140|
	v_mul_f32_e32 v159, 0x3fb8aa3b, v159
	v_exp_f32_e32 v159, v159
	s_nop 0
	v_add_f32_e32 v159, 1.0, v159
	v_rcp_f32_e32 v159, v159
	s_nop 0
	v_fma_f32 v159, v159, -2.0, 1.0
	v_and_b32_e32 v141, 0xffff0000, v141
	v_mul_f32_e32 v160, 0x3d372713, v141
	v_mul_f32_e32 v160, v160, v141
	v_fma_f32 v160, v160, v141, v141
	v_mul_f32_e32 v160, 0x3f4c422a, v160
	v_add_f32_e64 v161, |v160|, |v160|
	v_mul_f32_e32 v161, 0x3fb8aa3b, v161
	v_exp_f32_e32 v161, v161
	s_nop 0
	v_add_f32_e32 v161, 1.0, v161
	v_rcp_f32_e32 v161, v161
	s_nop 0
	v_fma_f32 v161, v161, -2.0, 1.0
	v_bfi_b32 v140, s30, v159, v140
	v_mul_f32_e32 v135, 0.5, v135
	v_add_f32_e32 v140, 1.0, v140
	v_mul_f32_e32 v135, v135, v140
	s_waitcnt vmcnt(0)
	v_add_f32_e32 v112, v112, v134
	v_mul_f32_e32 v140, v112, v135
	v_mul_f32_e32 v112, 0.5, v123
	v_bfi_b32 v123, s30, v127, v125
	v_add_f32_e32 v123, 1.0, v123
	v_mul_f32_e32 v112, v112, v123
	v_add_f32_e32 v110, v110, v134
	v_bfi_b32 v135, s30, v132, v131
	v_mov_b32_e32 v132, v111
	v_mul_f32_e32 v112, v110, v112
	v_mul_f32_e32 v123, 0.5, v129
	v_pk_add_f32 v[110:111], v[132:133], v[134:135]
	v_bfi_b32 v135, s30, v161, v160
	v_mul_f32_e32 v111, v123, v111
	v_mul_f32_e32 v110, v110, v111
	v_mov_b32_e32 v132, v113
	v_cvt_pk_bf16_f32 v112, v112, v110
	v_lshlrev_b64 v[110:111], 12, v[138:139]
	v_mul_f32_e32 v123, 0.5, v141
	v_pk_add_f32 v[138:139], v[132:133], v[134:135]
	v_lshl_add_u64 v[110:111], s[12:13], 0, v[110:111]
	v_mul_f32_e32 v113, v123, v139
	v_lshl_add_u64 v[110:111], s[22:23], 1, v[110:111]
	v_mul_f32_e32 v113, v138, v113
	v_lshl_add_u64 v[136:137], v[136:137], 0, s[14:15]
	v_lshl_add_u64 v[110:111], v[110:111], 0, v[114:115]
	v_cvt_pk_bf16_f32 v113, v140, v113
	global_store_dwordx2 v[110:111], v[112:113], off offset:2048
	global_load_dwordx2 v[112:113], v[136:137], off offset:32
	s_waitcnt vmcnt(0)
	v_lshlrev_b32_e32 v123, 16, v112
	v_mul_f32_e32 v125, 0x3d372713, v123
	v_mul_f32_e32 v125, v125, v123
	v_fma_f32 v125, v125, v123, v123
	v_mul_f32_e32 v125, 0x3f4c422a, v125
	v_add_f32_e64 v127, |v125|, |v125|
	v_mul_f32_e32 v127, 0x3fb8aa3b, v127
	v_exp_f32_e32 v127, v127
	s_nop 0
	v_add_f32_e32 v127, 1.0, v127
	v_rcp_f32_e32 v127, v127
	s_nop 0
	v_fma_f32 v127, v127, -2.0, 1.0
	v_and_b32_e32 v112, 0xffff0000, v112
	v_mul_f32_e32 v129, 0x3d372713, v112
	v_mul_f32_e32 v129, v129, v112
	v_fma_f32 v129, v129, v112, v112
	v_mul_f32_e32 v129, 0x3f4c422a, v129
	v_add_f32_e64 v131, |v129|, |v129|
	v_mul_f32_e32 v131, 0x3fb8aa3b, v131
	v_exp_f32_e32 v131, v131
	s_nop 0
	v_add_f32_e32 v131, 1.0, v131
	v_rcp_f32_e32 v131, v131
	s_nop 0
	v_fma_f32 v131, v131, -2.0, 1.0
	v_lshlrev_b32_e32 v132, 16, v113
	v_mul_f32_e32 v135, 0x3d372713, v132
	v_mul_f32_e32 v135, v135, v132
	v_fma_f32 v135, v135, v132, v132
	v_mul_f32_e32 v135, 0x3f4c422a, v135
	v_add_f32_e64 v138, |v135|, |v135|
	v_mul_f32_e32 v138, 0x3fb8aa3b, v138
	v_exp_f32_e32 v138, v138
	s_nop 0
	v_add_f32_e32 v138, 1.0, v138
	v_rcp_f32_e32 v138, v138
	s_nop 0
	v_fma_f32 v138, v138, -2.0, 1.0
	v_and_b32_e32 v113, 0xffff0000, v113
	v_mul_f32_e32 v139, 0x3d372713, v113
	v_mul_f32_e32 v139, v139, v113
	v_fma_f32 v139, v139, v113, v113
	v_mul_f32_e32 v139, 0x3f4c422a, v139
	v_add_f32_e64 v140, |v139|, |v139|
	v_mul_f32_e32 v140, 0x3fb8aa3b, v140
	v_exp_f32_e32 v140, v140
	s_nop 0
	v_add_f32_e32 v140, 1.0, v140
	v_rcp_f32_e32 v140, v140
	s_nop 0
	v_fma_f32 v140, v140, -2.0, 1.0
	v_bfi_b32 v135, s30, v138, v135
	v_mul_f32_e32 v132, 0.5, v132
	v_add_f32_e32 v135, 1.0, v135
	v_mul_f32_e32 v132, v132, v135
	v_add_f32_e32 v108, v108, v134
	v_mul_f32_e32 v138, v108, v132
	v_mul_f32_e32 v108, 0.5, v123
	v_bfi_b32 v123, s30, v127, v125
	v_add_f32_e32 v123, 1.0, v123
	v_mul_f32_e32 v108, v108, v123
	v_add_f32_e32 v106, v106, v134
	v_bfi_b32 v135, s30, v131, v129
	v_mov_b32_e32 v132, v107
	v_mul_f32_e32 v108, v106, v108
	v_mul_f32_e32 v112, 0.5, v112
	v_pk_add_f32 v[106:107], v[132:133], v[134:135]
	v_bfi_b32 v135, s30, v140, v139
	v_mul_f32_e32 v107, v112, v107
	v_mul_f32_e32 v106, v106, v107
	v_mov_b32_e32 v132, v109
	v_cvt_pk_bf16_f32 v106, v108, v106
	v_mul_f32_e32 v107, 0.5, v113
	v_pk_add_f32 v[108:109], v[132:133], v[134:135]
	s_nop 0
	v_mul_f32_e32 v107, v107, v109
	v_mul_f32_e32 v107, v108, v107
	v_cvt_pk_bf16_f32 v107, v138, v107
	global_store_dwordx2 v[110:111], v[106:107], off offset:2080
	global_load_dwordx2 v[106:107], v[136:137], off offset:64
	s_waitcnt vmcnt(0)
	v_lshlrev_b32_e32 v108, 16, v106
	v_mul_f32_e32 v109, 0x3d372713, v108
	v_mul_f32_e32 v109, v109, v108
	v_fma_f32 v109, v109, v108, v108
	v_mul_f32_e32 v109, 0x3f4c422a, v109
	v_add_f32_e64 v112, |v109|, |v109|
	v_mul_f32_e32 v112, 0x3fb8aa3b, v112
	v_exp_f32_e32 v112, v112
	s_nop 0
	v_add_f32_e32 v112, 1.0, v112
	v_rcp_f32_e32 v112, v112
	s_nop 0
	v_fma_f32 v112, v112, -2.0, 1.0
	v_and_b32_e32 v106, 0xffff0000, v106
	v_mul_f32_e32 v113, 0x3d372713, v106
	v_mul_f32_e32 v113, v113, v106
	v_fma_f32 v113, v113, v106, v106
	v_mul_f32_e32 v113, 0x3f4c422a, v113
	v_add_f32_e64 v123, |v113|, |v113|
	v_mul_f32_e32 v123, 0x3fb8aa3b, v123
	v_exp_f32_e32 v123, v123
	s_nop 0
	v_add_f32_e32 v123, 1.0, v123
	v_rcp_f32_e32 v123, v123
	s_nop 0
	v_fma_f32 v123, v123, -2.0, 1.0
	v_lshlrev_b32_e32 v125, 16, v107
	v_mul_f32_e32 v127, 0x3d372713, v125
	v_mul_f32_e32 v127, v127, v125
	v_fma_f32 v127, v127, v125, v125
	v_mul_f32_e32 v127, 0x3f4c422a, v127
	v_add_f32_e64 v129, |v127|, |v127|
	v_mul_f32_e32 v129, 0x3fb8aa3b, v129
	v_exp_f32_e32 v129, v129
	s_nop 0
	v_add_f32_e32 v129, 1.0, v129
	v_rcp_f32_e32 v129, v129
	s_nop 0
	v_fma_f32 v129, v129, -2.0, 1.0
	v_and_b32_e32 v107, 0xffff0000, v107
	v_mul_f32_e32 v131, 0x3d372713, v107
	v_mul_f32_e32 v131, v131, v107
	v_fma_f32 v131, v131, v107, v107
	v_mul_f32_e32 v131, 0x3f4c422a, v131
	v_add_f32_e64 v138, |v131|, |v131|
	v_mul_f32_e32 v138, 0x3fb8aa3b, v138
	v_exp_f32_e32 v138, v138
	s_nop 0
	v_add_f32_e32 v138, 1.0, v138
	v_rcp_f32_e32 v138, v138
	s_nop 0
	v_fma_f32 v138, v138, -2.0, 1.0
	v_bfi_b32 v127, s30, v129, v127
	v_mul_f32_e32 v125, 0.5, v125
	v_add_f32_e32 v127, 1.0, v127
	v_mul_f32_e32 v125, v125, v127
	v_add_f32_e32 v104, v104, v134
	v_mul_f32_e32 v125, v104, v125
	v_mul_f32_e32 v104, 0.5, v108
	v_bfi_b32 v108, s30, v112, v109
	v_add_f32_e32 v108, 1.0, v108
	v_mul_f32_e32 v104, v104, v108
	v_add_f32_e32 v102, v102, v134
	v_bfi_b32 v135, s30, v123, v113
	v_mov_b32_e32 v132, v103
	v_mul_f32_e32 v104, v102, v104
	v_mul_f32_e32 v106, 0.5, v106
	v_pk_add_f32 v[102:103], v[132:133], v[134:135]
	v_bfi_b32 v135, s30, v138, v131
	v_mul_f32_e32 v103, v106, v103
	v_mul_f32_e32 v102, v102, v103
	v_mov_b32_e32 v132, v105
	v_cvt_pk_bf16_f32 v102, v104, v102
	v_mul_f32_e32 v103, 0.5, v107
	v_pk_add_f32 v[104:105], v[132:133], v[134:135]
	s_nop 0
	v_mul_f32_e32 v103, v103, v105
	v_mul_f32_e32 v103, v104, v103
	v_cvt_pk_bf16_f32 v103, v125, v103
	global_store_dwordx2 v[110:111], v[102:103], off offset:2112
	global_load_dwordx2 v[102:103], v[136:137], off offset:96
	s_waitcnt vmcnt(0)
	v_lshlrev_b32_e32 v104, 16, v102
	v_mul_f32_e32 v105, 0x3d372713, v104
	v_mul_f32_e32 v105, v105, v104
	v_fma_f32 v105, v105, v104, v104
	v_mul_f32_e32 v105, 0x3f4c422a, v105
	v_add_f32_e64 v106, |v105|, |v105|
	v_mul_f32_e32 v106, 0x3fb8aa3b, v106
	v_exp_f32_e32 v106, v106
	s_nop 0
	v_add_f32_e32 v106, 1.0, v106
	v_rcp_f32_e32 v106, v106
	s_nop 0
	v_fma_f32 v106, v106, -2.0, 1.0
	v_and_b32_e32 v102, 0xffff0000, v102
	v_mul_f32_e32 v107, 0x3d372713, v102
	v_mul_f32_e32 v107, v107, v102
	v_fma_f32 v107, v107, v102, v102
	v_mul_f32_e32 v107, 0x3f4c422a, v107
	v_add_f32_e64 v108, |v107|, |v107|
	v_mul_f32_e32 v108, 0x3fb8aa3b, v108
	v_exp_f32_e32 v108, v108
	s_nop 0
	v_add_f32_e32 v108, 1.0, v108
	v_rcp_f32_e32 v108, v108
	s_nop 0
	v_fma_f32 v108, v108, -2.0, 1.0
	v_lshlrev_b32_e32 v109, 16, v103
	v_mul_f32_e32 v112, 0x3d372713, v109
	v_mul_f32_e32 v112, v112, v109
	v_fma_f32 v112, v112, v109, v109
	v_mul_f32_e32 v112, 0x3f4c422a, v112
	v_add_f32_e64 v113, |v112|, |v112|
	v_mul_f32_e32 v113, 0x3fb8aa3b, v113
	v_exp_f32_e32 v113, v113
	s_nop 0
	v_add_f32_e32 v113, 1.0, v113
	v_rcp_f32_e32 v113, v113
	s_nop 0
	v_fma_f32 v113, v113, -2.0, 1.0
	v_and_b32_e32 v103, 0xffff0000, v103
	v_mul_f32_e32 v123, 0x3d372713, v103
	v_mul_f32_e32 v123, v123, v103
	v_fma_f32 v123, v123, v103, v103
	v_mul_f32_e32 v123, 0x3f4c422a, v123
	v_add_f32_e64 v125, |v123|, |v123|
	v_mul_f32_e32 v125, 0x3fb8aa3b, v125
	v_exp_f32_e32 v125, v125
	s_nop 0
	v_add_f32_e32 v125, 1.0, v125
	v_rcp_f32_e32 v125, v125
	s_nop 0
	v_fma_f32 v125, v125, -2.0, 1.0
	v_bfi_b32 v112, s30, v113, v112
	v_mul_f32_e32 v109, 0.5, v109
	v_add_f32_e32 v112, 1.0, v112
	v_mul_f32_e32 v109, v109, v112
	v_add_f32_e32 v100, v100, v134
	v_mul_f32_e32 v109, v100, v109
	v_mul_f32_e32 v100, 0.5, v104
	v_bfi_b32 v104, s30, v106, v105
	v_add_f32_e32 v104, 1.0, v104
	v_mul_f32_e32 v100, v100, v104
	v_add_f32_e32 v98, v98, v134
	v_bfi_b32 v135, s30, v108, v107
	v_mov_b32_e32 v132, v99
	v_mul_f32_e32 v100, v98, v100
	v_mul_f32_e32 v102, 0.5, v102
	v_pk_add_f32 v[98:99], v[132:133], v[134:135]
	v_bfi_b32 v135, s30, v125, v123
	v_mul_f32_e32 v99, v102, v99
	v_mul_f32_e32 v98, v98, v99
	v_mov_b32_e32 v132, v101
	v_cvt_pk_bf16_f32 v98, v100, v98
	v_mul_f32_e32 v99, 0.5, v103
	v_pk_add_f32 v[100:101], v[132:133], v[134:135]
	v_or_b32_e32 v102, s18, v118
	v_mul_f32_e32 v99, v99, v101
	v_mul_f32_e32 v99, v100, v99
	v_mov_b64_e32 v[100:101], s[0:1]
	v_mad_u64_u32 v[100:101], s[2:3], v102, s11, v[100:101]
	v_mad_i32_i24 v101, s19, v157, v101
	v_lshl_add_u64 v[100:101], s[22:23], 1, v[100:101]
	v_lshl_add_u64 v[100:101], v[100:101], 0, v[114:115]
	v_add_co_u32_e32 v104, vcc, 0x1000, v100
	v_cvt_pk_bf16_f32 v99, v109, v99
	s_nop 0
	v_addc_co_u32_e32 v105, vcc, 0, v101, vcc
	global_load_dwordx2 v[104:105], v[104:105], off offset:3968
	s_ashr_i32 s21, s20, 31
	global_store_dwordx2 v[110:111], v[98:99], off offset:2144
	v_lshl_add_u64 v[98:99], s[20:21], 0, v[116:117]
	v_lshl_add_u64 v[98:99], v[98:99], 2, s[6:7]
	global_load_dword v98, v[98:99], off offset:64
	v_mov_b32_e32 v103, s19
	s_waitcnt vmcnt(2)
	v_lshlrev_b32_e32 v99, 16, v104
	v_mul_f32_e32 v106, 0x3d372713, v99
	v_mul_f32_e32 v106, v106, v99
	v_fma_f32 v106, v106, v99, v99
	v_mul_f32_e32 v106, 0x3f4c422a, v106
	v_add_f32_e64 v107, |v106|, |v106|
	v_mul_f32_e32 v107, 0x3fb8aa3b, v107
	v_exp_f32_e32 v107, v107
	s_nop 0
	v_add_f32_e32 v107, 1.0, v107
	v_rcp_f32_e32 v107, v107
	s_nop 0
	v_fma_f32 v107, v107, -2.0, 1.0
	v_and_b32_e32 v104, 0xffff0000, v104
	v_mul_f32_e32 v108, 0x3d372713, v104
	v_mul_f32_e32 v108, v108, v104
	v_fma_f32 v108, v108, v104, v104
	v_mul_f32_e32 v108, 0x3f4c422a, v108
	v_add_f32_e64 v109, |v108|, |v108|
	v_mul_f32_e32 v109, 0x3fb8aa3b, v109
	v_exp_f32_e32 v109, v109
	s_nop 0
	v_add_f32_e32 v109, 1.0, v109
	v_rcp_f32_e32 v109, v109
	s_nop 0
	v_fma_f32 v109, v109, -2.0, 1.0
	v_lshlrev_b32_e32 v110, 16, v105
	v_mul_f32_e32 v111, 0x3d372713, v110
	v_mul_f32_e32 v111, v111, v110
	v_fma_f32 v111, v111, v110, v110
	v_mul_f32_e32 v111, 0x3f4c422a, v111
	v_add_f32_e64 v112, |v111|, |v111|
	v_mul_f32_e32 v112, 0x3fb8aa3b, v112
	v_exp_f32_e32 v112, v112
	s_nop 0
	v_add_f32_e32 v112, 1.0, v112
	v_rcp_f32_e32 v112, v112
	s_nop 0
	v_fma_f32 v112, v112, -2.0, 1.0
	v_and_b32_e32 v105, 0xffff0000, v105
	v_mul_f32_e32 v113, 0x3d372713, v105
	v_mul_f32_e32 v113, v113, v105
	v_fma_f32 v113, v113, v105, v105
	v_mul_f32_e32 v113, 0x3f4c422a, v113
	v_add_f32_e64 v123, |v113|, |v113|
	v_mul_f32_e32 v123, 0x3fb8aa3b, v123
	v_exp_f32_e32 v123, v123
	s_nop 0
	v_add_f32_e32 v123, 1.0, v123
	v_rcp_f32_e32 v123, v123
	s_nop 0
	v_fma_f32 v123, v123, -2.0, 1.0
	v_bfi_b32 v111, s30, v112, v111
	v_mul_f32_e32 v110, 0.5, v110
	v_add_f32_e32 v111, 1.0, v111
	v_mul_f32_e32 v110, v110, v111
	s_waitcnt vmcnt(0)
	v_add_f32_e32 v96, v96, v98
	v_mul_f32_e32 v110, v96, v110
	v_mul_f32_e32 v96, 0.5, v99
	v_bfi_b32 v99, s30, v107, v106
	v_add_f32_e32 v99, 1.0, v99
	v_mul_f32_e32 v96, v96, v99
	v_add_f32_e32 v94, v94, v98
	v_bfi_b32 v99, s30, v109, v108
	v_mov_b32_e32 v132, v95
	v_mul_f32_e32 v96, v94, v96
	v_mul_f32_e32 v104, 0.5, v104
	v_pk_add_f32 v[94:95], v[132:133], v[98:99]
	v_bfi_b32 v99, s30, v123, v113
	v_mul_f32_e32 v95, v104, v95
	v_mul_f32_e32 v94, v94, v95
	v_mov_b32_e32 v132, v97
	v_cvt_pk_bf16_f32 v96, v96, v94
	v_lshlrev_b64 v[94:95], 12, v[102:103]
	v_mul_f32_e32 v104, 0.5, v105
	v_pk_add_f32 v[102:103], v[132:133], v[98:99]
	v_lshl_add_u64 v[94:95], s[12:13], 0, v[94:95]
	v_mul_f32_e32 v97, v104, v103
	v_lshl_add_u64 v[94:95], s[22:23], 1, v[94:95]
	v_mul_f32_e32 v97, v102, v97
	v_lshl_add_u64 v[100:101], v[100:101], 0, s[14:15]
	v_lshl_add_u64 v[94:95], v[94:95], 0, v[114:115]
	v_cvt_pk_bf16_f32 v97, v110, v97
	global_store_dwordx2 v[94:95], v[96:97], off offset:2048
	global_load_dwordx2 v[96:97], v[100:101], off offset:32
	s_waitcnt vmcnt(0)
	v_lshlrev_b32_e32 v99, 16, v96
	v_mul_f32_e32 v102, 0x3d372713, v99
	v_mul_f32_e32 v102, v102, v99
	v_fma_f32 v102, v102, v99, v99
	v_mul_f32_e32 v102, 0x3f4c422a, v102
	v_add_f32_e64 v103, |v102|, |v102|
	v_mul_f32_e32 v103, 0x3fb8aa3b, v103
	v_exp_f32_e32 v103, v103
	s_nop 0
	v_add_f32_e32 v103, 1.0, v103
	v_rcp_f32_e32 v103, v103
	s_nop 0
	v_fma_f32 v103, v103, -2.0, 1.0
	v_and_b32_e32 v96, 0xffff0000, v96
	v_mul_f32_e32 v104, 0x3d372713, v96
	v_mul_f32_e32 v104, v104, v96
	v_fma_f32 v104, v104, v96, v96
	v_mul_f32_e32 v104, 0x3f4c422a, v104
	v_add_f32_e64 v105, |v104|, |v104|
	v_mul_f32_e32 v105, 0x3fb8aa3b, v105
	v_exp_f32_e32 v105, v105
	s_nop 0
	v_add_f32_e32 v105, 1.0, v105
	v_rcp_f32_e32 v105, v105
	s_nop 0
	v_fma_f32 v105, v105, -2.0, 1.0
	v_lshlrev_b32_e32 v106, 16, v97
	v_mul_f32_e32 v107, 0x3d372713, v106
	v_mul_f32_e32 v107, v107, v106
	v_fma_f32 v107, v107, v106, v106
	v_mul_f32_e32 v107, 0x3f4c422a, v107
	v_add_f32_e64 v108, |v107|, |v107|
	v_mul_f32_e32 v108, 0x3fb8aa3b, v108
	v_exp_f32_e32 v108, v108
	s_nop 0
	v_add_f32_e32 v108, 1.0, v108
	v_rcp_f32_e32 v108, v108
	s_nop 0
	v_fma_f32 v108, v108, -2.0, 1.0
	v_and_b32_e32 v97, 0xffff0000, v97
	v_mul_f32_e32 v109, 0x3d372713, v97
	v_mul_f32_e32 v109, v109, v97
	v_fma_f32 v109, v109, v97, v97
	v_mul_f32_e32 v109, 0x3f4c422a, v109
	v_add_f32_e64 v110, |v109|, |v109|
	v_mul_f32_e32 v110, 0x3fb8aa3b, v110
	v_exp_f32_e32 v110, v110
	s_nop 0
	v_add_f32_e32 v110, 1.0, v110
	v_rcp_f32_e32 v110, v110
	s_nop 0
	v_fma_f32 v110, v110, -2.0, 1.0
	v_bfi_b32 v107, s30, v108, v107
	v_mul_f32_e32 v106, 0.5, v106
	v_add_f32_e32 v107, 1.0, v107
	v_mul_f32_e32 v106, v106, v107
	v_add_f32_e32 v92, v92, v98
	v_mul_f32_e32 v106, v92, v106
	v_mul_f32_e32 v92, 0.5, v99
	v_bfi_b32 v99, s30, v103, v102
	v_add_f32_e32 v99, 1.0, v99
	v_mul_f32_e32 v92, v92, v99
	v_add_f32_e32 v90, v90, v98
	v_bfi_b32 v99, s30, v105, v104
	v_mov_b32_e32 v132, v91
	v_mul_f32_e32 v92, v90, v92
	v_mul_f32_e32 v96, 0.5, v96
	v_pk_add_f32 v[90:91], v[132:133], v[98:99]
	v_bfi_b32 v99, s30, v110, v109
	v_mul_f32_e32 v91, v96, v91
	v_mul_f32_e32 v90, v90, v91
	v_mov_b32_e32 v132, v93
	v_cvt_pk_bf16_f32 v90, v92, v90
	v_mul_f32_e32 v91, 0.5, v97
	v_pk_add_f32 v[92:93], v[132:133], v[98:99]
	s_nop 0
	v_mul_f32_e32 v91, v91, v93
	v_mul_f32_e32 v91, v92, v91
	v_cvt_pk_bf16_f32 v91, v106, v91
	global_store_dwordx2 v[94:95], v[90:91], off offset:2080
	global_load_dwordx2 v[90:91], v[100:101], off offset:64
	s_waitcnt vmcnt(0)
	v_lshlrev_b32_e32 v92, 16, v90
	v_mul_f32_e32 v93, 0x3d372713, v92
	v_mul_f32_e32 v93, v93, v92
	v_fma_f32 v93, v93, v92, v92
	v_mul_f32_e32 v93, 0x3f4c422a, v93
	v_add_f32_e64 v96, |v93|, |v93|
	v_mul_f32_e32 v96, 0x3fb8aa3b, v96
	v_exp_f32_e32 v96, v96
	s_nop 0
	v_add_f32_e32 v96, 1.0, v96
	v_rcp_f32_e32 v96, v96
	s_nop 0
	v_fma_f32 v96, v96, -2.0, 1.0
	v_and_b32_e32 v90, 0xffff0000, v90
	v_mul_f32_e32 v97, 0x3d372713, v90
	v_mul_f32_e32 v97, v97, v90
	v_fma_f32 v97, v97, v90, v90
	v_mul_f32_e32 v97, 0x3f4c422a, v97
	v_add_f32_e64 v99, |v97|, |v97|
	v_mul_f32_e32 v99, 0x3fb8aa3b, v99
	v_exp_f32_e32 v99, v99
	s_nop 0
	v_add_f32_e32 v99, 1.0, v99
	v_rcp_f32_e32 v99, v99
	s_nop 0
	v_fma_f32 v99, v99, -2.0, 1.0
	v_lshlrev_b32_e32 v102, 16, v91
	v_mul_f32_e32 v103, 0x3d372713, v102
	v_mul_f32_e32 v103, v103, v102
	v_fma_f32 v103, v103, v102, v102
	v_mul_f32_e32 v103, 0x3f4c422a, v103
	v_add_f32_e64 v104, |v103|, |v103|
	v_mul_f32_e32 v104, 0x3fb8aa3b, v104
	v_exp_f32_e32 v104, v104
	s_nop 0
	v_add_f32_e32 v104, 1.0, v104
	v_rcp_f32_e32 v104, v104
	s_nop 0
	v_fma_f32 v104, v104, -2.0, 1.0
	v_and_b32_e32 v91, 0xffff0000, v91
	v_mul_f32_e32 v105, 0x3d372713, v91
	v_mul_f32_e32 v105, v105, v91
	v_fma_f32 v105, v105, v91, v91
	v_mul_f32_e32 v105, 0x3f4c422a, v105
	v_add_f32_e64 v106, |v105|, |v105|
	v_mul_f32_e32 v106, 0x3fb8aa3b, v106
	v_exp_f32_e32 v106, v106
	s_nop 0
	v_add_f32_e32 v106, 1.0, v106
	v_rcp_f32_e32 v106, v106
	s_nop 0
	v_fma_f32 v106, v106, -2.0, 1.0
	v_bfi_b32 v103, s30, v104, v103
	v_mul_f32_e32 v102, 0.5, v102
	v_add_f32_e32 v103, 1.0, v103
	v_mul_f32_e32 v102, v102, v103
	v_add_f32_e32 v88, v88, v98
	v_mul_f32_e32 v102, v88, v102
	v_mul_f32_e32 v88, 0.5, v92
	v_bfi_b32 v92, s30, v96, v93
	v_add_f32_e32 v92, 1.0, v92
	v_mul_f32_e32 v88, v88, v92
	v_add_f32_e32 v86, v86, v98
	v_bfi_b32 v99, s30, v99, v97
	v_mov_b32_e32 v132, v87
	v_mul_f32_e32 v88, v86, v88
	v_mul_f32_e32 v90, 0.5, v90
	v_pk_add_f32 v[86:87], v[132:133], v[98:99]
	v_bfi_b32 v99, s30, v106, v105
	v_mul_f32_e32 v87, v90, v87
	v_mul_f32_e32 v86, v86, v87
	v_mov_b32_e32 v132, v89
	v_cvt_pk_bf16_f32 v86, v88, v86
	v_mul_f32_e32 v87, 0.5, v91
	v_pk_add_f32 v[88:89], v[132:133], v[98:99]
	s_nop 0
	v_mul_f32_e32 v87, v87, v89
	v_mul_f32_e32 v87, v88, v87
	v_cvt_pk_bf16_f32 v87, v102, v87
	global_store_dwordx2 v[94:95], v[86:87], off offset:2112
	global_load_dwordx2 v[86:87], v[100:101], off offset:96
	s_waitcnt vmcnt(0)
	v_lshlrev_b32_e32 v88, 16, v86
	v_mul_f32_e32 v89, 0x3d372713, v88
	v_mul_f32_e32 v89, v89, v88
	v_fma_f32 v89, v89, v88, v88
	v_mul_f32_e32 v89, 0x3f4c422a, v89
	v_add_f32_e64 v90, |v89|, |v89|
	v_mul_f32_e32 v90, 0x3fb8aa3b, v90
	v_exp_f32_e32 v90, v90
	s_nop 0
	v_add_f32_e32 v90, 1.0, v90
	v_rcp_f32_e32 v90, v90
	s_nop 0
	v_fma_f32 v90, v90, -2.0, 1.0
	v_and_b32_e32 v86, 0xffff0000, v86
	v_mul_f32_e32 v91, 0x3d372713, v86
	v_mul_f32_e32 v91, v91, v86
	v_fma_f32 v91, v91, v86, v86
	v_mul_f32_e32 v91, 0x3f4c422a, v91
	v_add_f32_e64 v92, |v91|, |v91|
	v_mul_f32_e32 v92, 0x3fb8aa3b, v92
	v_exp_f32_e32 v92, v92
	s_nop 0
	v_add_f32_e32 v92, 1.0, v92
	v_rcp_f32_e32 v92, v92
	s_nop 0
	v_fma_f32 v92, v92, -2.0, 1.0
	v_lshlrev_b32_e32 v93, 16, v87
	v_mul_f32_e32 v96, 0x3d372713, v93
	v_mul_f32_e32 v96, v96, v93
	v_fma_f32 v96, v96, v93, v93
	v_mul_f32_e32 v96, 0x3f4c422a, v96
	v_add_f32_e64 v97, |v96|, |v96|
	v_mul_f32_e32 v97, 0x3fb8aa3b, v97
	v_exp_f32_e32 v97, v97
	s_nop 0
	v_add_f32_e32 v97, 1.0, v97
	v_rcp_f32_e32 v97, v97
	s_nop 0
	v_fma_f32 v97, v97, -2.0, 1.0
	v_and_b32_e32 v87, 0xffff0000, v87
	v_mul_f32_e32 v99, 0x3d372713, v87
	v_mul_f32_e32 v99, v99, v87
	v_fma_f32 v99, v99, v87, v87
	v_mul_f32_e32 v100, 0x3f4c422a, v99
	v_cmp_nlt_f32_e64 s[2:3], |v100|, s26
	s_and_saveexec_b64 s[18:19], s[2:3]
	s_xor_b64 s[18:19], exec, s[18:19]
	s_cbranch_execz .LBB0_3450
	v_add_f32_e64 v99, |v100|, |v100|
	v_mul_f32_e32 v101, 0x3fb8aa3b, v99
	v_rndne_f32_e32 v102, v101
	v_sub_f32_e32 v103, v101, v102
	v_fma_f32 v101, v99, s27, -v101
	v_fmac_f32_e32 v101, 0x32a5705f, v99
	v_add_f32_e32 v101, v103, v101
	v_cvt_i32_f32_e32 v102, v102
	v_exp_f32_e32 v101, v101
	v_cmp_ngt_f32_e32 vcc, s28, v99
	v_ldexp_f32 v101, v101, v102
	s_nop 0
	v_cndmask_b32_e32 v101, 0, v101, vcc
	v_cmp_nlt_f32_e32 vcc, s29, v99
	s_nop 1
	v_cndmask_b32_e32 v99, v158, v101, vcc
	v_add_f32_e32 v99, 1.0, v99
	v_rcp_f32_e32 v99, v99
	s_nop 0
	v_fma_f32 v101, v99, -2.0, 1.0
